# diff-attn row-sum adds moved into K-fragment LDS wait windows; GEMM K-loops: 3 of 6 stage DMAs issued inside MFMA block (vmcnt 8->5); nt loads in mla_fin
# speedup vs baseline: 1.0059x; 1.0059x over previous
; #define PG8_STAGE(bufoff, gbase, voff) do { _Pragma("unroll") for (int _i = 0; _i < 2; ++_i) \
;         __builtin_amdgcn_global_load_lds((const unsigned*)((const char*)(gbase) + (voff)[_i]), (PG8_LAS unsigned*)(lds + (bufoff) + ldsw + _i * 8192), 16, 0, 0); } while (0)
; #define PG8_WAIT_V(n) asm volatile("s_waitcnt vmcnt(" #n ")" ::: "memory")
; #define PG8_BAR __builtin_amdgcn_s_barrier()
; template <class Epi, class Sched, bool ALIGN_EPI = false, bool SP2 = false, bool GATHER = false>
; __device__ __forceinline__ void gemm_phase(PG8_LAS unsigned char* lds, const Gemm g, const Sched& S, const Epi& E, int tid_in, const int* rowsrc = nullptr, PG8_LAS int* idx_lds = nullptr) {
;     ...
;         for (int t = 0; t < nt; t += 2) {
;             const bool last = (t == nt - 2);
;             if constexpr (GATHER) {
; #pragma unroll
;                 for (int h_ = 0; h_ < 2; ++h_) { gS[h_][0] = last ? gN[h_][0] : gA[h_][0]; gS[h_][1] = last ? gN[h_][1] : gA[h_][1]; } }
;             const char* a1 = cA + (size_t)(t + 1) * kstep;
;             const char* a2 = last ? nA : cA + (size_t)(t + 2) * kstep; const char* b2 = last ? nB : cB + (size_t)(t + 2) * kstep;
;             const char* a3 = a2 + kstep; const char* b3 = b2 + kstep;
;             if (last && has_next) S.a_ready(nxt);
;             if constexpr (SP2) {
;             PG8_LDB(B0, 0, 0); PG8_LDB(B1, 0, 1); PG8_SCHED; PG8_LDA(At, 0, 0); PG8_STAGE(PG8_SA(1, 1), a1 + hstepA, PG8_OA(1));
;             PG8_WAIT_V(8); PG8_WAIT_L(0); PG8_BAR; PG8_MMA(0, 0, At, B0); PG8_MMA(0, 1, At, B1); PG8_BAR; PG8_SCHED;
;             PG8_LDA(At, 0, 1); PG8_STAGE(PG8_SB(0, 0), b2, voffB); PG8_STAGE(PG8_SB(0, 1), b2 + hstep, voffB); PG8_STAGE(PG8_SA(0, 0), a2, PG8_OS(0));
;             PG8_WAIT_V(8); PG8_WAIT_L(0); PG8_BAR; PG8_MMA(1, 0, At, B0); PG8_MMA(1, 1, At, B1); PG8_BAR; PG8_SCHED;
;             PG8_LDB(B0, 1, 0); PG8_LDB(B1, 1, 1); PG8_SCHED; PG8_LDA(At, 1, 0); PG8_STAGE(PG8_SA(0, 1), a2 + hstepA, PG8_OS(1));
;             PG8_WAIT_V(8); PG8_WAIT_L(0); PG8_BAR; PG8_MMA(0, 0, At, B0); PG8_MMA(0, 1, At, B1); PG8_BAR; PG8_SCHED;
;             PG8_LDA(At, 1, 1); PG8_STAGE(PG8_SB(1, 0), b3, voffB); PG8_STAGE(PG8_SB(1, 1), b3 + hstep, voffB); PG8_STAGE(PG8_SA(1, 0), a3, PG8_OS(0));
;             PG8_WAIT_V(8); PG8_WAIT_L(0); PG8_BAR; PG8_MMA(1, 0, At, B0); PG8_MMA(1, 1, At, B1); PG8_BAR; PG8_SCHED;
.LBB0_390:
	s_add_u32 s20, s18, 0xfffc0080
	s_addc_u32 s21, s19, -1
	s_add_i32 s52, 0, 0x10000
	s_cmp_eq_u32 s51, 12
	s_cselect_b32 s23, s13, s21
	s_cselect_b32 s22, s47, s20
	v_add_u32_e32 v144, s52, v149
	s_cselect_b32 s21, s9, s50
	s_cselect_b32 s20, s48, s49
	s_add_i32 s54, 0, 0x14000
	ds_read_b128 v[140:143], v144
	ds_read_b128 v[152:155], v144 offset:1024
	ds_read_b128 v[156:159], v144 offset:2048
	ds_read_b128 v[160:163], v144 offset:3072
	v_add_u32_e32 v144, s54, v149
	ds_read_b128 v[164:167], v144
	ds_read_b128 v[168:171], v144 offset:1024
	ds_read_b128 v[172:175], v144 offset:2048
	ds_read_b128 v[176:179], v144 offset:3072
	v_lshl_add_u64 v[144:145], s[18:19], 0, v[136:137]
	s_add_i32 m0, s29, 0xc000
	ds_read_b128 v[180:183], v151
	ds_read_b128 v[184:187], v151 offset:1024
	ds_read_b128 v[188:191], v151 offset:2048
	ds_read_b128 v[192:195], v151 offset:3072
	ds_read_b128 v[196:199], v151 offset:4096
	ds_read_b128 v[200:203], v151 offset:5120
	ds_read_b128 v[204:207], v151 offset:6144
	ds_read_b128 v[208:211], v151 offset:7168
	global_load_lds_dwordx4 v[144:145], off
	v_lshl_add_u64 v[144:145], s[18:19], 0, v[138:139]
	s_add_i32 m0, s29, 0xe000
	s_nop 0
	global_load_lds_dwordx4 v[144:145], off
	s_waitcnt vmcnt(8)
	s_waitcnt lgkmcnt(0)
	s_barrier
	s_setprio 1
	s_waitcnt lgkmcnt(0)
	v_mfma_f32_16x16x32_bf16 v[126:129], v[140:143], v[180:183], v[126:129]
	v_mfma_f32_16x16x32_bf16 v[122:125], v[156:159], v[180:183], v[122:125]
	v_mfma_f32_16x16x32_bf16 v[110:113], v[140:143], v[188:191], v[110:113]
	v_mfma_f32_16x16x32_bf16 v[106:109], v[156:159], v[188:191], v[106:109]
	v_mfma_f32_16x16x32_bf16 v[94:97], v[140:143], v[196:199], v[94:97]
	v_mfma_f32_16x16x32_bf16 v[90:93], v[156:159], v[196:199], v[90:93]
	v_mfma_f32_16x16x32_bf16 v[78:81], v[140:143], v[204:207], v[78:81]
	v_mfma_f32_16x16x32_bf16 v[74:77], v[156:159], v[204:207], v[74:77]
	v_mfma_f32_16x16x32_bf16 v[126:129], v[152:155], v[184:187], v[126:129]
	v_mfma_f32_16x16x32_bf16 v[122:125], v[160:163], v[184:187], v[122:125]
	v_mfma_f32_16x16x32_bf16 v[110:113], v[152:155], v[192:195], v[110:113]
	v_mfma_f32_16x16x32_bf16 v[106:109], v[160:163], v[192:195], v[106:109]
	v_mfma_f32_16x16x32_bf16 v[94:97], v[152:155], v[200:203], v[94:97]
	v_mfma_f32_16x16x32_bf16 v[90:93], v[160:163], v[200:203], v[90:93]
	v_mfma_f32_16x16x32_bf16 v[78:81], v[152:155], v[208:211], v[78:81]
	v_mfma_f32_16x16x32_bf16 v[74:77], v[160:163], v[208:211], v[74:77]
	s_setprio 0
	s_setprio 1
	v_mfma_f32_16x16x32_bf16 v[118:121], v[164:167], v[180:183], v[118:121]
	v_mfma_f32_16x16x32_bf16 v[114:117], v[172:175], v[180:183], v[114:117]
	v_mfma_f32_16x16x32_bf16 v[102:105], v[164:167], v[188:191], v[102:105]
	v_mfma_f32_16x16x32_bf16 v[98:101], v[172:175], v[188:191], v[98:101]
	v_mfma_f32_16x16x32_bf16 v[86:89], v[164:167], v[196:199], v[86:89]
	v_mfma_f32_16x16x32_bf16 v[82:85], v[172:175], v[196:199], v[82:85]
	v_mfma_f32_16x16x32_bf16 v[70:73], v[164:167], v[204:207], v[70:73]
	v_mfma_f32_16x16x32_bf16 v[66:69], v[172:175], v[204:207], v[66:69]
	v_mfma_f32_16x16x32_bf16 v[118:121], v[168:171], v[184:187], v[118:121]
	v_mfma_f32_16x16x32_bf16 v[114:117], v[176:179], v[184:187], v[114:117]
	v_mfma_f32_16x16x32_bf16 v[102:105], v[168:171], v[192:195], v[102:105]
	v_mfma_f32_16x16x32_bf16 v[98:101], v[176:179], v[192:195], v[98:101]
	v_mfma_f32_16x16x32_bf16 v[86:89], v[168:171], v[200:203], v[86:89]
	v_mfma_f32_16x16x32_bf16 v[82:85], v[176:179], v[200:203], v[82:85]
	v_mfma_f32_16x16x32_bf16 v[70:73], v[168:171], v[208:211], v[70:73]
	v_mfma_f32_16x16x32_bf16 v[66:69], v[176:179], v[208:211], v[66:69]
	s_setprio 0
	s_barrier
	s_add_i32 s52, s52, s28
	v_lshl_add_u64 v[144:145], s[20:21], 0, v[0:1]
	s_mov_b32 m0, s52
	ds_read_b128 v[180:183], v151 offset:16384
	ds_read_b128 v[184:187], v151 offset:17408
	ds_read_b128 v[188:191], v151 offset:18432
	ds_read_b128 v[192:195], v151 offset:19456
	ds_read_b128 v[196:199], v151 offset:20480
	ds_read_b128 v[200:203], v151 offset:21504
	ds_read_b128 v[204:207], v151 offset:22528
	ds_read_b128 v[208:211], v151 offset:23552
	global_load_lds_dwordx4 v[144:145], off
	s_add_i32 m0, s52, 0x2000
	s_add_u32 s52, s20, 0x40000
	v_lshl_add_u64 v[212:213], s[20:21], 0, v[130:131]
	s_addc_u32 s53, s21, 0
	s_add_i32 s54, s54, s28
	global_load_lds_dwordx4 v[212:213], off
	v_lshl_add_u64 v[214:215], s[52:53], 0, v[0:1]
	s_mov_b32 m0, s54
	v_lshl_add_u64 v[216:217], s[22:23], 0, v[132:133]
	global_load_lds_dwordx4 v[214:215], off
	s_waitcnt vmcnt(5)
	s_waitcnt lgkmcnt(0)
	s_barrier
; #define PG8_STAGE(bufoff, gbase, voff) do { _Pragma("unroll") for (int _i = 0; _i < 2; ++_i) \
;         __builtin_amdgcn_global_load_lds((const unsigned*)((const char*)(gbase) + (voff)[_i]), (PG8_LAS unsigned*)(lds + (bufoff) + ldsw + _i * 8192), 16, 0, 0); } while (0)
; #define PG8_WAIT_V(n) asm volatile("s_waitcnt vmcnt(" #n ")" ::: "memory")
; #define PG8_BAR __builtin_amdgcn_s_barrier()
; template <class Epi, class Sched, bool ALIGN_EPI = false, bool SP2 = false, bool GATHER = false>
; __device__ __forceinline__ void gemm_phase(PG8_LAS unsigned char* lds, const Gemm g, const Sched& S, const Epi& E, int tid_in, const int* rowsrc = nullptr, PG8_LAS int* idx_lds = nullptr) {
;     ...
;         for (int t = 0; t < nt; t += 2) {
;             const bool last = (t == nt - 2);
;             if constexpr (GATHER) {
; #pragma unroll
;                 for (int h_ = 0; h_ < 2; ++h_) { gS[h_][0] = last ? gN[h_][0] : gA[h_][0]; gS[h_][1] = last ? gN[h_][1] : gA[h_][1]; } }
;             const char* a1 = cA + (size_t)(t + 1) * kstep;
;             const char* a2 = last ? nA : cA + (size_t)(t + 2) * kstep; const char* b2 = last ? nB : cB + (size_t)(t + 2) * kstep;
;             const char* a3 = a2 + kstep; const char* b3 = b2 + kstep;
;             if (last && has_next) S.a_ready(nxt);
;             if constexpr (SP2) {
;             PG8_LDB(B0, 0, 0); PG8_LDB(B1, 0, 1); PG8_SCHED; PG8_LDA(At, 0, 0); PG8_STAGE(PG8_SA(1, 1), a1 + hstepA, PG8_OA(1));
;             PG8_WAIT_V(8); PG8_WAIT_L(0); PG8_BAR; PG8_MMA(0, 0, At, B0); PG8_MMA(0, 1, At, B1); PG8_BAR; PG8_SCHED;
;             PG8_LDA(At, 0, 1); PG8_STAGE(PG8_SB(0, 0), b2, voffB); PG8_STAGE(PG8_SB(0, 1), b2 + hstep, voffB); PG8_STAGE(PG8_SA(0, 0), a2, PG8_OS(0));
;             PG8_WAIT_V(8); PG8_WAIT_L(0); PG8_BAR; PG8_MMA(1, 0, At, B0); PG8_MMA(1, 1, At, B1); PG8_BAR; PG8_SCHED;
;             PG8_LDB(B0, 1, 0); PG8_LDB(B1, 1, 1); PG8_SCHED; PG8_LDA(At, 1, 0); PG8_STAGE(PG8_SA(0, 1), a2 + hstepA, PG8_OS(1));
;             PG8_WAIT_V(8); PG8_WAIT_L(0); PG8_BAR; PG8_MMA(0, 0, At, B0); PG8_MMA(0, 1, At, B1); PG8_BAR; PG8_SCHED;
;             PG8_LDA(At, 1, 1); PG8_STAGE(PG8_SB(1, 0), b3, voffB); PG8_STAGE(PG8_SB(1, 1), b3 + hstep, voffB); PG8_STAGE(PG8_SA(1, 0), a3, PG8_OS(0));
;             PG8_WAIT_V(8); PG8_WAIT_L(0); PG8_BAR; PG8_MMA(1, 0, At, B0); PG8_MMA(1, 1, At, B1); PG8_BAR; PG8_SCHED;
	s_setprio 1
	s_waitcnt lgkmcnt(0)
	v_mfma_f32_16x16x32_bf16 v[62:65], v[140:143], v[180:183], v[62:65]
	v_mfma_f32_16x16x32_bf16 v[58:61], v[156:159], v[180:183], v[58:61]
	v_mfma_f32_16x16x32_bf16 v[46:49], v[140:143], v[188:191], v[46:49]
	v_mfma_f32_16x16x32_bf16 v[42:45], v[156:159], v[188:191], v[42:45]
	v_mfma_f32_16x16x32_bf16 v[30:33], v[140:143], v[196:199], v[30:33]
	v_mfma_f32_16x16x32_bf16 v[26:29], v[156:159], v[196:199], v[26:29]
	v_mfma_f32_16x16x32_bf16 v[14:17], v[140:143], v[204:207], v[14:17]
	v_mfma_f32_16x16x32_bf16 v[10:13], v[156:159], v[204:207], v[10:13]
	v_lshl_add_u64 v[214:215], s[52:53], 0, v[130:131]
	s_add_i32 m0, s54, 0x2000
	s_nop 0
	global_load_lds_dwordx4 v[214:215], off
	v_mfma_f32_16x16x32_bf16 v[62:65], v[152:155], v[184:187], v[62:65]
	v_mfma_f32_16x16x32_bf16 v[58:61], v[160:163], v[184:187], v[58:61]
	v_mfma_f32_16x16x32_bf16 v[46:49], v[152:155], v[192:195], v[46:49]
	v_mfma_f32_16x16x32_bf16 v[42:45], v[160:163], v[192:195], v[42:45]
	v_mfma_f32_16x16x32_bf16 v[30:33], v[152:155], v[200:203], v[30:33]
	v_mfma_f32_16x16x32_bf16 v[26:29], v[160:163], v[200:203], v[26:29]
	v_mfma_f32_16x16x32_bf16 v[14:17], v[152:155], v[208:211], v[14:17]
	v_mfma_f32_16x16x32_bf16 v[10:13], v[160:163], v[208:211], v[10:13]
	v_lshl_add_u64 v[214:215], s[22:23], 0, v[134:135]
	s_mov_b32 m0, s29
	s_nop 0
	global_load_lds_dwordx4 v[214:215], off
	s_setprio 0
	s_setprio 1
	v_mfma_f32_16x16x32_bf16 v[54:57], v[164:167], v[180:183], v[54:57]
	v_mfma_f32_16x16x32_bf16 v[50:53], v[172:175], v[180:183], v[50:53]
	v_mfma_f32_16x16x32_bf16 v[38:41], v[164:167], v[188:191], v[38:41]
	v_mfma_f32_16x16x32_bf16 v[34:37], v[172:175], v[188:191], v[34:37]
	v_mfma_f32_16x16x32_bf16 v[22:25], v[164:167], v[196:199], v[22:25]
	v_mfma_f32_16x16x32_bf16 v[18:21], v[172:175], v[196:199], v[18:21]
	v_mfma_f32_16x16x32_bf16 v[6:9], v[164:167], v[204:207], v[6:9]
	v_mfma_f32_16x16x32_bf16 v[2:5], v[172:175], v[204:207], v[2:5]
	s_mov_b32 m0, s30
	s_nop 0
	global_load_lds_dwordx4 v[216:217], off
	v_mfma_f32_16x16x32_bf16 v[54:57], v[168:171], v[184:187], v[54:57]
	v_mfma_f32_16x16x32_bf16 v[50:53], v[176:179], v[184:187], v[50:53]
	v_mfma_f32_16x16x32_bf16 v[38:41], v[168:171], v[192:195], v[38:41]
	v_mfma_f32_16x16x32_bf16 v[34:37], v[176:179], v[192:195], v[34:37]
	v_mfma_f32_16x16x32_bf16 v[22:25], v[168:171], v[200:203], v[22:25]
	v_mfma_f32_16x16x32_bf16 v[18:21], v[176:179], v[200:203], v[18:21]
	v_mfma_f32_16x16x32_bf16 v[6:9], v[168:171], v[208:211], v[6:9]
	v_mfma_f32_16x16x32_bf16 v[2:5], v[176:179], v[208:211], v[2:5]
	s_setprio 0
	s_barrier
	s_add_i32 s52, 0, 0x18000
	s_add_i32 s53, 0, 0x1c000
	v_add_u32_e32 v160, s52, v149
	v_add_u32_e32 v176, s53, v149
	ds_read_b128 v[140:143], v160
	ds_read_b128 v[152:155], v160 offset:1024
	ds_read_b128 v[156:159], v160 offset:2048
	ds_read_b128 v[160:163], v160 offset:3072
	ds_read_b128 v[164:167], v176
	ds_read_b128 v[168:171], v176 offset:1024
	ds_read_b128 v[172:175], v176 offset:2048
	ds_read_b128 v[176:179], v176 offset:3072
	s_add_u32 s22, s22, 0x40000
	s_addc_u32 s23, s23, 0
	s_mov_b32 m0, s31
	v_lshl_add_u64 v[218:219], s[22:23], 0, v[134:135]
	ds_read_b128 v[180:183], v151 offset:32768
	ds_read_b128 v[184:187], v151 offset:33792
	ds_read_b128 v[188:191], v151 offset:34816
	ds_read_b128 v[192:195], v151 offset:35840
	ds_read_b128 v[196:199], v151 offset:36864
	ds_read_b128 v[200:203], v151 offset:37888
	ds_read_b128 v[204:207], v151 offset:38912
	ds_read_b128 v[208:211], v151 offset:39936
	global_load_lds_dwordx4 v[218:219], off
	v_lshl_add_u64 v[218:219], s[22:23], 0, v[132:133]
	s_mov_b32 m0, s36
	s_nop 0
	global_load_lds_dwordx4 v[218:219], off
	s_waitcnt vmcnt(8)
	s_waitcnt lgkmcnt(0)
	s_barrier
	s_setprio 1
	s_waitcnt lgkmcnt(0)
	v_mfma_f32_16x16x32_bf16 v[126:129], v[140:143], v[180:183], v[126:129]
	v_mfma_f32_16x16x32_bf16 v[122:125], v[156:159], v[180:183], v[122:125]
	v_mfma_f32_16x16x32_bf16 v[110:113], v[140:143], v[188:191], v[110:113]
	v_mfma_f32_16x16x32_bf16 v[106:109], v[156:159], v[188:191], v[106:109]
	v_mfma_f32_16x16x32_bf16 v[94:97], v[140:143], v[196:199], v[94:97]
	v_mfma_f32_16x16x32_bf16 v[90:93], v[156:159], v[196:199], v[90:93]
	v_mfma_f32_16x16x32_bf16 v[78:81], v[140:143], v[204:207], v[78:81]
	v_mfma_f32_16x16x32_bf16 v[74:77], v[156:159], v[204:207], v[74:77]
	v_mfma_f32_16x16x32_bf16 v[126:129], v[152:155], v[184:187], v[126:129]
	v_mfma_f32_16x16x32_bf16 v[122:125], v[160:163], v[184:187], v[122:125]
	v_mfma_f32_16x16x32_bf16 v[110:113], v[152:155], v[192:195], v[110:113]
	v_mfma_f32_16x16x32_bf16 v[106:109], v[160:163], v[192:195], v[106:109]
	v_mfma_f32_16x16x32_bf16 v[94:97], v[152:155], v[200:203], v[94:97]
	v_mfma_f32_16x16x32_bf16 v[90:93], v[160:163], v[200:203], v[90:93]
	v_mfma_f32_16x16x32_bf16 v[78:81], v[152:155], v[208:211], v[78:81]
	v_mfma_f32_16x16x32_bf16 v[74:77], v[160:163], v[208:211], v[74:77]
	s_setprio 0
	s_setprio 1
	v_mfma_f32_16x16x32_bf16 v[118:121], v[164:167], v[180:183], v[118:121]
	v_mfma_f32_16x16x32_bf16 v[114:117], v[172:175], v[180:183], v[114:117]
	v_mfma_f32_16x16x32_bf16 v[102:105], v[164:167], v[188:191], v[102:105]
	v_mfma_f32_16x16x32_bf16 v[98:101], v[172:175], v[188:191], v[98:101]
	v_mfma_f32_16x16x32_bf16 v[86:89], v[164:167], v[196:199], v[86:89]
	v_mfma_f32_16x16x32_bf16 v[82:85], v[172:175], v[196:199], v[82:85]
	v_mfma_f32_16x16x32_bf16 v[70:73], v[164:167], v[204:207], v[70:73]
	v_mfma_f32_16x16x32_bf16 v[66:69], v[172:175], v[204:207], v[66:69]
	v_mfma_f32_16x16x32_bf16 v[118:121], v[168:171], v[184:187], v[118:121]
	v_mfma_f32_16x16x32_bf16 v[114:117], v[176:179], v[184:187], v[114:117]
	v_mfma_f32_16x16x32_bf16 v[102:105], v[168:171], v[192:195], v[102:105]
	v_mfma_f32_16x16x32_bf16 v[98:101], v[176:179], v[192:195], v[98:101]
	v_mfma_f32_16x16x32_bf16 v[86:89], v[168:171], v[200:203], v[86:89]
	v_mfma_f32_16x16x32_bf16 v[82:85], v[176:179], v[200:203], v[82:85]
	v_mfma_f32_16x16x32_bf16 v[70:73], v[168:171], v[208:211], v[70:73]
	v_mfma_f32_16x16x32_bf16 v[66:69], v[176:179], v[208:211], v[66:69]
	s_setprio 0
	s_barrier
; #define PG8_STAGE(bufoff, gbase, voff) do { _Pragma("unroll") for (int _i = 0; _i < 2; ++_i) \
;         __builtin_amdgcn_global_load_lds((const unsigned*)((const char*)(gbase) + (voff)[_i]), (PG8_LAS unsigned*)(lds + (bufoff) + ldsw + _i * 8192), 16, 0, 0); } while (0)
; #define PG8_WAIT_V(n) asm volatile("s_waitcnt vmcnt(" #n ")" ::: "memory")
; #define PG8_BAR __builtin_amdgcn_s_barrier()
; template <class Epi, class Sched, bool ALIGN_EPI = false, bool SP2 = false, bool GATHER = false>
; __device__ __forceinline__ void gemm_phase(PG8_LAS unsigned char* lds, const Gemm g, const Sched& S, const Epi& E, int tid_in, const int* rowsrc = nullptr, PG8_LAS int* idx_lds = nullptr) {
;     ...
;         for (int t = 0; t < nt; t += 2) {
;             const bool last = (t == nt - 2);
;             if constexpr (GATHER) {
; #pragma unroll
;                 for (int h_ = 0; h_ < 2; ++h_) { gS[h_][0] = last ? gN[h_][0] : gA[h_][0]; gS[h_][1] = last ? gN[h_][1] : gA[h_][1]; } }
;             const char* a1 = cA + (size_t)(t + 1) * kstep;
;             const char* a2 = last ? nA : cA + (size_t)(t + 2) * kstep; const char* b2 = last ? nB : cB + (size_t)(t + 2) * kstep;
;             const char* a3 = a2 + kstep; const char* b3 = b2 + kstep;
;             if (last && has_next) S.a_ready(nxt);
;             if constexpr (SP2) {
;             PG8_LDB(B0, 0, 0); PG8_LDB(B1, 0, 1); PG8_SCHED; PG8_LDA(At, 0, 0); PG8_STAGE(PG8_SA(1, 1), a1 + hstepA, PG8_OA(1));
;             PG8_WAIT_V(8); PG8_WAIT_L(0); PG8_BAR; PG8_MMA(0, 0, At, B0); PG8_MMA(0, 1, At, B1); PG8_BAR; PG8_SCHED;
;             PG8_LDA(At, 0, 1); PG8_STAGE(PG8_SB(0, 0), b2, voffB); PG8_STAGE(PG8_SB(0, 1), b2 + hstep, voffB); PG8_STAGE(PG8_SA(0, 0), a2, PG8_OS(0));
;             PG8_WAIT_V(8); PG8_WAIT_L(0); PG8_BAR; PG8_MMA(1, 0, At, B0); PG8_MMA(1, 1, At, B1); PG8_BAR; PG8_SCHED;
;             PG8_LDB(B0, 1, 0); PG8_LDB(B1, 1, 1); PG8_SCHED; PG8_LDA(At, 1, 0); PG8_STAGE(PG8_SA(0, 1), a2 + hstepA, PG8_OS(1));
;             PG8_WAIT_V(8); PG8_WAIT_L(0); PG8_BAR; PG8_MMA(0, 0, At, B0); PG8_MMA(0, 1, At, B1); PG8_BAR; PG8_SCHED;
;             PG8_LDA(At, 1, 1); PG8_STAGE(PG8_SB(1, 0), b3, voffB); PG8_STAGE(PG8_SB(1, 1), b3 + hstep, voffB); PG8_STAGE(PG8_SA(1, 0), a3, PG8_OS(0));
;             PG8_WAIT_V(8); PG8_WAIT_L(0); PG8_BAR; PG8_MMA(1, 0, At, B0); PG8_MMA(1, 1, At, B1); PG8_BAR; PG8_SCHED;
	s_add_i32 s22, s52, s28
	v_lshl_add_u64 v[144:145], v[144:145], 0, s[10:11]
	s_mov_b32 m0, s22
	ds_read_b128 v[180:183], v151 offset:49152
	ds_read_b128 v[184:187], v151 offset:50176
	ds_read_b128 v[188:191], v151 offset:51200
	ds_read_b128 v[192:195], v151 offset:52224
	ds_read_b128 v[196:199], v151 offset:53248
	ds_read_b128 v[200:203], v151 offset:54272
	ds_read_b128 v[204:207], v151 offset:55296
	ds_read_b128 v[208:211], v151 offset:56320
	global_load_lds_dwordx4 v[144:145], off
	s_add_i32 m0, s22, 0x2000
	s_add_u32 s20, s20, 0x40080
	v_lshl_add_u64 v[144:145], v[212:213], 0, s[10:11]
	s_addc_u32 s21, s21, 0
	s_add_i32 s22, s53, s28
	global_load_lds_dwordx4 v[144:145], off
	v_lshl_add_u64 v[144:145], s[20:21], 0, v[0:1]
	s_mov_b32 m0, s22
	s_nop 0
	global_load_lds_dwordx4 v[144:145], off
	s_waitcnt vmcnt(5)
	s_waitcnt lgkmcnt(0)
	s_barrier
	s_setprio 1
	s_waitcnt lgkmcnt(0)
	v_mfma_f32_16x16x32_bf16 v[62:65], v[140:143], v[180:183], v[62:65]
	v_mfma_f32_16x16x32_bf16 v[58:61], v[156:159], v[180:183], v[58:61]
	v_mfma_f32_16x16x32_bf16 v[46:49], v[140:143], v[188:191], v[46:49]
	v_mfma_f32_16x16x32_bf16 v[42:45], v[156:159], v[188:191], v[42:45]
	v_mfma_f32_16x16x32_bf16 v[30:33], v[140:143], v[196:199], v[30:33]
	v_mfma_f32_16x16x32_bf16 v[26:29], v[156:159], v[196:199], v[26:29]
	v_mfma_f32_16x16x32_bf16 v[14:17], v[140:143], v[204:207], v[14:17]
	v_mfma_f32_16x16x32_bf16 v[10:13], v[156:159], v[204:207], v[10:13]
	v_lshl_add_u64 v[144:145], s[20:21], 0, v[130:131]
	s_add_i32 m0, s22, 0x2000
	s_nop 0
	global_load_lds_dwordx4 v[144:145], off
	v_mfma_f32_16x16x32_bf16 v[62:65], v[152:155], v[184:187], v[62:65]
	v_mfma_f32_16x16x32_bf16 v[58:61], v[160:163], v[184:187], v[58:61]
	v_mfma_f32_16x16x32_bf16 v[46:49], v[152:155], v[192:195], v[46:49]
	v_mfma_f32_16x16x32_bf16 v[42:45], v[160:163], v[192:195], v[42:45]
	v_mfma_f32_16x16x32_bf16 v[30:33], v[152:155], v[200:203], v[30:33]
	v_mfma_f32_16x16x32_bf16 v[26:29], v[160:163], v[200:203], v[26:29]
	v_mfma_f32_16x16x32_bf16 v[14:17], v[152:155], v[208:211], v[14:17]
	v_mfma_f32_16x16x32_bf16 v[10:13], v[160:163], v[208:211], v[10:13]
	v_lshl_add_u64 v[144:145], v[214:215], 0, s[10:11]
	s_mov_b32 m0, s38
	s_nop 0
	global_load_lds_dwordx4 v[144:145], off
	s_setprio 0
	s_setprio 1
	v_mfma_f32_16x16x32_bf16 v[54:57], v[164:167], v[180:183], v[54:57]
	v_mfma_f32_16x16x32_bf16 v[50:53], v[172:175], v[180:183], v[50:53]
	v_mfma_f32_16x16x32_bf16 v[38:41], v[164:167], v[188:191], v[38:41]
	v_mfma_f32_16x16x32_bf16 v[34:37], v[172:175], v[188:191], v[34:37]
	v_mfma_f32_16x16x32_bf16 v[22:25], v[164:167], v[196:199], v[22:25]
	v_mfma_f32_16x16x32_bf16 v[18:21], v[172:175], v[196:199], v[18:21]
	v_mfma_f32_16x16x32_bf16 v[6:9], v[164:167], v[204:207], v[6:9]
	v_mfma_f32_16x16x32_bf16 v[2:5], v[172:175], v[204:207], v[2:5]
	v_lshl_add_u64 v[144:145], v[216:217], 0, s[10:11]
	s_mov_b32 m0, s39
	s_nop 0
	global_load_lds_dwordx4 v[144:145], off
	v_mfma_f32_16x16x32_bf16 v[54:57], v[168:171], v[184:187], v[54:57]
	v_mfma_f32_16x16x32_bf16 v[50:53], v[176:179], v[184:187], v[50:53]
	v_mfma_f32_16x16x32_bf16 v[38:41], v[168:171], v[192:195], v[38:41]
	v_mfma_f32_16x16x32_bf16 v[34:37], v[176:179], v[192:195], v[34:37]
	v_mfma_f32_16x16x32_bf16 v[22:25], v[168:171], v[200:203], v[22:25]
	v_mfma_f32_16x16x32_bf16 v[18:21], v[176:179], v[200:203], v[18:21]
	v_mfma_f32_16x16x32_bf16 v[6:9], v[168:171], v[208:211], v[6:9]
	v_mfma_f32_16x16x32_bf16 v[2:5], v[176:179], v[208:211], v[2:5]
	s_setprio 0
	s_barrier
	s_add_i32 s51, s51, 2
	s_add_u32 s18, s18, 0x100
	s_addc_u32 s19, s19, 0
	s_add_u32 s49, s49, 0x100
	s_addc_u32 s50, s50, 0
	s_cmp_gt_u32 s51, 13
	s_cbranch_scc0 .LBB0_390
	s_and_b64 vcc, exec, s[6:7]
	s_cbranch_vccz .LBB0_393
	s_barrier

; #define PG8_STAGE(bufoff, gbase, voff) do { _Pragma("unroll") for (int _i = 0; _i < 2; ++_i) \
;         __builtin_amdgcn_global_load_lds((const unsigned*)((const char*)(gbase) + (voff)[_i]), (PG8_LAS unsigned*)(lds + (bufoff) + ldsw + _i * 8192), 16, 0, 0); } while (0)
; #define PG8_WAIT_V(n) asm volatile("s_waitcnt vmcnt(" #n ")" ::: "memory")
; #define PG8_BAR __builtin_amdgcn_s_barrier()
; template <class Epi, class Sched, bool ALIGN_EPI = false, bool SP2 = false, bool GATHER = false>
; __device__ __forceinline__ void gemm_phase(PG8_LAS unsigned char* lds, const Gemm g, const Sched& S, const Epi& E, int tid_in, const int* rowsrc = nullptr, PG8_LAS int* idx_lds = nullptr) {
;     ...
;         for (int t = 0; t < nt; t += 2) {
;             const bool last = (t == nt - 2);
;             if constexpr (GATHER) {
; #pragma unroll
;                 for (int h_ = 0; h_ < 2; ++h_) { gS[h_][0] = last ? gN[h_][0] : gA[h_][0]; gS[h_][1] = last ? gN[h_][1] : gA[h_][1]; } }
;             const char* a1 = cA + (size_t)(t + 1) * kstep;
;             const char* a2 = last ? nA : cA + (size_t)(t + 2) * kstep; const char* b2 = last ? nB : cB + (size_t)(t + 2) * kstep;
;             const char* a3 = a2 + kstep; const char* b3 = b2 + kstep;
;             if (last && has_next) S.a_ready(nxt);
;             if constexpr (SP2) {
;             PG8_LDB(B0, 0, 0); PG8_LDB(B1, 0, 1); PG8_SCHED; PG8_LDA(At, 0, 0); PG8_STAGE(PG8_SA(1, 1), a1 + hstepA, PG8_OA(1));
;             PG8_WAIT_V(8); PG8_WAIT_L(0); PG8_BAR; PG8_MMA(0, 0, At, B0); PG8_MMA(0, 1, At, B1); PG8_BAR; PG8_SCHED;
;             PG8_LDA(At, 0, 1); PG8_STAGE(PG8_SB(0, 0), b2, voffB); PG8_STAGE(PG8_SB(0, 1), b2 + hstep, voffB); PG8_STAGE(PG8_SA(0, 0), a2, PG8_OS(0));
;             PG8_WAIT_V(8); PG8_WAIT_L(0); PG8_BAR; PG8_MMA(1, 0, At, B0); PG8_MMA(1, 1, At, B1); PG8_BAR; PG8_SCHED;
;             PG8_LDB(B0, 1, 0); PG8_LDB(B1, 1, 1); PG8_SCHED; PG8_LDA(At, 1, 0); PG8_STAGE(PG8_SA(0, 1), a2 + hstepA, PG8_OS(1));
;             PG8_WAIT_V(8); PG8_WAIT_L(0); PG8_BAR; PG8_MMA(0, 0, At, B0); PG8_MMA(0, 1, At, B1); PG8_BAR; PG8_SCHED;
;             PG8_LDA(At, 1, 1); PG8_STAGE(PG8_SB(1, 0), b3, voffB); PG8_STAGE(PG8_SB(1, 1), b3 + hstep, voffB); PG8_STAGE(PG8_SA(1, 0), a3, PG8_OS(0));
;             PG8_WAIT_V(8); PG8_WAIT_L(0); PG8_BAR; PG8_MMA(1, 0, At, B0); PG8_MMA(1, 1, At, B1); PG8_BAR; PG8_SCHED;
.LBB0_615:
	s_add_u32 s22, s20, 0xfff80080
	s_addc_u32 s23, s21, -1
	s_add_i32 s58, 0, 0x10000
	s_cmp_eq_u32 s57, 28
	s_cselect_b32 s25, s9, s23
	s_cselect_b32 s24, s17, s22
	s_cselect_b32 s23, s7, s56
	s_cselect_b32 s22, s19, s55
	s_add_i32 s60, 0, 0x14000
	v_add_u32_e32 v142, s58, v184
	v_add_u32_e32 v182, s60, v184
	ds_read_b128 v[122:125], v142
	ds_read_b128 v[126:129], v142 offset:1024
	ds_read_b128 v[134:137], v142 offset:2048
	ds_read_b128 v[142:145], v142 offset:3072
	ds_read_b128 v[174:177], v182
	ds_read_b128 v[178:181], v182 offset:1024
	ds_read_b128 v[188:191], v182 offset:2048
	ds_read_b128 v[192:195], v182 offset:3072
	v_lshl_add_u64 v[182:183], s[20:21], 0, v[170:171]
	s_add_i32 m0, s39, 0xc000
	ds_read_b128 v[196:199], v186
	ds_read_b128 v[200:203], v186 offset:1024
	ds_read_b128 v[204:207], v186 offset:2048
	ds_read_b128 v[208:211], v186 offset:3072
	ds_read_b128 v[212:215], v186 offset:4096
	ds_read_b128 v[216:219], v186 offset:5120
	ds_read_b128 v[220:223], v186 offset:6144
	ds_read_b128 v[224:227], v186 offset:7168
	global_load_lds_dwordx4 v[182:183], off
	v_lshl_add_u64 v[182:183], s[20:21], 0, v[172:173]
	s_add_i32 m0, s39, 0xe000
	s_nop 0
	global_load_lds_dwordx4 v[182:183], off
	s_waitcnt vmcnt(8)
	s_waitcnt lgkmcnt(0)
	s_barrier
	s_setprio 1
	s_waitcnt lgkmcnt(0)
	v_mfma_f32_16x16x32_bf16 v[138:141], v[122:125], v[196:199], v[138:141]
	v_mfma_f32_16x16x32_bf16 v[130:133], v[134:137], v[196:199], v[130:133]
	v_mfma_f32_16x16x32_bf16 v[118:121], v[122:125], v[204:207], v[118:121]
	v_mfma_f32_16x16x32_bf16 v[106:109], v[134:137], v[204:207], v[106:109]
	v_mfma_f32_16x16x32_bf16 v[102:105], v[122:125], v[212:215], v[102:105]
	v_mfma_f32_16x16x32_bf16 v[90:93], v[134:137], v[212:215], v[90:93]
	v_mfma_f32_16x16x32_bf16 v[86:89], v[122:125], v[220:223], v[86:89]
	v_mfma_f32_16x16x32_bf16 v[74:77], v[134:137], v[220:223], v[74:77]
	v_mfma_f32_16x16x32_bf16 v[138:141], v[126:129], v[200:203], v[138:141]
	v_mfma_f32_16x16x32_bf16 v[130:133], v[142:145], v[200:203], v[130:133]
	v_mfma_f32_16x16x32_bf16 v[118:121], v[126:129], v[208:211], v[118:121]
	v_mfma_f32_16x16x32_bf16 v[106:109], v[142:145], v[208:211], v[106:109]
	v_mfma_f32_16x16x32_bf16 v[102:105], v[126:129], v[216:219], v[102:105]
	v_mfma_f32_16x16x32_bf16 v[90:93], v[142:145], v[216:219], v[90:93]
	v_mfma_f32_16x16x32_bf16 v[86:89], v[126:129], v[224:227], v[86:89]
	v_mfma_f32_16x16x32_bf16 v[74:77], v[142:145], v[224:227], v[74:77]
	s_setprio 0
	s_setprio 1
	v_mfma_f32_16x16x32_bf16 v[114:117], v[174:177], v[196:199], v[114:117]
	v_mfma_f32_16x16x32_bf16 v[110:113], v[188:191], v[196:199], v[110:113]
	v_mfma_f32_16x16x32_bf16 v[98:101], v[174:177], v[204:207], v[98:101]
	v_mfma_f32_16x16x32_bf16 v[94:97], v[188:191], v[204:207], v[94:97]
	v_mfma_f32_16x16x32_bf16 v[82:85], v[174:177], v[212:215], v[82:85]
	v_mfma_f32_16x16x32_bf16 v[78:81], v[188:191], v[212:215], v[78:81]
	v_mfma_f32_16x16x32_bf16 v[70:73], v[174:177], v[220:223], v[70:73]
	v_mfma_f32_16x16x32_bf16 v[66:69], v[188:191], v[220:223], v[66:69]
	v_mfma_f32_16x16x32_bf16 v[114:117], v[178:181], v[200:203], v[114:117]
	v_mfma_f32_16x16x32_bf16 v[110:113], v[192:195], v[200:203], v[110:113]
	v_mfma_f32_16x16x32_bf16 v[98:101], v[178:181], v[208:211], v[98:101]
	v_mfma_f32_16x16x32_bf16 v[94:97], v[192:195], v[208:211], v[94:97]
	v_mfma_f32_16x16x32_bf16 v[82:85], v[178:181], v[216:219], v[82:85]
	v_mfma_f32_16x16x32_bf16 v[78:81], v[192:195], v[216:219], v[78:81]
	v_mfma_f32_16x16x32_bf16 v[70:73], v[178:181], v[224:227], v[70:73]
	v_mfma_f32_16x16x32_bf16 v[66:69], v[192:195], v[224:227], v[66:69]
	s_setprio 0
	s_barrier
	s_add_i32 s58, s58, s38
	v_lshl_add_u64 v[182:183], s[22:23], 0, v[0:1]
	s_mov_b32 m0, s58
	ds_read_b128 v[196:199], v186 offset:16384
	ds_read_b128 v[200:203], v186 offset:17408
	ds_read_b128 v[204:207], v186 offset:18432
	ds_read_b128 v[208:211], v186 offset:19456
	ds_read_b128 v[212:215], v186 offset:20480
	ds_read_b128 v[216:219], v186 offset:21504
	ds_read_b128 v[220:223], v186 offset:22528
	ds_read_b128 v[224:227], v186 offset:23552
	global_load_lds_dwordx4 v[182:183], off
	s_add_i32 m0, s58, 0x2000
	s_add_u32 s58, s22, 0x80000
	v_lshl_add_u64 v[228:229], s[22:23], 0, v[148:149]
	s_addc_u32 s59, s23, 0
	s_add_i32 s60, s60, s38
	global_load_lds_dwordx4 v[228:229], off
	v_lshl_add_u64 v[230:231], s[58:59], 0, v[0:1]
	s_mov_b32 m0, s60
	v_lshl_add_u64 v[232:233], s[24:25], 0, v[150:151]
	global_load_lds_dwordx4 v[230:231], off
	s_waitcnt vmcnt(5)
	s_waitcnt lgkmcnt(0)
	s_barrier
; #define PG8_STAGE(bufoff, gbase, voff) do { _Pragma("unroll") for (int _i = 0; _i < 2; ++_i) \
;         __builtin_amdgcn_global_load_lds((const unsigned*)((const char*)(gbase) + (voff)[_i]), (PG8_LAS unsigned*)(lds + (bufoff) + ldsw + _i * 8192), 16, 0, 0); } while (0)
; #define PG8_WAIT_V(n) asm volatile("s_waitcnt vmcnt(" #n ")" ::: "memory")
; #define PG8_BAR __builtin_amdgcn_s_barrier()
; template <class Epi, class Sched, bool ALIGN_EPI = false, bool SP2 = false, bool GATHER = false>
; __device__ __forceinline__ void gemm_phase(PG8_LAS unsigned char* lds, const Gemm g, const Sched& S, const Epi& E, int tid_in, const int* rowsrc = nullptr, PG8_LAS int* idx_lds = nullptr) {
;     ...
;         for (int t = 0; t < nt; t += 2) {
;             const bool last = (t == nt - 2);
;             if constexpr (GATHER) {
; #pragma unroll
;                 for (int h_ = 0; h_ < 2; ++h_) { gS[h_][0] = last ? gN[h_][0] : gA[h_][0]; gS[h_][1] = last ? gN[h_][1] : gA[h_][1]; } }
;             const char* a1 = cA + (size_t)(t + 1) * kstep;
;             const char* a2 = last ? nA : cA + (size_t)(t + 2) * kstep; const char* b2 = last ? nB : cB + (size_t)(t + 2) * kstep;
;             const char* a3 = a2 + kstep; const char* b3 = b2 + kstep;
;             if (last && has_next) S.a_ready(nxt);
;             if constexpr (SP2) {
;             PG8_LDB(B0, 0, 0); PG8_LDB(B1, 0, 1); PG8_SCHED; PG8_LDA(At, 0, 0); PG8_STAGE(PG8_SA(1, 1), a1 + hstepA, PG8_OA(1));
;             PG8_WAIT_V(8); PG8_WAIT_L(0); PG8_BAR; PG8_MMA(0, 0, At, B0); PG8_MMA(0, 1, At, B1); PG8_BAR; PG8_SCHED;
;             PG8_LDA(At, 0, 1); PG8_STAGE(PG8_SB(0, 0), b2, voffB); PG8_STAGE(PG8_SB(0, 1), b2 + hstep, voffB); PG8_STAGE(PG8_SA(0, 0), a2, PG8_OS(0));
;             PG8_WAIT_V(8); PG8_WAIT_L(0); PG8_BAR; PG8_MMA(1, 0, At, B0); PG8_MMA(1, 1, At, B1); PG8_BAR; PG8_SCHED;
;             PG8_LDB(B0, 1, 0); PG8_LDB(B1, 1, 1); PG8_SCHED; PG8_LDA(At, 1, 0); PG8_STAGE(PG8_SA(0, 1), a2 + hstepA, PG8_OS(1));
;             PG8_WAIT_V(8); PG8_WAIT_L(0); PG8_BAR; PG8_MMA(0, 0, At, B0); PG8_MMA(0, 1, At, B1); PG8_BAR; PG8_SCHED;
;             PG8_LDA(At, 1, 1); PG8_STAGE(PG8_SB(1, 0), b3, voffB); PG8_STAGE(PG8_SB(1, 1), b3 + hstep, voffB); PG8_STAGE(PG8_SA(1, 0), a3, PG8_OS(0));
;             PG8_WAIT_V(8); PG8_WAIT_L(0); PG8_BAR; PG8_MMA(1, 0, At, B0); PG8_MMA(1, 1, At, B1); PG8_BAR; PG8_SCHED;
	s_setprio 1
	s_waitcnt lgkmcnt(0)
	v_mfma_f32_16x16x32_bf16 v[62:65], v[122:125], v[196:199], v[62:65]
	v_mfma_f32_16x16x32_bf16 v[58:61], v[134:137], v[196:199], v[58:61]
	v_mfma_f32_16x16x32_bf16 v[54:57], v[122:125], v[204:207], v[54:57]
	v_mfma_f32_16x16x32_bf16 v[42:45], v[134:137], v[204:207], v[42:45]
	v_mfma_f32_16x16x32_bf16 v[38:41], v[122:125], v[212:215], v[38:41]
	v_mfma_f32_16x16x32_bf16 v[26:29], v[134:137], v[212:215], v[26:29]
	v_mfma_f32_16x16x32_bf16 v[22:25], v[122:125], v[220:223], v[22:25]
	v_mfma_f32_16x16x32_bf16 v[10:13], v[134:137], v[220:223], v[10:13]
	v_lshl_add_u64 v[230:231], s[58:59], 0, v[148:149]
	s_add_i32 m0, s60, 0x2000
	s_nop 0
	global_load_lds_dwordx4 v[230:231], off
	v_mfma_f32_16x16x32_bf16 v[62:65], v[126:129], v[200:203], v[62:65]
	v_mfma_f32_16x16x32_bf16 v[58:61], v[142:145], v[200:203], v[58:61]
	v_mfma_f32_16x16x32_bf16 v[54:57], v[126:129], v[208:211], v[54:57]
	v_mfma_f32_16x16x32_bf16 v[42:45], v[142:145], v[208:211], v[42:45]
	v_mfma_f32_16x16x32_bf16 v[38:41], v[126:129], v[216:219], v[38:41]
	v_mfma_f32_16x16x32_bf16 v[26:29], v[142:145], v[216:219], v[26:29]
	v_mfma_f32_16x16x32_bf16 v[22:25], v[126:129], v[224:227], v[22:25]
	v_mfma_f32_16x16x32_bf16 v[10:13], v[142:145], v[224:227], v[10:13]
	v_lshl_add_u64 v[230:231], s[24:25], 0, v[152:153]
	s_mov_b32 m0, s39
	s_nop 0
	global_load_lds_dwordx4 v[230:231], off
	s_setprio 0
	s_setprio 1
	v_mfma_f32_16x16x32_bf16 v[50:53], v[174:177], v[196:199], v[50:53]
	v_mfma_f32_16x16x32_bf16 v[46:49], v[188:191], v[196:199], v[46:49]
	v_mfma_f32_16x16x32_bf16 v[34:37], v[174:177], v[204:207], v[34:37]
	v_mfma_f32_16x16x32_bf16 v[30:33], v[188:191], v[204:207], v[30:33]
	v_mfma_f32_16x16x32_bf16 v[18:21], v[174:177], v[212:215], v[18:21]
	v_mfma_f32_16x16x32_bf16 v[14:17], v[188:191], v[212:215], v[14:17]
	v_mfma_f32_16x16x32_bf16 v[6:9], v[174:177], v[220:223], v[6:9]
	v_mfma_f32_16x16x32_bf16 v[2:5], v[188:191], v[220:223], v[2:5]
	s_mov_b32 m0, s41
	s_nop 0
	global_load_lds_dwordx4 v[232:233], off
	v_mfma_f32_16x16x32_bf16 v[50:53], v[178:181], v[200:203], v[50:53]
	v_mfma_f32_16x16x32_bf16 v[46:49], v[192:195], v[200:203], v[46:49]
	v_mfma_f32_16x16x32_bf16 v[34:37], v[178:181], v[208:211], v[34:37]
	v_mfma_f32_16x16x32_bf16 v[30:33], v[192:195], v[208:211], v[30:33]
	v_mfma_f32_16x16x32_bf16 v[18:21], v[178:181], v[216:219], v[18:21]
	v_mfma_f32_16x16x32_bf16 v[14:17], v[192:195], v[216:219], v[14:17]
	v_mfma_f32_16x16x32_bf16 v[6:9], v[178:181], v[224:227], v[6:9]
	v_mfma_f32_16x16x32_bf16 v[2:5], v[192:195], v[224:227], v[2:5]
	s_setprio 0
	s_barrier
	s_add_i32 s58, 0, 0x18000
	s_add_i32 s59, 0, 0x1c000
	v_add_u32_e32 v142, s58, v184
	v_add_u32_e32 v187, s59, v184
	ds_read_b128 v[122:125], v142
	ds_read_b128 v[126:129], v142 offset:1024
	ds_read_b128 v[134:137], v142 offset:2048
	ds_read_b128 v[142:145], v142 offset:3072
	ds_read_b128 v[174:177], v187
	ds_read_b128 v[178:181], v187 offset:1024
	ds_read_b128 v[188:191], v187 offset:2048
	ds_read_b128 v[192:195], v187 offset:3072
	s_add_u32 s24, s24, 0x80000
	s_addc_u32 s25, s25, 0
	s_mov_b32 m0, s43
	v_lshl_add_u64 v[234:235], s[24:25], 0, v[152:153]
	ds_read_b128 v[196:199], v186 offset:32768
	ds_read_b128 v[200:203], v186 offset:33792
	ds_read_b128 v[204:207], v186 offset:34816
	ds_read_b128 v[208:211], v186 offset:35840
	ds_read_b128 v[212:215], v186 offset:36864
	ds_read_b128 v[216:219], v186 offset:37888
	ds_read_b128 v[220:223], v186 offset:38912
	ds_read_b128 v[224:227], v186 offset:39936
	global_load_lds_dwordx4 v[234:235], off
	v_lshl_add_u64 v[234:235], s[24:25], 0, v[150:151]
	s_mov_b32 m0, s45
	s_nop 0
	global_load_lds_dwordx4 v[234:235], off
	s_waitcnt vmcnt(8)
	s_waitcnt lgkmcnt(0)
	s_barrier
	s_setprio 1
	s_waitcnt lgkmcnt(0)
	v_mfma_f32_16x16x32_bf16 v[138:141], v[122:125], v[196:199], v[138:141]
	v_mfma_f32_16x16x32_bf16 v[130:133], v[134:137], v[196:199], v[130:133]
	v_mfma_f32_16x16x32_bf16 v[118:121], v[122:125], v[204:207], v[118:121]
	v_mfma_f32_16x16x32_bf16 v[106:109], v[134:137], v[204:207], v[106:109]
	v_mfma_f32_16x16x32_bf16 v[102:105], v[122:125], v[212:215], v[102:105]
	v_mfma_f32_16x16x32_bf16 v[90:93], v[134:137], v[212:215], v[90:93]
	v_mfma_f32_16x16x32_bf16 v[86:89], v[122:125], v[220:223], v[86:89]
	v_mfma_f32_16x16x32_bf16 v[74:77], v[134:137], v[220:223], v[74:77]
	v_mfma_f32_16x16x32_bf16 v[138:141], v[126:129], v[200:203], v[138:141]
	v_mfma_f32_16x16x32_bf16 v[130:133], v[142:145], v[200:203], v[130:133]
	v_mfma_f32_16x16x32_bf16 v[118:121], v[126:129], v[208:211], v[118:121]
	v_mfma_f32_16x16x32_bf16 v[106:109], v[142:145], v[208:211], v[106:109]
	v_mfma_f32_16x16x32_bf16 v[102:105], v[126:129], v[216:219], v[102:105]
	v_mfma_f32_16x16x32_bf16 v[90:93], v[142:145], v[216:219], v[90:93]
	v_mfma_f32_16x16x32_bf16 v[86:89], v[126:129], v[224:227], v[86:89]
	v_mfma_f32_16x16x32_bf16 v[74:77], v[142:145], v[224:227], v[74:77]
	s_setprio 0
	s_setprio 1
	v_mfma_f32_16x16x32_bf16 v[114:117], v[174:177], v[196:199], v[114:117]
	v_mfma_f32_16x16x32_bf16 v[110:113], v[188:191], v[196:199], v[110:113]
	v_mfma_f32_16x16x32_bf16 v[98:101], v[174:177], v[204:207], v[98:101]
	v_mfma_f32_16x16x32_bf16 v[94:97], v[188:191], v[204:207], v[94:97]
	v_mfma_f32_16x16x32_bf16 v[82:85], v[174:177], v[212:215], v[82:85]
	v_mfma_f32_16x16x32_bf16 v[78:81], v[188:191], v[212:215], v[78:81]
	v_mfma_f32_16x16x32_bf16 v[70:73], v[174:177], v[220:223], v[70:73]
	v_mfma_f32_16x16x32_bf16 v[66:69], v[188:191], v[220:223], v[66:69]
	v_mfma_f32_16x16x32_bf16 v[114:117], v[178:181], v[200:203], v[114:117]
	v_mfma_f32_16x16x32_bf16 v[110:113], v[192:195], v[200:203], v[110:113]
	v_mfma_f32_16x16x32_bf16 v[98:101], v[178:181], v[208:211], v[98:101]
	v_mfma_f32_16x16x32_bf16 v[94:97], v[192:195], v[208:211], v[94:97]
	v_mfma_f32_16x16x32_bf16 v[82:85], v[178:181], v[216:219], v[82:85]
	v_mfma_f32_16x16x32_bf16 v[78:81], v[192:195], v[216:219], v[78:81]
	v_mfma_f32_16x16x32_bf16 v[70:73], v[178:181], v[224:227], v[70:73]
	v_mfma_f32_16x16x32_bf16 v[66:69], v[192:195], v[224:227], v[66:69]
	s_setprio 0
	s_barrier
; #define PG8_STAGE(bufoff, gbase, voff) do { _Pragma("unroll") for (int _i = 0; _i < 2; ++_i) \
;         __builtin_amdgcn_global_load_lds((const unsigned*)((const char*)(gbase) + (voff)[_i]), (PG8_LAS unsigned*)(lds + (bufoff) + ldsw + _i * 8192), 16, 0, 0); } while (0)
; #define PG8_WAIT_V(n) asm volatile("s_waitcnt vmcnt(" #n ")" ::: "memory")
; #define PG8_BAR __builtin_amdgcn_s_barrier()
; template <class Epi, class Sched, bool ALIGN_EPI = false, bool SP2 = false, bool GATHER = false>
; __device__ __forceinline__ void gemm_phase(PG8_LAS unsigned char* lds, const Gemm g, const Sched& S, const Epi& E, int tid_in, const int* rowsrc = nullptr, PG8_LAS int* idx_lds = nullptr) {
;     ...
;         for (int t = 0; t < nt; t += 2) {
;             const bool last = (t == nt - 2);
;             if constexpr (GATHER) {
; #pragma unroll
;                 for (int h_ = 0; h_ < 2; ++h_) { gS[h_][0] = last ? gN[h_][0] : gA[h_][0]; gS[h_][1] = last ? gN[h_][1] : gA[h_][1]; } }
;             const char* a1 = cA + (size_t)(t + 1) * kstep;
;             const char* a2 = last ? nA : cA + (size_t)(t + 2) * kstep; const char* b2 = last ? nB : cB + (size_t)(t + 2) * kstep;
;             const char* a3 = a2 + kstep; const char* b3 = b2 + kstep;
;             if (last && has_next) S.a_ready(nxt);
;             if constexpr (SP2) {
;             PG8_LDB(B0, 0, 0); PG8_LDB(B1, 0, 1); PG8_SCHED; PG8_LDA(At, 0, 0); PG8_STAGE(PG8_SA(1, 1), a1 + hstepA, PG8_OA(1));
;             PG8_WAIT_V(8); PG8_WAIT_L(0); PG8_BAR; PG8_MMA(0, 0, At, B0); PG8_MMA(0, 1, At, B1); PG8_BAR; PG8_SCHED;
;             PG8_LDA(At, 0, 1); PG8_STAGE(PG8_SB(0, 0), b2, voffB); PG8_STAGE(PG8_SB(0, 1), b2 + hstep, voffB); PG8_STAGE(PG8_SA(0, 0), a2, PG8_OS(0));
;             PG8_WAIT_V(8); PG8_WAIT_L(0); PG8_BAR; PG8_MMA(1, 0, At, B0); PG8_MMA(1, 1, At, B1); PG8_BAR; PG8_SCHED;
;             PG8_LDB(B0, 1, 0); PG8_LDB(B1, 1, 1); PG8_SCHED; PG8_LDA(At, 1, 0); PG8_STAGE(PG8_SA(0, 1), a2 + hstepA, PG8_OS(1));
;             PG8_WAIT_V(8); PG8_WAIT_L(0); PG8_BAR; PG8_MMA(0, 0, At, B0); PG8_MMA(0, 1, At, B1); PG8_BAR; PG8_SCHED;
;             PG8_LDA(At, 1, 1); PG8_STAGE(PG8_SB(1, 0), b3, voffB); PG8_STAGE(PG8_SB(1, 1), b3 + hstep, voffB); PG8_STAGE(PG8_SA(1, 0), a3, PG8_OS(0));
;             PG8_WAIT_V(8); PG8_WAIT_L(0); PG8_BAR; PG8_MMA(1, 0, At, B0); PG8_MMA(1, 1, At, B1); PG8_BAR; PG8_SCHED;
	s_add_i32 s24, s58, s38
	v_lshl_add_u64 v[182:183], v[182:183], 0, s[10:11]
	s_mov_b32 m0, s24
	ds_read_b128 v[196:199], v186 offset:49152
	ds_read_b128 v[200:203], v186 offset:50176
	ds_read_b128 v[204:207], v186 offset:51200
	ds_read_b128 v[208:211], v186 offset:52224
	ds_read_b128 v[212:215], v186 offset:53248
	ds_read_b128 v[216:219], v186 offset:54272
	ds_read_b128 v[220:223], v186 offset:55296
	ds_read_b128 v[224:227], v186 offset:56320
	global_load_lds_dwordx4 v[182:183], off
	s_add_i32 m0, s24, 0x2000
	s_add_u32 s22, s22, 0x80080
	v_lshl_add_u64 v[182:183], v[228:229], 0, s[10:11]
	s_addc_u32 s23, s23, 0
	s_add_i32 s24, s59, s38
	global_load_lds_dwordx4 v[182:183], off
	v_lshl_add_u64 v[182:183], s[22:23], 0, v[0:1]
	s_mov_b32 m0, s24
	s_nop 0
	global_load_lds_dwordx4 v[182:183], off
	s_waitcnt vmcnt(5)
	s_waitcnt lgkmcnt(0)
	s_barrier
	s_setprio 1
	s_waitcnt lgkmcnt(0)
	v_mfma_f32_16x16x32_bf16 v[62:65], v[122:125], v[196:199], v[62:65]
	v_mfma_f32_16x16x32_bf16 v[58:61], v[134:137], v[196:199], v[58:61]
	v_mfma_f32_16x16x32_bf16 v[54:57], v[122:125], v[204:207], v[54:57]
	v_mfma_f32_16x16x32_bf16 v[42:45], v[134:137], v[204:207], v[42:45]
	v_mfma_f32_16x16x32_bf16 v[38:41], v[122:125], v[212:215], v[38:41]
	v_mfma_f32_16x16x32_bf16 v[26:29], v[134:137], v[212:215], v[26:29]
	v_mfma_f32_16x16x32_bf16 v[22:25], v[122:125], v[220:223], v[22:25]
	v_mfma_f32_16x16x32_bf16 v[10:13], v[134:137], v[220:223], v[10:13]
	v_lshl_add_u64 v[182:183], s[22:23], 0, v[148:149]
	s_add_i32 m0, s24, 0x2000
	s_nop 0
	global_load_lds_dwordx4 v[182:183], off
	v_mfma_f32_16x16x32_bf16 v[62:65], v[126:129], v[200:203], v[62:65]
	v_mfma_f32_16x16x32_bf16 v[58:61], v[142:145], v[200:203], v[58:61]
	v_mfma_f32_16x16x32_bf16 v[54:57], v[126:129], v[208:211], v[54:57]
	v_mfma_f32_16x16x32_bf16 v[42:45], v[142:145], v[208:211], v[42:45]
	v_mfma_f32_16x16x32_bf16 v[38:41], v[126:129], v[216:219], v[38:41]
	v_mfma_f32_16x16x32_bf16 v[26:29], v[142:145], v[216:219], v[26:29]
	v_mfma_f32_16x16x32_bf16 v[22:25], v[126:129], v[224:227], v[22:25]
	v_mfma_f32_16x16x32_bf16 v[10:13], v[142:145], v[224:227], v[10:13]
	v_lshl_add_u64 v[182:183], v[230:231], 0, s[10:11]
	s_mov_b32 m0, s52
	s_nop 0
	global_load_lds_dwordx4 v[182:183], off
	s_setprio 0
	s_setprio 1
	v_mfma_f32_16x16x32_bf16 v[50:53], v[174:177], v[196:199], v[50:53]
	v_mfma_f32_16x16x32_bf16 v[46:49], v[188:191], v[196:199], v[46:49]
	v_mfma_f32_16x16x32_bf16 v[34:37], v[174:177], v[204:207], v[34:37]
	v_mfma_f32_16x16x32_bf16 v[30:33], v[188:191], v[204:207], v[30:33]
	v_mfma_f32_16x16x32_bf16 v[18:21], v[174:177], v[212:215], v[18:21]
	v_mfma_f32_16x16x32_bf16 v[14:17], v[188:191], v[212:215], v[14:17]
	v_mfma_f32_16x16x32_bf16 v[6:9], v[174:177], v[220:223], v[6:9]
	v_mfma_f32_16x16x32_bf16 v[2:5], v[188:191], v[220:223], v[2:5]
	v_lshl_add_u64 v[182:183], v[232:233], 0, s[10:11]
	s_mov_b32 m0, s53
	s_nop 0
	global_load_lds_dwordx4 v[182:183], off
	v_mfma_f32_16x16x32_bf16 v[50:53], v[178:181], v[200:203], v[50:53]
	v_mfma_f32_16x16x32_bf16 v[46:49], v[192:195], v[200:203], v[46:49]
	v_mfma_f32_16x16x32_bf16 v[34:37], v[178:181], v[208:211], v[34:37]
	v_mfma_f32_16x16x32_bf16 v[30:33], v[192:195], v[208:211], v[30:33]
	v_mfma_f32_16x16x32_bf16 v[18:21], v[178:181], v[216:219], v[18:21]
	v_mfma_f32_16x16x32_bf16 v[14:17], v[192:195], v[216:219], v[14:17]
	v_mfma_f32_16x16x32_bf16 v[6:9], v[178:181], v[224:227], v[6:9]
	v_mfma_f32_16x16x32_bf16 v[2:5], v[192:195], v[224:227], v[2:5]
	s_setprio 0
	s_barrier
	s_add_i32 s57, s57, 2
	s_add_u32 s20, s20, 0x100
	s_addc_u32 s21, s21, 0
	s_add_u32 s55, s55, 0x100
	s_addc_u32 s56, s56, 0
	s_cmp_gt_u32 s57, 29
	s_cbranch_scc0 .LBB0_615
	s_and_b64 vcc, exec, s[4:5]
	s_cbranch_vccz .LBB0_618
	s_barrier

; #define PG8_STAGE(bufoff, gbase, voff) do { _Pragma("unroll") for (int _i = 0; _i < 2; ++_i) \
;         __builtin_amdgcn_global_load_lds((const unsigned*)((const char*)(gbase) + (voff)[_i]), (PG8_LAS unsigned*)(lds + (bufoff) + ldsw + _i * 8192), 16, 0, 0); } while (0)
; #define PG8_WAIT_V(n) asm volatile("s_waitcnt vmcnt(" #n ")" ::: "memory")
; #define PG8_BAR __builtin_amdgcn_s_barrier()
; template <class Epi, class Sched, bool ALIGN_EPI = false, bool SP2 = false, bool GATHER = false>
; __device__ __forceinline__ void gemm_phase(PG8_LAS unsigned char* lds, const Gemm g, const Sched& S, const Epi& E, int tid_in, const int* rowsrc = nullptr, PG8_LAS int* idx_lds = nullptr) {
;     ...
;         for (int t = 0; t < nt; t += 2) {
;             const bool last = (t == nt - 2);
;             if constexpr (GATHER) {
; #pragma unroll
;                 for (int h_ = 0; h_ < 2; ++h_) { gS[h_][0] = last ? gN[h_][0] : gA[h_][0]; gS[h_][1] = last ? gN[h_][1] : gA[h_][1]; } }
;             const char* a1 = cA + (size_t)(t + 1) * kstep;
;             const char* a2 = last ? nA : cA + (size_t)(t + 2) * kstep; const char* b2 = last ? nB : cB + (size_t)(t + 2) * kstep;
;             const char* a3 = a2 + kstep; const char* b3 = b2 + kstep;
;             if (last && has_next) S.a_ready(nxt);
;             if constexpr (SP2) {
;             PG8_LDB(B0, 0, 0); PG8_LDB(B1, 0, 1); PG8_SCHED; PG8_LDA(At, 0, 0); PG8_STAGE(PG8_SA(1, 1), a1 + hstepA, PG8_OA(1));
;             PG8_WAIT_V(8); PG8_WAIT_L(0); PG8_BAR; PG8_MMA(0, 0, At, B0); PG8_MMA(0, 1, At, B1); PG8_BAR; PG8_SCHED;
;             PG8_LDA(At, 0, 1); PG8_STAGE(PG8_SB(0, 0), b2, voffB); PG8_STAGE(PG8_SB(0, 1), b2 + hstep, voffB); PG8_STAGE(PG8_SA(0, 0), a2, PG8_OS(0));
;             PG8_WAIT_V(8); PG8_WAIT_L(0); PG8_BAR; PG8_MMA(1, 0, At, B0); PG8_MMA(1, 1, At, B1); PG8_BAR; PG8_SCHED;
;             PG8_LDB(B0, 1, 0); PG8_LDB(B1, 1, 1); PG8_SCHED; PG8_LDA(At, 1, 0); PG8_STAGE(PG8_SA(0, 1), a2 + hstepA, PG8_OS(1));
;             PG8_WAIT_V(8); PG8_WAIT_L(0); PG8_BAR; PG8_MMA(0, 0, At, B0); PG8_MMA(0, 1, At, B1); PG8_BAR; PG8_SCHED;
;             PG8_LDA(At, 1, 1); PG8_STAGE(PG8_SB(1, 0), b3, voffB); PG8_STAGE(PG8_SB(1, 1), b3 + hstep, voffB); PG8_STAGE(PG8_SA(1, 0), a3, PG8_OS(0));
;             PG8_WAIT_V(8); PG8_WAIT_L(0); PG8_BAR; PG8_MMA(1, 0, At, B0); PG8_MMA(1, 1, At, B1); PG8_BAR; PG8_SCHED;
.LBB0_692:
	s_add_u32 s22, s20, 0xfffc0080
	s_addc_u32 s23, s21, -1
	s_add_i32 s52, 0, 0x10000
	s_cmp_eq_u32 s51, 12
	s_cselect_b32 s25, s15, s23
	s_cselect_b32 s24, s47, s22
	s_cselect_b32 s23, s13, s50
	s_cselect_b32 s22, s48, s49
	s_add_i32 s54, 0, 0x14000
	v_add_u32_e32 v158, s52, v145
	v_add_u32_e32 v174, s54, v145
	ds_read_b128 v[140:143], v158
	ds_read_b128 v[150:153], v158 offset:1024
	ds_read_b128 v[154:157], v158 offset:2048
	ds_read_b128 v[158:161], v158 offset:3072
	ds_read_b128 v[162:165], v174
	ds_read_b128 v[166:169], v174 offset:1024
	ds_read_b128 v[170:173], v174 offset:2048
	ds_read_b128 v[174:177], v174 offset:3072
	v_lshl_add_u64 v[178:179], s[20:21], 0, v[136:137]
	s_add_i32 m0, s31, 0xc000
	ds_read_b128 v[184:187], v149
	ds_read_b128 v[188:191], v149 offset:1024
	ds_read_b128 v[192:195], v149 offset:2048
	ds_read_b128 v[196:199], v149 offset:3072
	ds_read_b128 v[200:203], v149 offset:4096
	ds_read_b128 v[204:207], v149 offset:5120
	ds_read_b128 v[208:211], v149 offset:6144
	ds_read_b128 v[212:215], v149 offset:7168
	global_load_lds_dwordx4 v[178:179], off
	v_lshl_add_u64 v[178:179], s[20:21], 0, v[138:139]
	s_add_i32 m0, s31, 0xe000
	s_nop 0
	global_load_lds_dwordx4 v[178:179], off
	s_waitcnt vmcnt(8)
	s_waitcnt lgkmcnt(0)
	s_barrier
	s_setprio 1
	s_waitcnt lgkmcnt(0)
	v_mfma_f32_16x16x32_bf16 v[126:129], v[140:143], v[184:187], v[126:129]
	v_mfma_f32_16x16x32_bf16 v[122:125], v[154:157], v[184:187], v[122:125]
	v_mfma_f32_16x16x32_bf16 v[118:121], v[140:143], v[192:195], v[118:121]
	v_mfma_f32_16x16x32_bf16 v[110:113], v[154:157], v[192:195], v[110:113]
	v_mfma_f32_16x16x32_bf16 v[102:105], v[140:143], v[200:203], v[102:105]
	v_mfma_f32_16x16x32_bf16 v[94:97], v[154:157], v[200:203], v[94:97]
	v_mfma_f32_16x16x32_bf16 v[86:89], v[140:143], v[208:211], v[86:89]
	v_mfma_f32_16x16x32_bf16 v[78:81], v[154:157], v[208:211], v[78:81]
	v_mfma_f32_16x16x32_bf16 v[126:129], v[150:153], v[188:191], v[126:129]
	v_mfma_f32_16x16x32_bf16 v[122:125], v[158:161], v[188:191], v[122:125]
	v_mfma_f32_16x16x32_bf16 v[118:121], v[150:153], v[196:199], v[118:121]
	v_mfma_f32_16x16x32_bf16 v[110:113], v[158:161], v[196:199], v[110:113]
	v_mfma_f32_16x16x32_bf16 v[102:105], v[150:153], v[204:207], v[102:105]
	v_mfma_f32_16x16x32_bf16 v[94:97], v[158:161], v[204:207], v[94:97]
	v_mfma_f32_16x16x32_bf16 v[86:89], v[150:153], v[212:215], v[86:89]
	v_mfma_f32_16x16x32_bf16 v[78:81], v[158:161], v[212:215], v[78:81]
	s_setprio 0
	s_setprio 1
	v_mfma_f32_16x16x32_bf16 v[114:117], v[162:165], v[184:187], v[114:117]
	v_mfma_f32_16x16x32_bf16 v[106:109], v[170:173], v[184:187], v[106:109]
	v_mfma_f32_16x16x32_bf16 v[98:101], v[162:165], v[192:195], v[98:101]
	v_mfma_f32_16x16x32_bf16 v[90:93], v[170:173], v[192:195], v[90:93]
	v_mfma_f32_16x16x32_bf16 v[82:85], v[162:165], v[200:203], v[82:85]
	v_mfma_f32_16x16x32_bf16 v[74:77], v[170:173], v[200:203], v[74:77]
	v_mfma_f32_16x16x32_bf16 v[70:73], v[162:165], v[208:211], v[70:73]
	v_mfma_f32_16x16x32_bf16 v[66:69], v[170:173], v[208:211], v[66:69]
	v_mfma_f32_16x16x32_bf16 v[114:117], v[166:169], v[188:191], v[114:117]
	v_mfma_f32_16x16x32_bf16 v[106:109], v[174:177], v[188:191], v[106:109]
	v_mfma_f32_16x16x32_bf16 v[98:101], v[166:169], v[196:199], v[98:101]
	v_mfma_f32_16x16x32_bf16 v[90:93], v[174:177], v[196:199], v[90:93]
	v_mfma_f32_16x16x32_bf16 v[82:85], v[166:169], v[204:207], v[82:85]
	v_mfma_f32_16x16x32_bf16 v[74:77], v[174:177], v[204:207], v[74:77]
	v_mfma_f32_16x16x32_bf16 v[70:73], v[166:169], v[212:215], v[70:73]
	v_mfma_f32_16x16x32_bf16 v[66:69], v[174:177], v[212:215], v[66:69]
	s_setprio 0
	s_barrier
	s_add_i32 s52, s52, s30
	v_lshl_add_u64 v[178:179], s[22:23], 0, v[0:1]
	s_mov_b32 m0, s52
	ds_read_b128 v[184:187], v149 offset:16384
	ds_read_b128 v[188:191], v149 offset:17408
	ds_read_b128 v[192:195], v149 offset:18432
	ds_read_b128 v[196:199], v149 offset:19456
	ds_read_b128 v[200:203], v149 offset:20480
	ds_read_b128 v[204:207], v149 offset:21504
	ds_read_b128 v[208:211], v149 offset:22528
	ds_read_b128 v[212:215], v149 offset:23552
	global_load_lds_dwordx4 v[178:179], off
	s_add_i32 m0, s52, 0x2000
	s_add_u32 s52, s22, 0x40000
	v_lshl_add_u64 v[180:181], s[22:23], 0, v[130:131]
	s_addc_u32 s53, s23, 0
	s_add_i32 s54, s54, s30
	global_load_lds_dwordx4 v[180:181], off
	v_lshl_add_u64 v[182:183], s[52:53], 0, v[0:1]
	s_mov_b32 m0, s54
	v_lshl_add_u64 v[216:217], s[24:25], 0, v[132:133]
	global_load_lds_dwordx4 v[182:183], off
	s_waitcnt vmcnt(5)
	s_waitcnt lgkmcnt(0)
	s_barrier
; #define PG8_STAGE(bufoff, gbase, voff) do { _Pragma("unroll") for (int _i = 0; _i < 2; ++_i) \
;         __builtin_amdgcn_global_load_lds((const unsigned*)((const char*)(gbase) + (voff)[_i]), (PG8_LAS unsigned*)(lds + (bufoff) + ldsw + _i * 8192), 16, 0, 0); } while (0)
; #define PG8_WAIT_V(n) asm volatile("s_waitcnt vmcnt(" #n ")" ::: "memory")
; #define PG8_BAR __builtin_amdgcn_s_barrier()
; template <class Epi, class Sched, bool ALIGN_EPI = false, bool SP2 = false, bool GATHER = false>
; __device__ __forceinline__ void gemm_phase(PG8_LAS unsigned char* lds, const Gemm g, const Sched& S, const Epi& E, int tid_in, const int* rowsrc = nullptr, PG8_LAS int* idx_lds = nullptr) {
;     ...
;         for (int t = 0; t < nt; t += 2) {
;             const bool last = (t == nt - 2);
;             if constexpr (GATHER) {
; #pragma unroll
;                 for (int h_ = 0; h_ < 2; ++h_) { gS[h_][0] = last ? gN[h_][0] : gA[h_][0]; gS[h_][1] = last ? gN[h_][1] : gA[h_][1]; } }
;             const char* a1 = cA + (size_t)(t + 1) * kstep;
;             const char* a2 = last ? nA : cA + (size_t)(t + 2) * kstep; const char* b2 = last ? nB : cB + (size_t)(t + 2) * kstep;
;             const char* a3 = a2 + kstep; const char* b3 = b2 + kstep;
;             if (last && has_next) S.a_ready(nxt);
;             if constexpr (SP2) {
;             PG8_LDB(B0, 0, 0); PG8_LDB(B1, 0, 1); PG8_SCHED; PG8_LDA(At, 0, 0); PG8_STAGE(PG8_SA(1, 1), a1 + hstepA, PG8_OA(1));
;             PG8_WAIT_V(8); PG8_WAIT_L(0); PG8_BAR; PG8_MMA(0, 0, At, B0); PG8_MMA(0, 1, At, B1); PG8_BAR; PG8_SCHED;
;             PG8_LDA(At, 0, 1); PG8_STAGE(PG8_SB(0, 0), b2, voffB); PG8_STAGE(PG8_SB(0, 1), b2 + hstep, voffB); PG8_STAGE(PG8_SA(0, 0), a2, PG8_OS(0));
;             PG8_WAIT_V(8); PG8_WAIT_L(0); PG8_BAR; PG8_MMA(1, 0, At, B0); PG8_MMA(1, 1, At, B1); PG8_BAR; PG8_SCHED;
;             PG8_LDB(B0, 1, 0); PG8_LDB(B1, 1, 1); PG8_SCHED; PG8_LDA(At, 1, 0); PG8_STAGE(PG8_SA(0, 1), a2 + hstepA, PG8_OS(1));
;             PG8_WAIT_V(8); PG8_WAIT_L(0); PG8_BAR; PG8_MMA(0, 0, At, B0); PG8_MMA(0, 1, At, B1); PG8_BAR; PG8_SCHED;
;             PG8_LDA(At, 1, 1); PG8_STAGE(PG8_SB(1, 0), b3, voffB); PG8_STAGE(PG8_SB(1, 1), b3 + hstep, voffB); PG8_STAGE(PG8_SA(1, 0), a3, PG8_OS(0));
;             PG8_WAIT_V(8); PG8_WAIT_L(0); PG8_BAR; PG8_MMA(1, 0, At, B0); PG8_MMA(1, 1, At, B1); PG8_BAR; PG8_SCHED;
	s_setprio 1
	s_waitcnt lgkmcnt(0)
	v_mfma_f32_16x16x32_bf16 v[62:65], v[140:143], v[184:187], v[62:65]
	v_mfma_f32_16x16x32_bf16 v[58:61], v[154:157], v[184:187], v[58:61]
	v_mfma_f32_16x16x32_bf16 v[54:57], v[140:143], v[192:195], v[54:57]
	v_mfma_f32_16x16x32_bf16 v[46:49], v[154:157], v[192:195], v[46:49]
	v_mfma_f32_16x16x32_bf16 v[38:41], v[140:143], v[200:203], v[38:41]
	v_mfma_f32_16x16x32_bf16 v[30:33], v[154:157], v[200:203], v[30:33]
	v_mfma_f32_16x16x32_bf16 v[22:25], v[140:143], v[208:211], v[22:25]
	v_mfma_f32_16x16x32_bf16 v[14:17], v[154:157], v[208:211], v[14:17]
	v_lshl_add_u64 v[182:183], s[52:53], 0, v[130:131]
	s_add_i32 m0, s54, 0x2000
	s_nop 0
	global_load_lds_dwordx4 v[182:183], off
	v_mfma_f32_16x16x32_bf16 v[62:65], v[150:153], v[188:191], v[62:65]
	v_mfma_f32_16x16x32_bf16 v[58:61], v[158:161], v[188:191], v[58:61]
	v_mfma_f32_16x16x32_bf16 v[54:57], v[150:153], v[196:199], v[54:57]
	v_mfma_f32_16x16x32_bf16 v[46:49], v[158:161], v[196:199], v[46:49]
	v_mfma_f32_16x16x32_bf16 v[38:41], v[150:153], v[204:207], v[38:41]
	v_mfma_f32_16x16x32_bf16 v[30:33], v[158:161], v[204:207], v[30:33]
	v_mfma_f32_16x16x32_bf16 v[22:25], v[150:153], v[212:215], v[22:25]
	v_mfma_f32_16x16x32_bf16 v[14:17], v[158:161], v[212:215], v[14:17]
	v_lshl_add_u64 v[182:183], s[24:25], 0, v[134:135]
	s_mov_b32 m0, s31
	s_nop 0
	global_load_lds_dwordx4 v[182:183], off
	s_setprio 0
	s_setprio 1
	v_mfma_f32_16x16x32_bf16 v[50:53], v[162:165], v[184:187], v[50:53]
	v_mfma_f32_16x16x32_bf16 v[42:45], v[170:173], v[184:187], v[42:45]
	v_mfma_f32_16x16x32_bf16 v[34:37], v[162:165], v[192:195], v[34:37]
	v_mfma_f32_16x16x32_bf16 v[26:29], v[170:173], v[192:195], v[26:29]
	v_mfma_f32_16x16x32_bf16 v[18:21], v[162:165], v[200:203], v[18:21]
	v_mfma_f32_16x16x32_bf16 v[10:13], v[170:173], v[200:203], v[10:13]
	v_mfma_f32_16x16x32_bf16 v[6:9], v[162:165], v[208:211], v[6:9]
	v_mfma_f32_16x16x32_bf16 v[2:5], v[170:173], v[208:211], v[2:5]
	s_mov_b32 m0, s34
	s_nop 0
	global_load_lds_dwordx4 v[216:217], off
	v_mfma_f32_16x16x32_bf16 v[50:53], v[166:169], v[188:191], v[50:53]
	v_mfma_f32_16x16x32_bf16 v[42:45], v[174:177], v[188:191], v[42:45]
	v_mfma_f32_16x16x32_bf16 v[34:37], v[166:169], v[196:199], v[34:37]
	v_mfma_f32_16x16x32_bf16 v[26:29], v[174:177], v[196:199], v[26:29]
	v_mfma_f32_16x16x32_bf16 v[18:21], v[166:169], v[204:207], v[18:21]
	v_mfma_f32_16x16x32_bf16 v[10:13], v[174:177], v[204:207], v[10:13]
	v_mfma_f32_16x16x32_bf16 v[6:9], v[166:169], v[212:215], v[6:9]
	v_mfma_f32_16x16x32_bf16 v[2:5], v[174:177], v[212:215], v[2:5]
	s_setprio 0
	s_barrier
	s_add_i32 s52, 0, 0x18000
	s_add_i32 s53, 0, 0x1c000
	v_add_u32_e32 v158, s52, v145
	v_add_u32_e32 v174, s53, v145
	ds_read_b128 v[140:143], v158
	ds_read_b128 v[150:153], v158 offset:1024
	ds_read_b128 v[154:157], v158 offset:2048
	ds_read_b128 v[158:161], v158 offset:3072
	ds_read_b128 v[162:165], v174
	ds_read_b128 v[166:169], v174 offset:1024
	ds_read_b128 v[170:173], v174 offset:2048
	ds_read_b128 v[174:177], v174 offset:3072
	s_add_u32 s24, s24, 0x40000
	s_addc_u32 s25, s25, 0
	s_mov_b32 m0, s35
	v_lshl_add_u64 v[218:219], s[24:25], 0, v[134:135]
	ds_read_b128 v[184:187], v149 offset:32768
	ds_read_b128 v[188:191], v149 offset:33792
	ds_read_b128 v[192:195], v149 offset:34816
	ds_read_b128 v[196:199], v149 offset:35840
	ds_read_b128 v[200:203], v149 offset:36864
	ds_read_b128 v[204:207], v149 offset:37888
	ds_read_b128 v[208:211], v149 offset:38912
	ds_read_b128 v[212:215], v149 offset:39936
	global_load_lds_dwordx4 v[218:219], off
	v_lshl_add_u64 v[218:219], s[24:25], 0, v[132:133]
	s_mov_b32 m0, s36
	s_nop 0
	global_load_lds_dwordx4 v[218:219], off
	s_waitcnt vmcnt(8)
	s_waitcnt lgkmcnt(0)
	s_barrier
	s_setprio 1
	s_waitcnt lgkmcnt(0)
	v_mfma_f32_16x16x32_bf16 v[126:129], v[140:143], v[184:187], v[126:129]
	v_mfma_f32_16x16x32_bf16 v[122:125], v[154:157], v[184:187], v[122:125]
	v_mfma_f32_16x16x32_bf16 v[118:121], v[140:143], v[192:195], v[118:121]
	v_mfma_f32_16x16x32_bf16 v[110:113], v[154:157], v[192:195], v[110:113]
	v_mfma_f32_16x16x32_bf16 v[102:105], v[140:143], v[200:203], v[102:105]
	v_mfma_f32_16x16x32_bf16 v[94:97], v[154:157], v[200:203], v[94:97]
	v_mfma_f32_16x16x32_bf16 v[86:89], v[140:143], v[208:211], v[86:89]
	v_mfma_f32_16x16x32_bf16 v[78:81], v[154:157], v[208:211], v[78:81]
	v_mfma_f32_16x16x32_bf16 v[126:129], v[150:153], v[188:191], v[126:129]
	v_mfma_f32_16x16x32_bf16 v[122:125], v[158:161], v[188:191], v[122:125]
	v_mfma_f32_16x16x32_bf16 v[118:121], v[150:153], v[196:199], v[118:121]
	v_mfma_f32_16x16x32_bf16 v[110:113], v[158:161], v[196:199], v[110:113]
	v_mfma_f32_16x16x32_bf16 v[102:105], v[150:153], v[204:207], v[102:105]
	v_mfma_f32_16x16x32_bf16 v[94:97], v[158:161], v[204:207], v[94:97]
	v_mfma_f32_16x16x32_bf16 v[86:89], v[150:153], v[212:215], v[86:89]
	v_mfma_f32_16x16x32_bf16 v[78:81], v[158:161], v[212:215], v[78:81]
	s_setprio 0
	s_setprio 1
	v_mfma_f32_16x16x32_bf16 v[114:117], v[162:165], v[184:187], v[114:117]
	v_mfma_f32_16x16x32_bf16 v[106:109], v[170:173], v[184:187], v[106:109]
	v_mfma_f32_16x16x32_bf16 v[98:101], v[162:165], v[192:195], v[98:101]
	v_mfma_f32_16x16x32_bf16 v[90:93], v[170:173], v[192:195], v[90:93]
	v_mfma_f32_16x16x32_bf16 v[82:85], v[162:165], v[200:203], v[82:85]
	v_mfma_f32_16x16x32_bf16 v[74:77], v[170:173], v[200:203], v[74:77]
	v_mfma_f32_16x16x32_bf16 v[70:73], v[162:165], v[208:211], v[70:73]
	v_mfma_f32_16x16x32_bf16 v[66:69], v[170:173], v[208:211], v[66:69]
	v_mfma_f32_16x16x32_bf16 v[114:117], v[166:169], v[188:191], v[114:117]
	v_mfma_f32_16x16x32_bf16 v[106:109], v[174:177], v[188:191], v[106:109]
	v_mfma_f32_16x16x32_bf16 v[98:101], v[166:169], v[196:199], v[98:101]
	v_mfma_f32_16x16x32_bf16 v[90:93], v[174:177], v[196:199], v[90:93]
	v_mfma_f32_16x16x32_bf16 v[82:85], v[166:169], v[204:207], v[82:85]
	v_mfma_f32_16x16x32_bf16 v[74:77], v[174:177], v[204:207], v[74:77]
	v_mfma_f32_16x16x32_bf16 v[70:73], v[166:169], v[212:215], v[70:73]
	v_mfma_f32_16x16x32_bf16 v[66:69], v[174:177], v[212:215], v[66:69]
	s_setprio 0
	s_barrier
; #define PG8_STAGE(bufoff, gbase, voff) do { _Pragma("unroll") for (int _i = 0; _i < 2; ++_i) \
;         __builtin_amdgcn_global_load_lds((const unsigned*)((const char*)(gbase) + (voff)[_i]), (PG8_LAS unsigned*)(lds + (bufoff) + ldsw + _i * 8192), 16, 0, 0); } while (0)
; #define PG8_WAIT_V(n) asm volatile("s_waitcnt vmcnt(" #n ")" ::: "memory")
; #define PG8_BAR __builtin_amdgcn_s_barrier()
; template <class Epi, class Sched, bool ALIGN_EPI = false, bool SP2 = false, bool GATHER = false>
; __device__ __forceinline__ void gemm_phase(PG8_LAS unsigned char* lds, const Gemm g, const Sched& S, const Epi& E, int tid_in, const int* rowsrc = nullptr, PG8_LAS int* idx_lds = nullptr) {
;     ...
;         for (int t = 0; t < nt; t += 2) {
;             const bool last = (t == nt - 2);
;             if constexpr (GATHER) {
; #pragma unroll
;                 for (int h_ = 0; h_ < 2; ++h_) { gS[h_][0] = last ? gN[h_][0] : gA[h_][0]; gS[h_][1] = last ? gN[h_][1] : gA[h_][1]; } }
;             const char* a1 = cA + (size_t)(t + 1) * kstep;
;             const char* a2 = last ? nA : cA + (size_t)(t + 2) * kstep; const char* b2 = last ? nB : cB + (size_t)(t + 2) * kstep;
;             const char* a3 = a2 + kstep; const char* b3 = b2 + kstep;
;             if (last && has_next) S.a_ready(nxt);
;             if constexpr (SP2) {
;             PG8_LDB(B0, 0, 0); PG8_LDB(B1, 0, 1); PG8_SCHED; PG8_LDA(At, 0, 0); PG8_STAGE(PG8_SA(1, 1), a1 + hstepA, PG8_OA(1));
;             PG8_WAIT_V(8); PG8_WAIT_L(0); PG8_BAR; PG8_MMA(0, 0, At, B0); PG8_MMA(0, 1, At, B1); PG8_BAR; PG8_SCHED;
;             PG8_LDA(At, 0, 1); PG8_STAGE(PG8_SB(0, 0), b2, voffB); PG8_STAGE(PG8_SB(0, 1), b2 + hstep, voffB); PG8_STAGE(PG8_SA(0, 0), a2, PG8_OS(0));
;             PG8_WAIT_V(8); PG8_WAIT_L(0); PG8_BAR; PG8_MMA(1, 0, At, B0); PG8_MMA(1, 1, At, B1); PG8_BAR; PG8_SCHED;
;             PG8_LDB(B0, 1, 0); PG8_LDB(B1, 1, 1); PG8_SCHED; PG8_LDA(At, 1, 0); PG8_STAGE(PG8_SA(0, 1), a2 + hstepA, PG8_OS(1));
;             PG8_WAIT_V(8); PG8_WAIT_L(0); PG8_BAR; PG8_MMA(0, 0, At, B0); PG8_MMA(0, 1, At, B1); PG8_BAR; PG8_SCHED;
;             PG8_LDA(At, 1, 1); PG8_STAGE(PG8_SB(1, 0), b3, voffB); PG8_STAGE(PG8_SB(1, 1), b3 + hstep, voffB); PG8_STAGE(PG8_SA(1, 0), a3, PG8_OS(0));
;             PG8_WAIT_V(8); PG8_WAIT_L(0); PG8_BAR; PG8_MMA(1, 0, At, B0); PG8_MMA(1, 1, At, B1); PG8_BAR; PG8_SCHED;
	s_add_i32 s24, s52, s30
	v_lshl_add_u64 v[178:179], v[178:179], 0, s[10:11]
	s_mov_b32 m0, s24
	ds_read_b128 v[184:187], v149 offset:49152
	ds_read_b128 v[188:191], v149 offset:50176
	ds_read_b128 v[192:195], v149 offset:51200
	ds_read_b128 v[196:199], v149 offset:52224
	ds_read_b128 v[200:203], v149 offset:53248
	ds_read_b128 v[204:207], v149 offset:54272
	ds_read_b128 v[208:211], v149 offset:55296
	ds_read_b128 v[212:215], v149 offset:56320
	global_load_lds_dwordx4 v[178:179], off
	s_add_i32 m0, s24, 0x2000
	s_add_u32 s22, s22, 0x40080
	v_lshl_add_u64 v[178:179], v[180:181], 0, s[10:11]
	s_addc_u32 s23, s23, 0
	s_add_i32 s24, s53, s30
	global_load_lds_dwordx4 v[178:179], off
	v_lshl_add_u64 v[178:179], s[22:23], 0, v[0:1]
	s_mov_b32 m0, s24
	s_nop 0
	global_load_lds_dwordx4 v[178:179], off
	s_waitcnt vmcnt(5)
	s_waitcnt lgkmcnt(0)
	s_barrier
	s_setprio 1
	s_waitcnt lgkmcnt(0)
	v_mfma_f32_16x16x32_bf16 v[62:65], v[140:143], v[184:187], v[62:65]
	v_mfma_f32_16x16x32_bf16 v[58:61], v[154:157], v[184:187], v[58:61]
	v_mfma_f32_16x16x32_bf16 v[54:57], v[140:143], v[192:195], v[54:57]
	v_mfma_f32_16x16x32_bf16 v[46:49], v[154:157], v[192:195], v[46:49]
	v_mfma_f32_16x16x32_bf16 v[38:41], v[140:143], v[200:203], v[38:41]
	v_mfma_f32_16x16x32_bf16 v[30:33], v[154:157], v[200:203], v[30:33]
	v_mfma_f32_16x16x32_bf16 v[22:25], v[140:143], v[208:211], v[22:25]
	v_mfma_f32_16x16x32_bf16 v[14:17], v[154:157], v[208:211], v[14:17]
	v_lshl_add_u64 v[178:179], s[22:23], 0, v[130:131]
	s_add_i32 m0, s24, 0x2000
	s_nop 0
	global_load_lds_dwordx4 v[178:179], off
	v_mfma_f32_16x16x32_bf16 v[62:65], v[150:153], v[188:191], v[62:65]
	v_mfma_f32_16x16x32_bf16 v[58:61], v[158:161], v[188:191], v[58:61]
	v_mfma_f32_16x16x32_bf16 v[54:57], v[150:153], v[196:199], v[54:57]
	v_mfma_f32_16x16x32_bf16 v[46:49], v[158:161], v[196:199], v[46:49]
	v_mfma_f32_16x16x32_bf16 v[38:41], v[150:153], v[204:207], v[38:41]
	v_mfma_f32_16x16x32_bf16 v[30:33], v[158:161], v[204:207], v[30:33]
	v_mfma_f32_16x16x32_bf16 v[22:25], v[150:153], v[212:215], v[22:25]
	v_mfma_f32_16x16x32_bf16 v[14:17], v[158:161], v[212:215], v[14:17]
	v_lshl_add_u64 v[178:179], v[182:183], 0, s[10:11]
	s_mov_b32 m0, s38
	s_nop 0
	global_load_lds_dwordx4 v[178:179], off
	s_setprio 0
	s_setprio 1
	v_mfma_f32_16x16x32_bf16 v[50:53], v[162:165], v[184:187], v[50:53]
	v_mfma_f32_16x16x32_bf16 v[42:45], v[170:173], v[184:187], v[42:45]
	v_mfma_f32_16x16x32_bf16 v[34:37], v[162:165], v[192:195], v[34:37]
	v_mfma_f32_16x16x32_bf16 v[26:29], v[170:173], v[192:195], v[26:29]
	v_mfma_f32_16x16x32_bf16 v[18:21], v[162:165], v[200:203], v[18:21]
	v_mfma_f32_16x16x32_bf16 v[10:13], v[170:173], v[200:203], v[10:13]
	v_mfma_f32_16x16x32_bf16 v[6:9], v[162:165], v[208:211], v[6:9]
	v_mfma_f32_16x16x32_bf16 v[2:5], v[170:173], v[208:211], v[2:5]
	v_lshl_add_u64 v[178:179], v[216:217], 0, s[10:11]
	s_mov_b32 m0, s39
	s_nop 0
	global_load_lds_dwordx4 v[178:179], off
	v_mfma_f32_16x16x32_bf16 v[50:53], v[166:169], v[188:191], v[50:53]
	v_mfma_f32_16x16x32_bf16 v[42:45], v[174:177], v[188:191], v[42:45]
	v_mfma_f32_16x16x32_bf16 v[34:37], v[166:169], v[196:199], v[34:37]
	v_mfma_f32_16x16x32_bf16 v[26:29], v[174:177], v[196:199], v[26:29]
	v_mfma_f32_16x16x32_bf16 v[18:21], v[166:169], v[204:207], v[18:21]
	v_mfma_f32_16x16x32_bf16 v[10:13], v[174:177], v[204:207], v[10:13]
	v_mfma_f32_16x16x32_bf16 v[6:9], v[166:169], v[212:215], v[6:9]
	v_mfma_f32_16x16x32_bf16 v[2:5], v[174:177], v[212:215], v[2:5]
	s_setprio 0
	s_barrier
	s_add_i32 s51, s51, 2
	s_add_u32 s20, s20, 0x100
	s_addc_u32 s21, s21, 0
	s_add_u32 s49, s49, 0x100
	s_addc_u32 s50, s50, 0
	s_cmp_gt_u32 s51, 13
	s_cbranch_scc0 .LBB0_692
	s_and_b64 vcc, exec, s[8:9]
	s_cbranch_vccz .LBB0_695
	s_barrier

; __device__ __forceinline__ void finishSM(f32x16& p0, f32x16& p1, float& l_reg, bf16x8& pa0, bf16x8& pa1, bf16x8& pa2, bf16x8& pa3) {
; #pragma unroll
;   for (int r = 0; r < 16; ++r) p1[r] = __builtin_amdgcn_exp2f(p1[r]);
;   float ps = 0;
; #pragma unroll
;   for (int r = 0; r < 16; ++r) ps += p0[r];
; #pragma unroll
;   for (int r = 0; r < 16; ++r) ps += p1[r];
;   l_reg += ps;
;     ...
;   ATT_PK4(p0, 0, pa0); ATT_PK4(p0, 8, pa1); ATT_PK4(p1, 0, pa2); ATT_PK4(p1, 8, pa3);
;     ...
; }
; template <int DK>
; __device__ __forceinline__ void qkt(f32x16& p0, f32x16& p1, const char* Ks, const bf16x8* qr, int r32, int hi) {
;   p0 = f32x16{}; p1 = f32x16{};
; #pragma unroll
;   for (int d0 = 0; d0 < DK / 16; ++d0) { const int cb = (d0 * 16 + hi * 8) * 2;
;     const bf16x8 b0 = *reinterpret_cast<const bf16x8*>(Ks + ATT_KSWZ(r32, cb));
;     const bf16x8 b1 = *reinterpret_cast<const bf16x8*>(Ks + ATT_KSWZ(32 + r32, cb));
;     p0 = __builtin_amdgcn_mfma_f32_32x32x16_bf16(b0, qr[d0], p0, 0, 0, 0);
;     p1 = __builtin_amdgcn_mfma_f32_32x32x16_bf16(b1, qr[d0], p1, 0, 0, 0);
;   }
; }
; template <int N> __device__ __forceinline__ void lgkm_wait8(s16x4* v) { asm volatile("s_waitcnt lgkmcnt(%8)" : "+v"(v[0]), "+v"(v[1]), "+v"(v[2]), "+v"(v[3]), "+v"(v[4]), "+v"(v[5]), "+v"(v[6]), "+v"(v[7]) : "n"(N) : "memory"); }
; template <int DV, int GRP> __device__ __forceinline__ void v_group_read(s16x4* vf, int vb) {
;   sfor<0, 8>([&](auto ic) { constexpr int j = decltype(ic)::value; vf[j] = tr_read<v_rd_off<DV>(GRP, j / 2, j % 2)>(vb); });
; }
; __device__ __forceinline__ void pv_group(f32x16& od, const s16x4* vf, bf16x8 pa0, bf16x8 pa1, bf16x8 pa2, bf16x8 pa3) {
;     ...
;   od = __builtin_amdgcn_mfma_f32_32x32x16_bf16(pa0, ATT_PK(vf[0], vf[1]), od, 0, 0, 0);
;   od = __builtin_amdgcn_mfma_f32_32x32x16_bf16(pa1, ATT_PK(vf[2], vf[3]), od, 0, 0, 0);
;   od = __builtin_amdgcn_mfma_f32_32x32x16_bf16(pa2, ATT_PK(vf[4], vf[5]), od, 0, 0, 0);
;   od = __builtin_amdgcn_mfma_f32_32x32x16_bf16(pa3, ATT_PK(vf[6], vf[7]), od, 0, 0, 0);
;     ...
; }
; template <int DV> __device__ __forceinline__ void pv_all_pipe(f32x16* o, int vb, bf16x8 pa0, bf16x8 pa1, bf16x8 pa2, bf16x8 pa3) {
;   s16x4 va[8], vc[8];
;   v_group_read<DV, 0>(va, vb); v_group_read<DV, 1>(vc, vb);
;   lgkm_wait8<8>(va); pv_group(o[0], va, pa0, pa1, pa2, pa3);
;   if constexpr (DV == 128) {
;     s16x4 vd[8], ve[8];
;     v_group_read<DV, 2>(vd, vb);
.LBB0_856:
	s_add_i32 s30, 0, 0x14000
	v_add_u32_e32 v86, s30, v161
	ds_read_b128 v[82:85], v86
	ds_read_b128 v[86:89], v86 offset:8192
	v_add_u32_e32 v134, s30, v163
	ds_read_b128 v[130:133], v134
	ds_read_b128 v[134:137], v134 offset:8192
	v_exp_f32_e32 v66, v66
	v_add_f32_e32 v180, 0, v173
	v_add_f32_e32 v180, v174, v180
	v_add_f32_e32 v180, v175, v180
	v_add_f32_e32 v180, v184, v180
	v_add_f32_e32 v180, v185, v180
	v_add_f32_e32 v180, v186, v180
	v_add_f32_e32 v180, v187, v180
	v_add_f32_e32 v180, v188, v180
	v_add_f32_e32 v180, v189, v180
	v_add_f32_e32 v180, v190, v180
	v_add_f32_e32 v180, v191, v180
	v_add_f32_e32 v180, v192, v180
	v_add_f32_e32 v180, v193, v180
	v_add_f32_e32 v180, v194, v180
	v_add_f32_e32 v180, v195, v180
	v_add_f32_e32 v180, v196, v180
	s_waitcnt lgkmcnt(0)
	v_mfma_f32_32x32x16_bf16 v[98:113], v[82:85], v[114:117], 0
	v_exp_f32_e32 v67, v67
	v_exp_f32_e32 v68, v68
	v_exp_f32_e32 v69, v69
	v_exp_f32_e32 v70, v70
	v_exp_f32_e32 v71, v71
	v_exp_f32_e32 v72, v72
	v_exp_f32_e32 v73, v73
	v_mfma_f32_32x32x16_bf16 v[82:97], v[86:89], v[114:117], 0
	v_exp_f32_e32 v74, v74
	v_exp_f32_e32 v75, v75
	v_exp_f32_e32 v76, v76
	v_exp_f32_e32 v77, v77
	v_exp_f32_e32 v78, v78
	v_exp_f32_e32 v79, v79
	v_exp_f32_e32 v80, v80
	v_mfma_f32_32x32x16_bf16 v[98:113], v[130:133], v[118:121], v[98:113]
	v_exp_f32_e32 v81, v81
	s_andn2_b64 vcc, exec, s[26:27]
	v_mfma_f32_32x32x16_bf16 v[82:97], v[134:137], v[118:121], v[82:97]
	v_add_u32_e32 v134, s30, v165
	ds_read_b128 v[130:133], v134
	ds_read_b128 v[134:137], v134 offset:8192
	v_add_f32_e32 v180, v66, v180
	v_add_f32_e32 v180, v67, v180
	v_add_f32_e32 v180, v68, v180
	v_add_f32_e32 v180, v69, v180
	v_add_f32_e32 v180, v70, v180
	v_add_f32_e32 v180, v71, v180
	v_add_f32_e32 v180, v72, v180
	v_add_f32_e32 v180, v73, v180
	s_waitcnt lgkmcnt(0)
	v_mfma_f32_32x32x16_bf16 v[98:113], v[130:133], v[122:125], v[98:113]
	v_mfma_f32_32x32x16_bf16 v[82:97], v[134:137], v[122:125], v[82:97]
	v_add_u32_e32 v134, s30, v167
	ds_read_b128 v[130:133], v134
	ds_read_b128 v[134:137], v134 offset:8192
	v_add_f32_e32 v180, v74, v180
	v_add_f32_e32 v180, v75, v180
	v_add_f32_e32 v180, v76, v180
	v_add_f32_e32 v180, v77, v180
	v_add_f32_e32 v180, v78, v180
	v_add_f32_e32 v180, v79, v180
	v_add_f32_e32 v180, v80, v180
	v_add_f32_e32 v180, v81, v180
	s_waitcnt lgkmcnt(0)
	v_mfma_f32_32x32x16_bf16 v[98:113], v[130:133], v[126:129], v[98:113]
	v_mfma_f32_32x32x16_bf16 v[82:97], v[134:137], v[126:129], v[82:97]
	v_add_f32_e32 v172, v172, v180
	v_cvt_pk_bf16_f32 v130, v173, v174
	v_cvt_pk_bf16_f32 v131, v175, v184
	v_cvt_pk_bf16_f32 v132, v185, v186
	v_cvt_pk_bf16_f32 v133, v187, v188
	v_cvt_pk_bf16_f32 v134, v189, v190
	v_cvt_pk_bf16_f32 v135, v191, v192
	v_cvt_pk_bf16_f32 v136, v193, v194
	v_cvt_pk_bf16_f32 v137, v195, v196
	v_cvt_pk_bf16_f32 v138, v66, v67
	v_cvt_pk_bf16_f32 v139, v68, v69
	v_cvt_pk_bf16_f32 v140, v70, v71
	v_cvt_pk_bf16_f32 v141, v72, v73
	v_cvt_pk_bf16_f32 v142, v74, v75
	v_cvt_pk_bf16_f32 v143, v76, v77
	v_cvt_pk_bf16_f32 v144, v78, v79
	v_cvt_pk_bf16_f32 v145, v80, v81
	ds_read_b64_tr_b16 v[176:177], v169 offset:0
	ds_read_b64_tr_b16 v[178:179], v169 offset:0x800
	ds_read_b64_tr_b16 v[198:199], v169 offset:0x1000
	ds_read_b64_tr_b16 v[200:201], v169 offset:0x1800
	ds_read_b64_tr_b16 v[202:203], v169 offset:0x2000
	ds_read_b64_tr_b16 v[204:205], v169 offset:0x2800
	ds_read_b64_tr_b16 v[206:207], v169 offset:0x3000
	ds_read_b64_tr_b16 v[208:209], v169 offset:0x3800
	ds_read_b64_tr_b16 v[210:211], v169 offset:0x200
	ds_read_b64_tr_b16 v[212:213], v169 offset:0xa00
	ds_read_b64_tr_b16 v[214:215], v169 offset:0x1200
	s_nop 0
	v_permlane32_swap_b32_e32 v130, v132
	v_permlane32_swap_b32_e32 v131, v133
	ds_read_b64_tr_b16 v[216:217], v169 offset:0x1a00
	ds_read_b64_tr_b16 v[218:219], v169 offset:0x2200
	ds_read_b64_tr_b16 v[220:221], v169 offset:0x2a00
	ds_read_b64_tr_b16 v[222:223], v169 offset:0x3200
	ds_read_b64_tr_b16 v[224:225], v169 offset:0x3a00
	s_waitcnt lgkmcnt(8)
	v_permlane32_swap_b32_e32 v134, v136
	s_nop 0
	v_mfma_f32_32x32x16_bf16 v[2:17], v[130:133], v[176:179], v[2:17]
	v_permlane32_swap_b32_e32 v135, v137
	v_permlane32_swap_b32_e32 v138, v140
	v_permlane32_swap_b32_e32 v139, v141
	ds_read_b64_tr_b16 v[176:177], v169 offset:0x400
	v_mfma_f32_32x32x16_bf16 v[2:17], v[134:137], v[198:201], v[2:17]
	v_permlane32_swap_b32_e32 v142, v144
	v_permlane32_swap_b32_e32 v143, v145
	ds_read_b64_tr_b16 v[178:179], v169 offset:0xc00
	ds_read_b64_tr_b16 v[198:199], v169 offset:0x1400
	ds_read_b64_tr_b16 v[200:201], v169 offset:0x1c00
	v_mfma_f32_32x32x16_bf16 v[2:17], v[138:141], v[202:205], v[2:17]
	ds_read_b64_tr_b16 v[202:203], v169 offset:0x2400
	ds_read_b64_tr_b16 v[204:205], v169 offset:0x2c00
	v_exp_f32_e32 v197, v98
	v_mfma_f32_32x32x16_bf16 v[2:17], v[142:145], v[206:209], v[2:17]
	ds_read_b64_tr_b16 v[206:207], v169 offset:0x3400
	ds_read_b64_tr_b16 v[208:209], v169 offset:0x3c00
	s_waitcnt lgkmcnt(8)
	s_nop 0
	v_mfma_f32_32x32x16_bf16 v[50:65], v[130:133], v[210:213], v[50:65]
	ds_read_b64_tr_b16 v[210:211], v169 offset:0x600
	ds_read_b64_tr_b16 v[212:213], v169 offset:0xe00
	v_mfma_f32_32x32x16_bf16 v[50:65], v[134:137], v[214:217], v[50:65]
	ds_read_b64_tr_b16 v[214:215], v169 offset:0x1600
	ds_read_b64_tr_b16 v[216:217], v169 offset:0x1e00
	v_mfma_f32_32x32x16_bf16 v[50:65], v[138:141], v[218:221], v[50:65]
	ds_read_b64_tr_b16 v[218:219], v169 offset:0x2600
	ds_read_b64_tr_b16 v[220:221], v169 offset:0x2e00
	v_mfma_f32_32x32x16_bf16 v[50:65], v[142:145], v[222:225], v[50:65]
	ds_read_b64_tr_b16 v[222:223], v169 offset:0x3600
	ds_read_b64_tr_b16 v[224:225], v169 offset:0x3e00
	s_waitcnt lgkmcnt(8)
	s_nop 0
	s_waitcnt lgkmcnt(0)
	v_mfma_f32_32x32x16_bf16 v[34:49], v[130:133], v[176:179], v[34:49]
	v_mfma_f32_32x32x16_bf16 v[18:33], v[130:133], v[210:213], v[18:33]
	v_exp_f32_e32 v210, v105
	v_exp_f32_e32 v211, v111
	v_exp_f32_e32 v212, v113
	v_mfma_f32_32x32x16_bf16 v[34:49], v[134:137], v[198:201], v[34:49]
	v_exp_f32_e32 v200, v99
	v_exp_f32_e32 v198, v100
	v_exp_f32_e32 v199, v106
	v_exp_f32_e32 v201, v108
	v_mfma_f32_32x32x16_bf16 v[18:33], v[134:137], v[214:217], v[18:33]
	v_mfma_f32_32x32x16_bf16 v[34:49], v[138:141], v[202:205], v[34:49]
	v_exp_f32_e32 v202, v101
	v_exp_f32_e32 v204, v102
	v_exp_f32_e32 v205, v104
	v_exp_f32_e32 v203, v107
	v_mfma_f32_32x32x16_bf16 v[18:33], v[138:141], v[218:221], v[18:33]
	v_mfma_f32_32x32x16_bf16 v[34:49], v[142:145], v[206:209], v[34:49]
	v_exp_f32_e32 v207, v103
	v_exp_f32_e32 v209, v109
	v_exp_f32_e32 v206, v110
	v_exp_f32_e32 v208, v112
	v_mfma_f32_32x32x16_bf16 v[18:33], v[142:145], v[222:225], v[18:33]
	s_cbranch_vccnz .LBB0_865
	s_andn2_b64 vcc, exec, s[28:29]
	s_mov_b64 s[26:27], -1
	s_cbranch_vccnz .LBB0_859
	s_waitcnt vmcnt(0)
	s_mov_b64 s[26:27], 0

; __device__ __forceinline__ void finishSM(f32x16& p0, f32x16& p1, float& l_reg, bf16x8& pa0, bf16x8& pa1, bf16x8& pa2, bf16x8& pa3) {
; #pragma unroll
;   for (int r = 0; r < 16; ++r) p1[r] = __builtin_amdgcn_exp2f(p1[r]);
;   float ps = 0;
; #pragma unroll
;   for (int r = 0; r < 16; ++r) ps += p0[r];
; #pragma unroll
;   for (int r = 0; r < 16; ++r) ps += p1[r];
;   l_reg += ps;
;     ...
;   ATT_PK4(p0, 0, pa0); ATT_PK4(p0, 8, pa1); ATT_PK4(p1, 0, pa2); ATT_PK4(p1, 8, pa3);
;     ...
; }
; template <int DK>
; __device__ __forceinline__ void qkt(f32x16& p0, f32x16& p1, const char* Ks, const bf16x8* qr, int r32, int hi) {
;   p0 = f32x16{}; p1 = f32x16{};
; #pragma unroll
;   for (int d0 = 0; d0 < DK / 16; ++d0) { const int cb = (d0 * 16 + hi * 8) * 2;
;     const bf16x8 b0 = *reinterpret_cast<const bf16x8*>(Ks + ATT_KSWZ(r32, cb));
;     const bf16x8 b1 = *reinterpret_cast<const bf16x8*>(Ks + ATT_KSWZ(32 + r32, cb));
;     p0 = __builtin_amdgcn_mfma_f32_32x32x16_bf16(b0, qr[d0], p0, 0, 0, 0);
;     p1 = __builtin_amdgcn_mfma_f32_32x32x16_bf16(b1, qr[d0], p1, 0, 0, 0);
;   }
; }
; template <int N> __device__ __forceinline__ void lgkm_wait8(s16x4* v) { asm volatile("s_waitcnt lgkmcnt(%8)" : "+v"(v[0]), "+v"(v[1]), "+v"(v[2]), "+v"(v[3]), "+v"(v[4]), "+v"(v[5]), "+v"(v[6]), "+v"(v[7]) : "n"(N) : "memory"); }
; template <int DV, int GRP> __device__ __forceinline__ void v_group_read(s16x4* vf, int vb) {
;   sfor<0, 8>([&](auto ic) { constexpr int j = decltype(ic)::value; vf[j] = tr_read<v_rd_off<DV>(GRP, j / 2, j % 2)>(vb); });
; }
; __device__ __forceinline__ void pv_group(f32x16& od, const s16x4* vf, bf16x8 pa0, bf16x8 pa1, bf16x8 pa2, bf16x8 pa3) {
;     ...
;   od = __builtin_amdgcn_mfma_f32_32x32x16_bf16(pa0, ATT_PK(vf[0], vf[1]), od, 0, 0, 0);
;   od = __builtin_amdgcn_mfma_f32_32x32x16_bf16(pa1, ATT_PK(vf[2], vf[3]), od, 0, 0, 0);
;   od = __builtin_amdgcn_mfma_f32_32x32x16_bf16(pa2, ATT_PK(vf[4], vf[5]), od, 0, 0, 0);
;   od = __builtin_amdgcn_mfma_f32_32x32x16_bf16(pa3, ATT_PK(vf[6], vf[7]), od, 0, 0, 0);
;     ...
; }
; template <int DV> __device__ __forceinline__ void pv_all_pipe(f32x16* o, int vb, bf16x8 pa0, bf16x8 pa1, bf16x8 pa2, bf16x8 pa3) {
;   s16x4 va[8], vc[8];
;   v_group_read<DV, 0>(va, vb); v_group_read<DV, 1>(vc, vb);
;   lgkm_wait8<8>(va); pv_group(o[0], va, pa0, pa1, pa2, pa3);
;   if constexpr (DV == 128) {
;     s16x4 vd[8], ve[8];
;     v_group_read<DV, 2>(vd, vb);
.LBB0_863:
	s_add_i32 s26, 0, 0x18000
	v_add_u32_e32 v70, s26, v161
	ds_read_b128 v[66:69], v70
	ds_read_b128 v[70:73], v70 offset:8192
	v_add_u32_e32 v134, s26, v163
	ds_read_b128 v[130:133], v134
	ds_read_b128 v[134:137], v134 offset:8192
	v_exp_f32_e32 v82, v82
	v_add_f32_e32 v180, 0, v197
	v_add_f32_e32 v180, v200, v180
	v_add_f32_e32 v180, v198, v180
	v_add_f32_e32 v180, v202, v180
	v_add_f32_e32 v180, v204, v180
	v_add_f32_e32 v180, v207, v180
	v_add_f32_e32 v180, v205, v180
	v_add_f32_e32 v180, v210, v180
	v_add_f32_e32 v180, v199, v180
	v_add_f32_e32 v180, v203, v180
	v_add_f32_e32 v180, v201, v180
	v_add_f32_e32 v180, v209, v180
	v_add_f32_e32 v180, v206, v180
	v_add_f32_e32 v180, v211, v180
	v_add_f32_e32 v180, v208, v180
	v_add_f32_e32 v180, v212, v180
	s_waitcnt lgkmcnt(0)
	v_mfma_f32_32x32x16_bf16 v[98:113], v[66:69], v[114:117], 0
	v_exp_f32_e32 v83, v83
	v_exp_f32_e32 v84, v84
	v_exp_f32_e32 v85, v85
	v_exp_f32_e32 v86, v86
	v_exp_f32_e32 v87, v87
	v_exp_f32_e32 v88, v88
	v_exp_f32_e32 v89, v89
	v_mfma_f32_32x32x16_bf16 v[66:81], v[70:73], v[114:117], 0
	v_exp_f32_e32 v90, v90
	v_exp_f32_e32 v91, v91
	v_exp_f32_e32 v92, v92
	v_exp_f32_e32 v93, v93
	v_exp_f32_e32 v94, v94
	v_exp_f32_e32 v95, v95
	v_exp_f32_e32 v96, v96
	v_mfma_f32_32x32x16_bf16 v[98:113], v[130:133], v[118:121], v[98:113]
	v_exp_f32_e32 v97, v97
	v_mfma_f32_32x32x16_bf16 v[66:81], v[134:137], v[118:121], v[66:81]
	v_add_u32_e32 v134, s26, v165
	ds_read_b128 v[130:133], v134
	ds_read_b128 v[134:137], v134 offset:8192
	v_add_f32_e32 v180, v82, v180
	v_add_f32_e32 v180, v83, v180
	v_add_f32_e32 v180, v84, v180
	v_add_f32_e32 v180, v85, v180
	v_add_f32_e32 v180, v86, v180
	v_add_f32_e32 v180, v87, v180
	v_add_f32_e32 v180, v88, v180
	v_add_f32_e32 v180, v89, v180
	s_waitcnt lgkmcnt(0)
	v_mfma_f32_32x32x16_bf16 v[98:113], v[130:133], v[122:125], v[98:113]
	v_mfma_f32_32x32x16_bf16 v[66:81], v[134:137], v[122:125], v[66:81]
	v_add_u32_e32 v134, s26, v167
	ds_read_b128 v[130:133], v134
	ds_read_b128 v[134:137], v134 offset:8192
	v_add_f32_e32 v180, v90, v180
	v_add_f32_e32 v180, v91, v180
	v_add_f32_e32 v180, v92, v180
	v_add_f32_e32 v180, v93, v180
	v_add_f32_e32 v180, v94, v180
	v_add_f32_e32 v180, v95, v180
	v_add_f32_e32 v180, v96, v180
	v_add_f32_e32 v180, v97, v180
	s_waitcnt lgkmcnt(0)
	v_mfma_f32_32x32x16_bf16 v[98:113], v[130:133], v[126:129], v[98:113]
	v_mfma_f32_32x32x16_bf16 v[66:81], v[134:137], v[126:129], v[66:81]
	v_add_f32_e32 v172, v172, v180
	v_cvt_pk_bf16_f32 v130, v197, v200
	v_cvt_pk_bf16_f32 v131, v198, v202
	v_cvt_pk_bf16_f32 v132, v204, v207
	v_cvt_pk_bf16_f32 v133, v205, v210
	v_cvt_pk_bf16_f32 v134, v199, v203
	v_cvt_pk_bf16_f32 v135, v201, v209
	v_cvt_pk_bf16_f32 v136, v206, v211
	v_cvt_pk_bf16_f32 v137, v208, v212
	v_cvt_pk_bf16_f32 v138, v82, v83
	v_cvt_pk_bf16_f32 v139, v84, v85
	v_cvt_pk_bf16_f32 v140, v86, v87
	v_cvt_pk_bf16_f32 v141, v88, v89
	v_cvt_pk_bf16_f32 v142, v90, v91
	v_cvt_pk_bf16_f32 v143, v92, v93
	v_cvt_pk_bf16_f32 v144, v94, v95
	v_cvt_pk_bf16_f32 v145, v96, v97
	ds_read_b64_tr_b16 v[174:175], v170 offset:0
	ds_read_b64_tr_b16 v[176:177], v170 offset:0x800
	ds_read_b64_tr_b16 v[184:185], v170 offset:0x1000
	ds_read_b64_tr_b16 v[186:187], v170 offset:0x1800
	ds_read_b64_tr_b16 v[188:189], v170 offset:0x2000
	ds_read_b64_tr_b16 v[190:191], v170 offset:0x2800
	ds_read_b64_tr_b16 v[192:193], v170 offset:0x3000
	ds_read_b64_tr_b16 v[194:195], v170 offset:0x3800
	ds_read_b64_tr_b16 v[214:215], v170 offset:0x200
	ds_read_b64_tr_b16 v[216:217], v170 offset:0xa00
	ds_read_b64_tr_b16 v[218:219], v170 offset:0x1200
	s_nop 0
	v_permlane32_swap_b32_e32 v130, v132
	v_permlane32_swap_b32_e32 v131, v133
	ds_read_b64_tr_b16 v[220:221], v170 offset:0x1a00
	ds_read_b64_tr_b16 v[222:223], v170 offset:0x2200
	ds_read_b64_tr_b16 v[224:225], v170 offset:0x2a00
	ds_read_b64_tr_b16 v[226:227], v170 offset:0x3200
	ds_read_b64_tr_b16 v[228:229], v170 offset:0x3a00
	s_waitcnt lgkmcnt(8)
	v_permlane32_swap_b32_e32 v134, v136
	s_nop 0
	v_mfma_f32_32x32x16_bf16 v[2:17], v[130:133], v[174:177], v[2:17]
	v_permlane32_swap_b32_e32 v135, v137
	v_permlane32_swap_b32_e32 v138, v140
	v_permlane32_swap_b32_e32 v139, v141
	ds_read_b64_tr_b16 v[174:175], v170 offset:0x400
	v_mfma_f32_32x32x16_bf16 v[2:17], v[134:137], v[184:187], v[2:17]
	v_permlane32_swap_b32_e32 v142, v144
	v_permlane32_swap_b32_e32 v143, v145
	ds_read_b64_tr_b16 v[176:177], v170 offset:0xc00
	ds_read_b64_tr_b16 v[184:185], v170 offset:0x1400
	ds_read_b64_tr_b16 v[186:187], v170 offset:0x1c00
	v_mfma_f32_32x32x16_bf16 v[2:17], v[138:141], v[188:191], v[2:17]
	ds_read_b64_tr_b16 v[188:189], v170 offset:0x2400
	ds_read_b64_tr_b16 v[190:191], v170 offset:0x2c00
	v_exp_f32_e32 v173, v98
	v_exp_f32_e32 v196, v113
	v_mfma_f32_32x32x16_bf16 v[2:17], v[142:145], v[192:195], v[2:17]
	ds_read_b64_tr_b16 v[192:193], v170 offset:0x3400
	ds_read_b64_tr_b16 v[194:195], v170 offset:0x3c00
	s_waitcnt lgkmcnt(8)
	s_nop 0
	v_mfma_f32_32x32x16_bf16 v[50:65], v[130:133], v[214:217], v[50:65]
	ds_read_b64_tr_b16 v[214:215], v170 offset:0x600
	ds_read_b64_tr_b16 v[216:217], v170 offset:0xe00
	v_mfma_f32_32x32x16_bf16 v[50:65], v[134:137], v[218:221], v[50:65]
	ds_read_b64_tr_b16 v[218:219], v170 offset:0x1600
	ds_read_b64_tr_b16 v[220:221], v170 offset:0x1e00
	v_mfma_f32_32x32x16_bf16 v[50:65], v[138:141], v[222:225], v[50:65]
	ds_read_b64_tr_b16 v[222:223], v170 offset:0x2600
	ds_read_b64_tr_b16 v[224:225], v170 offset:0x2e00
	v_mfma_f32_32x32x16_bf16 v[50:65], v[142:145], v[226:229], v[50:65]
	ds_read_b64_tr_b16 v[226:227], v170 offset:0x3600
	ds_read_b64_tr_b16 v[228:229], v170 offset:0x3e00
	s_waitcnt lgkmcnt(8)
	s_nop 0
	s_waitcnt lgkmcnt(0)
	v_mfma_f32_32x32x16_bf16 v[34:49], v[130:133], v[174:177], v[34:49]
	v_exp_f32_e32 v174, v99
	v_exp_f32_e32 v175, v100
	v_mfma_f32_32x32x16_bf16 v[18:33], v[130:133], v[214:217], v[18:33]
	v_mfma_f32_32x32x16_bf16 v[34:49], v[134:137], v[184:187], v[34:49]
	v_exp_f32_e32 v184, v101
	v_exp_f32_e32 v185, v102
	v_exp_f32_e32 v186, v103
	v_exp_f32_e32 v187, v104
	v_mfma_f32_32x32x16_bf16 v[18:33], v[134:137], v[218:221], v[18:33]
	v_mfma_f32_32x32x16_bf16 v[34:49], v[138:141], v[188:191], v[34:49]
	v_exp_f32_e32 v188, v105
	v_exp_f32_e32 v189, v106
	v_exp_f32_e32 v190, v107
	v_exp_f32_e32 v191, v108
	v_mfma_f32_32x32x16_bf16 v[18:33], v[138:141], v[222:225], v[18:33]
	v_mfma_f32_32x32x16_bf16 v[34:49], v[142:145], v[192:195], v[34:49]
	v_exp_f32_e32 v192, v109
	v_exp_f32_e32 v193, v110
	v_exp_f32_e32 v194, v111
	v_exp_f32_e32 v195, v112
	v_mfma_f32_32x32x16_bf16 v[18:33], v[142:145], v[226:229], v[18:33]
	s_andn2_b64 vcc, exec, s[24:25]
	s_cbranch_vccz .LBB0_866

; __device__ __forceinline__ void finishSM(f32x16& p0, f32x16& p1, float& l_reg, bf16x8& pa0, bf16x8& pa1, bf16x8& pa2, bf16x8& pa3) {
; #pragma unroll
;   for (int r = 0; r < 16; ++r) p1[r] = __builtin_amdgcn_exp2f(p1[r]);
;   float ps = 0;
; #pragma unroll
;   for (int r = 0; r < 16; ++r) ps += p0[r];
; #pragma unroll
;   for (int r = 0; r < 16; ++r) ps += p1[r];
;   l_reg += ps;
;     ...
;   ATT_PK4(p0, 0, pa0); ATT_PK4(p0, 8, pa1); ATT_PK4(p1, 0, pa2); ATT_PK4(p1, 8, pa3);
;     ...
; }
; template <int DK>
; __device__ __forceinline__ void qkt(f32x16& p0, f32x16& p1, const char* Ks, const bf16x8* qr, int r32, int hi) {
;   p0 = f32x16{}; p1 = f32x16{};
; #pragma unroll
;   for (int d0 = 0; d0 < DK / 16; ++d0) { const int cb = (d0 * 16 + hi * 8) * 2;
;     const bf16x8 b0 = *reinterpret_cast<const bf16x8*>(Ks + ATT_KSWZ(r32, cb));
;     const bf16x8 b1 = *reinterpret_cast<const bf16x8*>(Ks + ATT_KSWZ(32 + r32, cb));
;     p0 = __builtin_amdgcn_mfma_f32_32x32x16_bf16(b0, qr[d0], p0, 0, 0, 0);
;     p1 = __builtin_amdgcn_mfma_f32_32x32x16_bf16(b1, qr[d0], p1, 0, 0, 0);
;   }
; }
; template <int N> __device__ __forceinline__ void lgkm_wait8(s16x4* v) { asm volatile("s_waitcnt lgkmcnt(%8)" : "+v"(v[0]), "+v"(v[1]), "+v"(v[2]), "+v"(v[3]), "+v"(v[4]), "+v"(v[5]), "+v"(v[6]), "+v"(v[7]) : "n"(N) : "memory"); }
; template <int DV, int GRP> __device__ __forceinline__ void v_group_read(s16x4* vf, int vb) {
;   sfor<0, 8>([&](auto ic) { constexpr int j = decltype(ic)::value; vf[j] = tr_read<v_rd_off<DV>(GRP, j / 2, j % 2)>(vb); });
; }
; __device__ __forceinline__ void pv_group(f32x16& od, const s16x4* vf, bf16x8 pa0, bf16x8 pa1, bf16x8 pa2, bf16x8 pa3) {
;     ...
;   od = __builtin_amdgcn_mfma_f32_32x32x16_bf16(pa0, ATT_PK(vf[0], vf[1]), od, 0, 0, 0);
;   od = __builtin_amdgcn_mfma_f32_32x32x16_bf16(pa1, ATT_PK(vf[2], vf[3]), od, 0, 0, 0);
;   od = __builtin_amdgcn_mfma_f32_32x32x16_bf16(pa2, ATT_PK(vf[4], vf[5]), od, 0, 0, 0);
;   od = __builtin_amdgcn_mfma_f32_32x32x16_bf16(pa3, ATT_PK(vf[6], vf[7]), od, 0, 0, 0);
;     ...
; }
; template <int DV> __device__ __forceinline__ void pv_all_pipe(f32x16* o, int vb, bf16x8 pa0, bf16x8 pa1, bf16x8 pa2, bf16x8 pa3) {
;   s16x4 va[8], vc[8];
;   v_group_read<DV, 0>(va, vb); v_group_read<DV, 1>(vc, vb);
;   lgkm_wait8<8>(va); pv_group(o[0], va, pa0, pa1, pa2, pa3);
;   if constexpr (DV == 128) {
;     s16x4 vd[8], ve[8];
;     v_group_read<DV, 2>(vd, vb);
.LBB0_872:
	s_add_i32 s24, 0, 0x1c000
	v_add_u32_e32 v86, s24, v161
	ds_read_b128 v[82:85], v86
	ds_read_b128 v[86:89], v86 offset:8192
	v_add_u32_e32 v134, s24, v163
	ds_read_b128 v[130:133], v134
	ds_read_b128 v[134:137], v134 offset:8192
	v_exp_f32_e32 v66, v66
	v_add_f32_e32 v180, 0, v173
	v_add_f32_e32 v180, v174, v180
	v_add_f32_e32 v180, v175, v180
	v_add_f32_e32 v180, v184, v180
	v_add_f32_e32 v180, v185, v180
	v_add_f32_e32 v180, v186, v180
	v_add_f32_e32 v180, v187, v180
	v_add_f32_e32 v180, v188, v180
	v_add_f32_e32 v180, v189, v180
	v_add_f32_e32 v180, v190, v180
	v_add_f32_e32 v180, v191, v180
	v_add_f32_e32 v180, v192, v180
	v_add_f32_e32 v180, v193, v180
	v_add_f32_e32 v180, v194, v180
	v_add_f32_e32 v180, v195, v180
	v_add_f32_e32 v180, v196, v180
	s_waitcnt lgkmcnt(0)
	v_mfma_f32_32x32x16_bf16 v[98:113], v[82:85], v[114:117], 0
	v_exp_f32_e32 v67, v67
	v_exp_f32_e32 v68, v68
	v_exp_f32_e32 v69, v69
	v_exp_f32_e32 v70, v70
	v_exp_f32_e32 v71, v71
	v_exp_f32_e32 v72, v72
	v_exp_f32_e32 v73, v73
	v_mfma_f32_32x32x16_bf16 v[82:97], v[86:89], v[114:117], 0
	v_exp_f32_e32 v74, v74
	v_exp_f32_e32 v75, v75
	v_exp_f32_e32 v76, v76
	v_exp_f32_e32 v77, v77
	v_exp_f32_e32 v78, v78
	v_exp_f32_e32 v79, v79
	v_exp_f32_e32 v80, v80
	v_mfma_f32_32x32x16_bf16 v[98:113], v[130:133], v[118:121], v[98:113]
	v_exp_f32_e32 v81, v81
	v_mfma_f32_32x32x16_bf16 v[82:97], v[134:137], v[118:121], v[82:97]
	v_add_u32_e32 v134, s24, v165
	ds_read_b128 v[130:133], v134
	ds_read_b128 v[134:137], v134 offset:8192
	v_add_f32_e32 v180, v66, v180
	v_add_f32_e32 v180, v67, v180
	v_add_f32_e32 v180, v68, v180
	v_add_f32_e32 v180, v69, v180
	v_add_f32_e32 v180, v70, v180
	v_add_f32_e32 v180, v71, v180
	v_add_f32_e32 v180, v72, v180
	v_add_f32_e32 v180, v73, v180
	s_waitcnt lgkmcnt(0)
	v_mfma_f32_32x32x16_bf16 v[98:113], v[130:133], v[122:125], v[98:113]
	v_mfma_f32_32x32x16_bf16 v[82:97], v[134:137], v[122:125], v[82:97]
	v_add_u32_e32 v134, s24, v167
	ds_read_b128 v[130:133], v134
	ds_read_b128 v[134:137], v134 offset:8192
	v_add_f32_e32 v180, v74, v180
	v_add_f32_e32 v180, v75, v180
	v_add_f32_e32 v180, v76, v180
	v_add_f32_e32 v180, v77, v180
	v_add_f32_e32 v180, v78, v180
	v_add_f32_e32 v180, v79, v180
	v_add_f32_e32 v180, v80, v180
	v_add_f32_e32 v180, v81, v180
	s_waitcnt lgkmcnt(0)
	v_mfma_f32_32x32x16_bf16 v[98:113], v[130:133], v[126:129], v[98:113]
	v_mfma_f32_32x32x16_bf16 v[82:97], v[134:137], v[126:129], v[82:97]
	v_add_f32_e32 v172, v172, v180
	v_cvt_pk_bf16_f32 v130, v173, v174
	v_cvt_pk_bf16_f32 v131, v175, v184
	v_cvt_pk_bf16_f32 v132, v185, v186
	v_cvt_pk_bf16_f32 v133, v187, v188
	v_cvt_pk_bf16_f32 v134, v189, v190
	v_cvt_pk_bf16_f32 v135, v191, v192
	v_cvt_pk_bf16_f32 v136, v193, v194
	v_cvt_pk_bf16_f32 v137, v195, v196
	v_cvt_pk_bf16_f32 v138, v66, v67
	v_cvt_pk_bf16_f32 v139, v68, v69
	v_cvt_pk_bf16_f32 v140, v70, v71
	v_cvt_pk_bf16_f32 v141, v72, v73
	v_cvt_pk_bf16_f32 v142, v74, v75
	v_cvt_pk_bf16_f32 v143, v76, v77
	v_cvt_pk_bf16_f32 v144, v78, v79
	v_cvt_pk_bf16_f32 v145, v80, v81
	ds_read_b64_tr_b16 v[176:177], v171 offset:0
	ds_read_b64_tr_b16 v[178:179], v171 offset:0x800
	ds_read_b64_tr_b16 v[198:199], v171 offset:0x1000
	ds_read_b64_tr_b16 v[200:201], v171 offset:0x1800
	ds_read_b64_tr_b16 v[202:203], v171 offset:0x2000
	ds_read_b64_tr_b16 v[204:205], v171 offset:0x2800
	ds_read_b64_tr_b16 v[206:207], v171 offset:0x3000
	ds_read_b64_tr_b16 v[208:209], v171 offset:0x3800
	ds_read_b64_tr_b16 v[210:211], v171 offset:0x200
	ds_read_b64_tr_b16 v[212:213], v171 offset:0xa00
	ds_read_b64_tr_b16 v[214:215], v171 offset:0x1200
	s_nop 0
	v_permlane32_swap_b32_e32 v130, v132
	v_permlane32_swap_b32_e32 v131, v133
	ds_read_b64_tr_b16 v[216:217], v171 offset:0x1a00
	ds_read_b64_tr_b16 v[218:219], v171 offset:0x2200
	ds_read_b64_tr_b16 v[220:221], v171 offset:0x2a00
	ds_read_b64_tr_b16 v[222:223], v171 offset:0x3200
	ds_read_b64_tr_b16 v[224:225], v171 offset:0x3a00
	s_waitcnt lgkmcnt(8)
	v_permlane32_swap_b32_e32 v134, v136
	s_nop 0
	v_mfma_f32_32x32x16_bf16 v[2:17], v[130:133], v[176:179], v[2:17]
	v_permlane32_swap_b32_e32 v135, v137
	v_permlane32_swap_b32_e32 v138, v140
	v_permlane32_swap_b32_e32 v139, v141
	ds_read_b64_tr_b16 v[176:177], v171 offset:0x400
	v_mfma_f32_32x32x16_bf16 v[2:17], v[134:137], v[198:201], v[2:17]
	v_permlane32_swap_b32_e32 v142, v144
	v_permlane32_swap_b32_e32 v143, v145
	ds_read_b64_tr_b16 v[178:179], v171 offset:0xc00
	ds_read_b64_tr_b16 v[198:199], v171 offset:0x1400
	ds_read_b64_tr_b16 v[200:201], v171 offset:0x1c00
	v_mfma_f32_32x32x16_bf16 v[2:17], v[138:141], v[202:205], v[2:17]
	ds_read_b64_tr_b16 v[202:203], v171 offset:0x2400
	ds_read_b64_tr_b16 v[204:205], v171 offset:0x2c00
	v_exp_f32_e32 v197, v98
	v_mfma_f32_32x32x16_bf16 v[2:17], v[142:145], v[206:209], v[2:17]
	ds_read_b64_tr_b16 v[206:207], v171 offset:0x3400
	ds_read_b64_tr_b16 v[208:209], v171 offset:0x3c00
	s_waitcnt lgkmcnt(8)
	s_nop 0
	v_mfma_f32_32x32x16_bf16 v[50:65], v[130:133], v[210:213], v[50:65]
	ds_read_b64_tr_b16 v[210:211], v171 offset:0x600
	ds_read_b64_tr_b16 v[212:213], v171 offset:0xe00
	v_mfma_f32_32x32x16_bf16 v[50:65], v[134:137], v[214:217], v[50:65]
	ds_read_b64_tr_b16 v[214:215], v171 offset:0x1600
	ds_read_b64_tr_b16 v[216:217], v171 offset:0x1e00
	v_mfma_f32_32x32x16_bf16 v[50:65], v[138:141], v[218:221], v[50:65]
	ds_read_b64_tr_b16 v[218:219], v171 offset:0x2600
	ds_read_b64_tr_b16 v[220:221], v171 offset:0x2e00
	v_mfma_f32_32x32x16_bf16 v[50:65], v[142:145], v[222:225], v[50:65]
	ds_read_b64_tr_b16 v[222:223], v171 offset:0x3600
	ds_read_b64_tr_b16 v[224:225], v171 offset:0x3e00
	s_waitcnt lgkmcnt(8)
	s_nop 0
	s_waitcnt lgkmcnt(0)
	v_mfma_f32_32x32x16_bf16 v[34:49], v[130:133], v[176:179], v[34:49]
	v_mfma_f32_32x32x16_bf16 v[18:33], v[130:133], v[210:213], v[18:33]
	v_exp_f32_e32 v210, v105
	v_exp_f32_e32 v211, v111
	v_exp_f32_e32 v212, v113
	v_mfma_f32_32x32x16_bf16 v[34:49], v[134:137], v[198:201], v[34:49]
	v_exp_f32_e32 v200, v99
	v_exp_f32_e32 v198, v100
	v_exp_f32_e32 v199, v106
	v_exp_f32_e32 v201, v108
	v_mfma_f32_32x32x16_bf16 v[18:33], v[134:137], v[214:217], v[18:33]
	v_mfma_f32_32x32x16_bf16 v[34:49], v[138:141], v[202:205], v[34:49]
	v_exp_f32_e32 v202, v101
	v_exp_f32_e32 v204, v102
	v_exp_f32_e32 v205, v104
	v_exp_f32_e32 v203, v107
	v_mfma_f32_32x32x16_bf16 v[18:33], v[138:141], v[218:221], v[18:33]
	v_mfma_f32_32x32x16_bf16 v[34:49], v[142:145], v[206:209], v[34:49]
	v_exp_f32_e32 v207, v103
	v_exp_f32_e32 v209, v109
	v_exp_f32_e32 v206, v110
	v_exp_f32_e32 v208, v112
	v_mfma_f32_32x32x16_bf16 v[18:33], v[142:145], v[222:225], v[18:33]
	s_cmp_ge_u32 s57, s97
	s_cbranch_scc1 .LBB0_880

; __device__ __forceinline__ void finishSM(f32x16& p0, f32x16& p1, float& l_reg, bf16x8& pa0, bf16x8& pa1, bf16x8& pa2, bf16x8& pa3) {
; #pragma unroll
;   for (int r = 0; r < 16; ++r) p1[r] = __builtin_amdgcn_exp2f(p1[r]);
;   float ps = 0;
; #pragma unroll
;   for (int r = 0; r < 16; ++r) ps += p0[r];
; #pragma unroll
;   for (int r = 0; r < 16; ++r) ps += p1[r];
;   l_reg += ps;
;     ...
;   ATT_PK4(p0, 0, pa0); ATT_PK4(p0, 8, pa1); ATT_PK4(p1, 0, pa2); ATT_PK4(p1, 8, pa3);
;     ...
; }
; template <int DK>
; __device__ __forceinline__ void qkt(f32x16& p0, f32x16& p1, const char* Ks, const bf16x8* qr, int r32, int hi) {
;   p0 = f32x16{}; p1 = f32x16{};
; #pragma unroll
;   for (int d0 = 0; d0 < DK / 16; ++d0) { const int cb = (d0 * 16 + hi * 8) * 2;
;     const bf16x8 b0 = *reinterpret_cast<const bf16x8*>(Ks + ATT_KSWZ(r32, cb));
;     const bf16x8 b1 = *reinterpret_cast<const bf16x8*>(Ks + ATT_KSWZ(32 + r32, cb));
;     p0 = __builtin_amdgcn_mfma_f32_32x32x16_bf16(b0, qr[d0], p0, 0, 0, 0);
;     p1 = __builtin_amdgcn_mfma_f32_32x32x16_bf16(b1, qr[d0], p1, 0, 0, 0);
;   }
; }
; template <int N> __device__ __forceinline__ void lgkm_wait8(s16x4* v) { asm volatile("s_waitcnt lgkmcnt(%8)" : "+v"(v[0]), "+v"(v[1]), "+v"(v[2]), "+v"(v[3]), "+v"(v[4]), "+v"(v[5]), "+v"(v[6]), "+v"(v[7]) : "n"(N) : "memory"); }
; template <int DV, int GRP> __device__ __forceinline__ void v_group_read(s16x4* vf, int vb) {
;   sfor<0, 8>([&](auto ic) { constexpr int j = decltype(ic)::value; vf[j] = tr_read<v_rd_off<DV>(GRP, j / 2, j % 2)>(vb); });
; }
; __device__ __forceinline__ void pv_group(f32x16& od, const s16x4* vf, bf16x8 pa0, bf16x8 pa1, bf16x8 pa2, bf16x8 pa3) {
;     ...
;   od = __builtin_amdgcn_mfma_f32_32x32x16_bf16(pa0, ATT_PK(vf[0], vf[1]), od, 0, 0, 0);
;   od = __builtin_amdgcn_mfma_f32_32x32x16_bf16(pa1, ATT_PK(vf[2], vf[3]), od, 0, 0, 0);
;   od = __builtin_amdgcn_mfma_f32_32x32x16_bf16(pa2, ATT_PK(vf[4], vf[5]), od, 0, 0, 0);
;   od = __builtin_amdgcn_mfma_f32_32x32x16_bf16(pa3, ATT_PK(vf[6], vf[7]), od, 0, 0, 0);
;     ...
; }
; template <int DV> __device__ __forceinline__ void pv_all_pipe(f32x16* o, int vb, bf16x8 pa0, bf16x8 pa1, bf16x8 pa2, bf16x8 pa3) {
;   s16x4 va[8], vc[8];
;   v_group_read<DV, 0>(va, vb); v_group_read<DV, 1>(vc, vb);
;   lgkm_wait8<8>(va); pv_group(o[0], va, pa0, pa1, pa2, pa3);
;   if constexpr (DV == 128) {
;     s16x4 vd[8], ve[8];
;     v_group_read<DV, 2>(vd, vb);
.LBB0_879:
	ds_read_b128 v[66:69], v162
	ds_read_b128 v[70:73], v162 offset:8192
	ds_read_b128 v[130:133], v164
	ds_read_b128 v[134:137], v164 offset:8192
	v_exp_f32_e32 v82, v82
	v_exp_f32_e32 v83, v83
	v_add_f32_e32 v180, 0, v197
	v_add_f32_e32 v180, v200, v180
	v_add_f32_e32 v180, v198, v180
	v_add_f32_e32 v180, v202, v180
	v_add_f32_e32 v180, v204, v180
	v_add_f32_e32 v180, v207, v180
	v_add_f32_e32 v180, v205, v180
	v_add_f32_e32 v180, v210, v180
	v_add_f32_e32 v180, v199, v180
	v_add_f32_e32 v180, v203, v180
	v_add_f32_e32 v180, v201, v180
	v_add_f32_e32 v180, v209, v180
	v_add_f32_e32 v180, v206, v180
	v_add_f32_e32 v180, v211, v180
	v_add_f32_e32 v180, v208, v180
	v_add_f32_e32 v180, v212, v180
	s_waitcnt lgkmcnt(0)
	v_mfma_f32_32x32x16_bf16 v[98:113], v[66:69], v[114:117], 0
	v_exp_f32_e32 v84, v84
	v_exp_f32_e32 v85, v85
	v_exp_f32_e32 v86, v86
	v_exp_f32_e32 v87, v87
	v_exp_f32_e32 v88, v88
	v_exp_f32_e32 v89, v89
	v_exp_f32_e32 v90, v90
	v_mfma_f32_32x32x16_bf16 v[66:81], v[70:73], v[114:117], 0
	v_exp_f32_e32 v91, v91
	v_exp_f32_e32 v92, v92
	v_exp_f32_e32 v93, v93
	v_exp_f32_e32 v94, v94
	v_exp_f32_e32 v95, v95
	v_exp_f32_e32 v96, v96
	v_exp_f32_e32 v97, v97
	v_mfma_f32_32x32x16_bf16 v[98:113], v[130:133], v[118:121], v[98:113]
	v_mfma_f32_32x32x16_bf16 v[66:81], v[134:137], v[118:121], v[66:81]
	ds_read_b128 v[130:133], v166
	ds_read_b128 v[134:137], v166 offset:8192
	v_add_f32_e32 v180, v82, v180
	v_add_f32_e32 v180, v83, v180
	v_add_f32_e32 v180, v84, v180
	v_add_f32_e32 v180, v85, v180
	v_add_f32_e32 v180, v86, v180
	v_add_f32_e32 v180, v87, v180
	v_add_f32_e32 v180, v88, v180
	v_add_f32_e32 v180, v89, v180
	s_waitcnt lgkmcnt(0)
	v_mfma_f32_32x32x16_bf16 v[98:113], v[130:133], v[122:125], v[98:113]
	v_mfma_f32_32x32x16_bf16 v[66:81], v[134:137], v[122:125], v[66:81]
	ds_read_b128 v[130:133], v168
	ds_read_b128 v[134:137], v168 offset:8192
	v_add_f32_e32 v180, v90, v180
	v_add_f32_e32 v180, v91, v180
	v_add_f32_e32 v180, v92, v180
	v_add_f32_e32 v180, v93, v180
	v_add_f32_e32 v180, v94, v180
	v_add_f32_e32 v180, v95, v180
	v_add_f32_e32 v180, v96, v180
	v_add_f32_e32 v180, v97, v180
	s_waitcnt lgkmcnt(0)
	v_mfma_f32_32x32x16_bf16 v[98:113], v[130:133], v[126:129], v[98:113]
	v_mfma_f32_32x32x16_bf16 v[66:81], v[134:137], v[126:129], v[66:81]
	v_add_f32_e32 v172, v172, v180
	v_cvt_pk_bf16_f32 v130, v197, v200
	v_cvt_pk_bf16_f32 v131, v198, v202
	v_cvt_pk_bf16_f32 v132, v204, v207
	v_cvt_pk_bf16_f32 v133, v205, v210
	v_cvt_pk_bf16_f32 v134, v199, v203
	v_cvt_pk_bf16_f32 v135, v201, v209
	v_cvt_pk_bf16_f32 v136, v206, v211
	v_cvt_pk_bf16_f32 v137, v208, v212
	v_cvt_pk_bf16_f32 v138, v82, v83
	v_cvt_pk_bf16_f32 v139, v84, v85
	v_cvt_pk_bf16_f32 v140, v86, v87
	v_cvt_pk_bf16_f32 v141, v88, v89
	v_cvt_pk_bf16_f32 v142, v90, v91
	v_cvt_pk_bf16_f32 v143, v92, v93
	v_cvt_pk_bf16_f32 v144, v94, v95
	v_cvt_pk_bf16_f32 v145, v96, v97
	ds_read_b64_tr_b16 v[174:175], v160 offset:0
	ds_read_b64_tr_b16 v[176:177], v160 offset:0x800
	ds_read_b64_tr_b16 v[184:185], v160 offset:0x1000
	ds_read_b64_tr_b16 v[186:187], v160 offset:0x1800
	ds_read_b64_tr_b16 v[188:189], v160 offset:0x2000
	ds_read_b64_tr_b16 v[190:191], v160 offset:0x2800
	ds_read_b64_tr_b16 v[192:193], v160 offset:0x3000
	ds_read_b64_tr_b16 v[194:195], v160 offset:0x3800
	ds_read_b64_tr_b16 v[214:215], v160 offset:0x200
	ds_read_b64_tr_b16 v[216:217], v160 offset:0xa00
	ds_read_b64_tr_b16 v[218:219], v160 offset:0x1200
	s_nop 0
	v_permlane32_swap_b32_e32 v130, v132
	v_permlane32_swap_b32_e32 v131, v133
	ds_read_b64_tr_b16 v[220:221], v160 offset:0x1a00
	ds_read_b64_tr_b16 v[222:223], v160 offset:0x2200
	ds_read_b64_tr_b16 v[224:225], v160 offset:0x2a00
	ds_read_b64_tr_b16 v[226:227], v160 offset:0x3200
	ds_read_b64_tr_b16 v[228:229], v160 offset:0x3a00
	s_waitcnt lgkmcnt(8)
	v_permlane32_swap_b32_e32 v134, v136
	s_nop 0
	v_mfma_f32_32x32x16_bf16 v[2:17], v[130:133], v[174:177], v[2:17]
	v_permlane32_swap_b32_e32 v135, v137
	v_permlane32_swap_b32_e32 v138, v140
	v_permlane32_swap_b32_e32 v139, v141
	ds_read_b64_tr_b16 v[174:175], v160 offset:0x400
	v_mfma_f32_32x32x16_bf16 v[2:17], v[134:137], v[184:187], v[2:17]
	v_permlane32_swap_b32_e32 v142, v144
	v_permlane32_swap_b32_e32 v143, v145
	ds_read_b64_tr_b16 v[176:177], v160 offset:0xc00
	ds_read_b64_tr_b16 v[184:185], v160 offset:0x1400
	ds_read_b64_tr_b16 v[186:187], v160 offset:0x1c00
	v_mfma_f32_32x32x16_bf16 v[2:17], v[138:141], v[188:191], v[2:17]
	ds_read_b64_tr_b16 v[188:189], v160 offset:0x2400
	ds_read_b64_tr_b16 v[190:191], v160 offset:0x2c00
	v_exp_f32_e32 v173, v98
	v_exp_f32_e32 v196, v113
	v_mfma_f32_32x32x16_bf16 v[2:17], v[142:145], v[192:195], v[2:17]
	ds_read_b64_tr_b16 v[192:193], v160 offset:0x3400
	ds_read_b64_tr_b16 v[194:195], v160 offset:0x3c00
	s_waitcnt lgkmcnt(8)
	s_nop 0
	v_mfma_f32_32x32x16_bf16 v[50:65], v[130:133], v[214:217], v[50:65]
	ds_read_b64_tr_b16 v[214:215], v160 offset:0x600
	ds_read_b64_tr_b16 v[216:217], v160 offset:0xe00
	v_mfma_f32_32x32x16_bf16 v[50:65], v[134:137], v[218:221], v[50:65]
	ds_read_b64_tr_b16 v[218:219], v160 offset:0x1600
	ds_read_b64_tr_b16 v[220:221], v160 offset:0x1e00
	v_mfma_f32_32x32x16_bf16 v[50:65], v[138:141], v[222:225], v[50:65]
	ds_read_b64_tr_b16 v[222:223], v160 offset:0x2600
	ds_read_b64_tr_b16 v[224:225], v160 offset:0x2e00
	v_mfma_f32_32x32x16_bf16 v[50:65], v[142:145], v[226:229], v[50:65]
	ds_read_b64_tr_b16 v[226:227], v160 offset:0x3600
	ds_read_b64_tr_b16 v[228:229], v160 offset:0x3e00
	s_waitcnt lgkmcnt(8)
	s_nop 0
	s_waitcnt lgkmcnt(0)
	v_mfma_f32_32x32x16_bf16 v[34:49], v[130:133], v[174:177], v[34:49]
	v_exp_f32_e32 v174, v99
	v_exp_f32_e32 v175, v100
	v_mfma_f32_32x32x16_bf16 v[18:33], v[130:133], v[214:217], v[18:33]
	v_mfma_f32_32x32x16_bf16 v[34:49], v[134:137], v[184:187], v[34:49]
	v_exp_f32_e32 v184, v101
	v_exp_f32_e32 v185, v102
	v_exp_f32_e32 v186, v103
	v_exp_f32_e32 v187, v104
	v_mfma_f32_32x32x16_bf16 v[18:33], v[134:137], v[218:221], v[18:33]
	v_mfma_f32_32x32x16_bf16 v[34:49], v[138:141], v[188:191], v[34:49]
	v_exp_f32_e32 v188, v105
	v_exp_f32_e32 v189, v106
	v_exp_f32_e32 v190, v107
	v_exp_f32_e32 v191, v108
	v_mfma_f32_32x32x16_bf16 v[18:33], v[138:141], v[222:225], v[18:33]
	v_mfma_f32_32x32x16_bf16 v[34:49], v[142:145], v[192:195], v[34:49]
	v_exp_f32_e32 v192, v109
	v_exp_f32_e32 v193, v110
	v_exp_f32_e32 v194, v111
	v_exp_f32_e32 v195, v112
	v_mfma_f32_32x32x16_bf16 v[18:33], v[142:145], v[226:229], v[18:33]

; #define PG8_STAGE(bufoff, gbase, voff) do { _Pragma("unroll") for (int _i = 0; _i < 2; ++_i) \
;         __builtin_amdgcn_global_load_lds((const unsigned*)((const char*)(gbase) + (voff)[_i]), (PG8_LAS unsigned*)(lds + (bufoff) + ldsw + _i * 8192), 16, 0, 0); } while (0)
; #define PG8_WAIT_V(n) asm volatile("s_waitcnt vmcnt(" #n ")" ::: "memory")
; #define PG8_BAR __builtin_amdgcn_s_barrier()
; template <class Epi, class Sched, bool ALIGN_EPI = false, bool SP2 = false, bool GATHER = false>
; __device__ __forceinline__ void gemm_phase(PG8_LAS unsigned char* lds, const Gemm g, const Sched& S, const Epi& E, int tid_in, const int* rowsrc = nullptr, PG8_LAS int* idx_lds = nullptr) {
;     ...
;         for (int t = 0; t < nt; t += 2) {
;             const bool last = (t == nt - 2);
;             if constexpr (GATHER) {
; #pragma unroll
;                 for (int h_ = 0; h_ < 2; ++h_) { gS[h_][0] = last ? gN[h_][0] : gA[h_][0]; gS[h_][1] = last ? gN[h_][1] : gA[h_][1]; } }
;             const char* a1 = cA + (size_t)(t + 1) * kstep;
;             const char* a2 = last ? nA : cA + (size_t)(t + 2) * kstep; const char* b2 = last ? nB : cB + (size_t)(t + 2) * kstep;
;             const char* a3 = a2 + kstep; const char* b3 = b2 + kstep;
;             if (last && has_next) S.a_ready(nxt);
;             if constexpr (SP2) {
;             PG8_LDB(B0, 0, 0); PG8_LDB(B1, 0, 1); PG8_SCHED; PG8_LDA(At, 0, 0); PG8_STAGE(PG8_SA(1, 1), a1 + hstepA, PG8_OA(1));
;             PG8_WAIT_V(8); PG8_WAIT_L(0); PG8_BAR; PG8_MMA(0, 0, At, B0); PG8_MMA(0, 1, At, B1); PG8_BAR; PG8_SCHED;
;             PG8_LDA(At, 0, 1); PG8_STAGE(PG8_SB(0, 0), b2, voffB); PG8_STAGE(PG8_SB(0, 1), b2 + hstep, voffB); PG8_STAGE(PG8_SA(0, 0), a2, PG8_OS(0));
;             PG8_WAIT_V(8); PG8_WAIT_L(0); PG8_BAR; PG8_MMA(1, 0, At, B0); PG8_MMA(1, 1, At, B1); PG8_BAR; PG8_SCHED;
;             PG8_LDB(B0, 1, 0); PG8_LDB(B1, 1, 1); PG8_SCHED; PG8_LDA(At, 1, 0); PG8_STAGE(PG8_SA(0, 1), a2 + hstepA, PG8_OS(1));
;             PG8_WAIT_V(8); PG8_WAIT_L(0); PG8_BAR; PG8_MMA(0, 0, At, B0); PG8_MMA(0, 1, At, B1); PG8_BAR; PG8_SCHED;
;             PG8_LDA(At, 1, 1); PG8_STAGE(PG8_SB(1, 0), b3, voffB); PG8_STAGE(PG8_SB(1, 1), b3 + hstep, voffB); PG8_STAGE(PG8_SA(1, 0), a3, PG8_OS(0));
;             PG8_WAIT_V(8); PG8_WAIT_L(0); PG8_BAR; PG8_MMA(1, 0, At, B0); PG8_MMA(1, 1, At, B1); PG8_BAR; PG8_SCHED;
.LBB0_1101:
	s_add_u32 s22, s20, 0xfffc0080
	s_addc_u32 s23, s21, -1
	s_add_i32 s58, 0, 0x10000
	s_cmp_eq_u32 s57, 12
	s_cselect_b32 s25, s9, s23
	s_cselect_b32 s24, s17, s22
	s_cselect_b32 s23, s7, s56
	s_cselect_b32 s22, s19, s55
	s_add_i32 s60, 0, 0x14000
	v_add_u32_e32 v142, s58, v184
	v_add_u32_e32 v182, s60, v184
	ds_read_b128 v[122:125], v142
	ds_read_b128 v[126:129], v142 offset:1024
	ds_read_b128 v[134:137], v142 offset:2048
	ds_read_b128 v[142:145], v142 offset:3072
	ds_read_b128 v[174:177], v182
	ds_read_b128 v[178:181], v182 offset:1024
	ds_read_b128 v[188:191], v182 offset:2048
	ds_read_b128 v[192:195], v182 offset:3072
	v_lshl_add_u64 v[182:183], s[20:21], 0, v[170:171]
	s_add_i32 m0, s39, 0xc000
	ds_read_b128 v[196:199], v186
	ds_read_b128 v[200:203], v186 offset:1024
	ds_read_b128 v[204:207], v186 offset:2048
	ds_read_b128 v[208:211], v186 offset:3072
	ds_read_b128 v[212:215], v186 offset:4096
	ds_read_b128 v[216:219], v186 offset:5120
	ds_read_b128 v[220:223], v186 offset:6144
	ds_read_b128 v[224:227], v186 offset:7168
	global_load_lds_dwordx4 v[182:183], off
	v_lshl_add_u64 v[182:183], s[20:21], 0, v[172:173]
	s_add_i32 m0, s39, 0xe000
	s_nop 0
	global_load_lds_dwordx4 v[182:183], off
	s_waitcnt vmcnt(8)
	s_waitcnt lgkmcnt(0)
	s_barrier
	s_setprio 1
	s_waitcnt lgkmcnt(0)
	v_mfma_f32_16x16x32_bf16 v[138:141], v[122:125], v[196:199], v[138:141]
	v_mfma_f32_16x16x32_bf16 v[130:133], v[134:137], v[196:199], v[130:133]
	v_mfma_f32_16x16x32_bf16 v[118:121], v[122:125], v[204:207], v[118:121]
	v_mfma_f32_16x16x32_bf16 v[106:109], v[134:137], v[204:207], v[106:109]
	v_mfma_f32_16x16x32_bf16 v[102:105], v[122:125], v[212:215], v[102:105]
	v_mfma_f32_16x16x32_bf16 v[90:93], v[134:137], v[212:215], v[90:93]
	v_mfma_f32_16x16x32_bf16 v[86:89], v[122:125], v[220:223], v[86:89]
	v_mfma_f32_16x16x32_bf16 v[74:77], v[134:137], v[220:223], v[74:77]
	v_mfma_f32_16x16x32_bf16 v[138:141], v[126:129], v[200:203], v[138:141]
	v_mfma_f32_16x16x32_bf16 v[130:133], v[142:145], v[200:203], v[130:133]
	v_mfma_f32_16x16x32_bf16 v[118:121], v[126:129], v[208:211], v[118:121]
	v_mfma_f32_16x16x32_bf16 v[106:109], v[142:145], v[208:211], v[106:109]
	v_mfma_f32_16x16x32_bf16 v[102:105], v[126:129], v[216:219], v[102:105]
	v_mfma_f32_16x16x32_bf16 v[90:93], v[142:145], v[216:219], v[90:93]
	v_mfma_f32_16x16x32_bf16 v[86:89], v[126:129], v[224:227], v[86:89]
	v_mfma_f32_16x16x32_bf16 v[74:77], v[142:145], v[224:227], v[74:77]
	s_setprio 0
	s_setprio 1
	v_mfma_f32_16x16x32_bf16 v[114:117], v[174:177], v[196:199], v[114:117]
	v_mfma_f32_16x16x32_bf16 v[110:113], v[188:191], v[196:199], v[110:113]
	v_mfma_f32_16x16x32_bf16 v[98:101], v[174:177], v[204:207], v[98:101]
	v_mfma_f32_16x16x32_bf16 v[94:97], v[188:191], v[204:207], v[94:97]
	v_mfma_f32_16x16x32_bf16 v[82:85], v[174:177], v[212:215], v[82:85]
	v_mfma_f32_16x16x32_bf16 v[78:81], v[188:191], v[212:215], v[78:81]
	v_mfma_f32_16x16x32_bf16 v[70:73], v[174:177], v[220:223], v[70:73]
	v_mfma_f32_16x16x32_bf16 v[66:69], v[188:191], v[220:223], v[66:69]
	v_mfma_f32_16x16x32_bf16 v[114:117], v[178:181], v[200:203], v[114:117]
	v_mfma_f32_16x16x32_bf16 v[110:113], v[192:195], v[200:203], v[110:113]
	v_mfma_f32_16x16x32_bf16 v[98:101], v[178:181], v[208:211], v[98:101]
	v_mfma_f32_16x16x32_bf16 v[94:97], v[192:195], v[208:211], v[94:97]
	v_mfma_f32_16x16x32_bf16 v[82:85], v[178:181], v[216:219], v[82:85]
	v_mfma_f32_16x16x32_bf16 v[78:81], v[192:195], v[216:219], v[78:81]
	v_mfma_f32_16x16x32_bf16 v[70:73], v[178:181], v[224:227], v[70:73]
	v_mfma_f32_16x16x32_bf16 v[66:69], v[192:195], v[224:227], v[66:69]
	s_setprio 0
	s_barrier
	s_add_i32 s58, s58, s38
	v_lshl_add_u64 v[182:183], s[22:23], 0, v[0:1]
	s_mov_b32 m0, s58
	ds_read_b128 v[196:199], v186 offset:16384
	ds_read_b128 v[200:203], v186 offset:17408
	ds_read_b128 v[204:207], v186 offset:18432
	ds_read_b128 v[208:211], v186 offset:19456
	ds_read_b128 v[212:215], v186 offset:20480
	ds_read_b128 v[216:219], v186 offset:21504
	ds_read_b128 v[220:223], v186 offset:22528
	ds_read_b128 v[224:227], v186 offset:23552
	global_load_lds_dwordx4 v[182:183], off
	s_add_i32 m0, s58, 0x2000
	s_add_u32 s58, s22, 0x40000
	v_lshl_add_u64 v[228:229], s[22:23], 0, v[148:149]
	s_addc_u32 s59, s23, 0
	s_add_i32 s60, s60, s38
	global_load_lds_dwordx4 v[228:229], off
	v_lshl_add_u64 v[230:231], s[58:59], 0, v[0:1]
	s_mov_b32 m0, s60
	v_lshl_add_u64 v[232:233], s[24:25], 0, v[150:151]
	global_load_lds_dwordx4 v[230:231], off
	s_waitcnt vmcnt(5)
	s_waitcnt lgkmcnt(0)
	s_barrier
; #define PG8_STAGE(bufoff, gbase, voff) do { _Pragma("unroll") for (int _i = 0; _i < 2; ++_i) \
;         __builtin_amdgcn_global_load_lds((const unsigned*)((const char*)(gbase) + (voff)[_i]), (PG8_LAS unsigned*)(lds + (bufoff) + ldsw + _i * 8192), 16, 0, 0); } while (0)
; #define PG8_WAIT_V(n) asm volatile("s_waitcnt vmcnt(" #n ")" ::: "memory")
; #define PG8_BAR __builtin_amdgcn_s_barrier()
; template <class Epi, class Sched, bool ALIGN_EPI = false, bool SP2 = false, bool GATHER = false>
; __device__ __forceinline__ void gemm_phase(PG8_LAS unsigned char* lds, const Gemm g, const Sched& S, const Epi& E, int tid_in, const int* rowsrc = nullptr, PG8_LAS int* idx_lds = nullptr) {
;     ...
;         for (int t = 0; t < nt; t += 2) {
;             const bool last = (t == nt - 2);
;             if constexpr (GATHER) {
; #pragma unroll
;                 for (int h_ = 0; h_ < 2; ++h_) { gS[h_][0] = last ? gN[h_][0] : gA[h_][0]; gS[h_][1] = last ? gN[h_][1] : gA[h_][1]; } }
;             const char* a1 = cA + (size_t)(t + 1) * kstep;
;             const char* a2 = last ? nA : cA + (size_t)(t + 2) * kstep; const char* b2 = last ? nB : cB + (size_t)(t + 2) * kstep;
;             const char* a3 = a2 + kstep; const char* b3 = b2 + kstep;
;             if (last && has_next) S.a_ready(nxt);
;             if constexpr (SP2) {
;             PG8_LDB(B0, 0, 0); PG8_LDB(B1, 0, 1); PG8_SCHED; PG8_LDA(At, 0, 0); PG8_STAGE(PG8_SA(1, 1), a1 + hstepA, PG8_OA(1));
;             PG8_WAIT_V(8); PG8_WAIT_L(0); PG8_BAR; PG8_MMA(0, 0, At, B0); PG8_MMA(0, 1, At, B1); PG8_BAR; PG8_SCHED;
;             PG8_LDA(At, 0, 1); PG8_STAGE(PG8_SB(0, 0), b2, voffB); PG8_STAGE(PG8_SB(0, 1), b2 + hstep, voffB); PG8_STAGE(PG8_SA(0, 0), a2, PG8_OS(0));
;             PG8_WAIT_V(8); PG8_WAIT_L(0); PG8_BAR; PG8_MMA(1, 0, At, B0); PG8_MMA(1, 1, At, B1); PG8_BAR; PG8_SCHED;
;             PG8_LDB(B0, 1, 0); PG8_LDB(B1, 1, 1); PG8_SCHED; PG8_LDA(At, 1, 0); PG8_STAGE(PG8_SA(0, 1), a2 + hstepA, PG8_OS(1));
;             PG8_WAIT_V(8); PG8_WAIT_L(0); PG8_BAR; PG8_MMA(0, 0, At, B0); PG8_MMA(0, 1, At, B1); PG8_BAR; PG8_SCHED;
;             PG8_LDA(At, 1, 1); PG8_STAGE(PG8_SB(1, 0), b3, voffB); PG8_STAGE(PG8_SB(1, 1), b3 + hstep, voffB); PG8_STAGE(PG8_SA(1, 0), a3, PG8_OS(0));
;             PG8_WAIT_V(8); PG8_WAIT_L(0); PG8_BAR; PG8_MMA(1, 0, At, B0); PG8_MMA(1, 1, At, B1); PG8_BAR; PG8_SCHED;
	s_setprio 1
	s_waitcnt lgkmcnt(0)
	v_mfma_f32_16x16x32_bf16 v[62:65], v[122:125], v[196:199], v[62:65]
	v_mfma_f32_16x16x32_bf16 v[58:61], v[134:137], v[196:199], v[58:61]
	v_mfma_f32_16x16x32_bf16 v[54:57], v[122:125], v[204:207], v[54:57]
	v_mfma_f32_16x16x32_bf16 v[42:45], v[134:137], v[204:207], v[42:45]
	v_mfma_f32_16x16x32_bf16 v[38:41], v[122:125], v[212:215], v[38:41]
	v_mfma_f32_16x16x32_bf16 v[26:29], v[134:137], v[212:215], v[26:29]
	v_mfma_f32_16x16x32_bf16 v[22:25], v[122:125], v[220:223], v[22:25]
	v_mfma_f32_16x16x32_bf16 v[10:13], v[134:137], v[220:223], v[10:13]
	v_lshl_add_u64 v[230:231], s[58:59], 0, v[148:149]
	s_add_i32 m0, s60, 0x2000
	s_nop 0
	global_load_lds_dwordx4 v[230:231], off
	v_mfma_f32_16x16x32_bf16 v[62:65], v[126:129], v[200:203], v[62:65]
	v_mfma_f32_16x16x32_bf16 v[58:61], v[142:145], v[200:203], v[58:61]
	v_mfma_f32_16x16x32_bf16 v[54:57], v[126:129], v[208:211], v[54:57]
	v_mfma_f32_16x16x32_bf16 v[42:45], v[142:145], v[208:211], v[42:45]
	v_mfma_f32_16x16x32_bf16 v[38:41], v[126:129], v[216:219], v[38:41]
	v_mfma_f32_16x16x32_bf16 v[26:29], v[142:145], v[216:219], v[26:29]
	v_mfma_f32_16x16x32_bf16 v[22:25], v[126:129], v[224:227], v[22:25]
	v_mfma_f32_16x16x32_bf16 v[10:13], v[142:145], v[224:227], v[10:13]
	v_lshl_add_u64 v[230:231], s[24:25], 0, v[152:153]
	s_mov_b32 m0, s39
	s_nop 0
	global_load_lds_dwordx4 v[230:231], off
	s_setprio 0
	s_setprio 1
	v_mfma_f32_16x16x32_bf16 v[50:53], v[174:177], v[196:199], v[50:53]
	v_mfma_f32_16x16x32_bf16 v[46:49], v[188:191], v[196:199], v[46:49]
	v_mfma_f32_16x16x32_bf16 v[34:37], v[174:177], v[204:207], v[34:37]
	v_mfma_f32_16x16x32_bf16 v[30:33], v[188:191], v[204:207], v[30:33]
	v_mfma_f32_16x16x32_bf16 v[18:21], v[174:177], v[212:215], v[18:21]
	v_mfma_f32_16x16x32_bf16 v[14:17], v[188:191], v[212:215], v[14:17]
	v_mfma_f32_16x16x32_bf16 v[6:9], v[174:177], v[220:223], v[6:9]
	v_mfma_f32_16x16x32_bf16 v[2:5], v[188:191], v[220:223], v[2:5]
	s_mov_b32 m0, s41
	s_nop 0
	global_load_lds_dwordx4 v[232:233], off
	v_mfma_f32_16x16x32_bf16 v[50:53], v[178:181], v[200:203], v[50:53]
	v_mfma_f32_16x16x32_bf16 v[46:49], v[192:195], v[200:203], v[46:49]
	v_mfma_f32_16x16x32_bf16 v[34:37], v[178:181], v[208:211], v[34:37]
	v_mfma_f32_16x16x32_bf16 v[30:33], v[192:195], v[208:211], v[30:33]
	v_mfma_f32_16x16x32_bf16 v[18:21], v[178:181], v[216:219], v[18:21]
	v_mfma_f32_16x16x32_bf16 v[14:17], v[192:195], v[216:219], v[14:17]
	v_mfma_f32_16x16x32_bf16 v[6:9], v[178:181], v[224:227], v[6:9]
	v_mfma_f32_16x16x32_bf16 v[2:5], v[192:195], v[224:227], v[2:5]
	s_setprio 0
	s_barrier
	s_add_i32 s58, 0, 0x18000
	s_add_i32 s59, 0, 0x1c000
	v_add_u32_e32 v142, s58, v184
	v_add_u32_e32 v187, s59, v184
	ds_read_b128 v[122:125], v142
	ds_read_b128 v[126:129], v142 offset:1024
	ds_read_b128 v[134:137], v142 offset:2048
	ds_read_b128 v[142:145], v142 offset:3072
	ds_read_b128 v[174:177], v187
	ds_read_b128 v[178:181], v187 offset:1024
	ds_read_b128 v[188:191], v187 offset:2048
	ds_read_b128 v[192:195], v187 offset:3072
	s_add_u32 s24, s24, 0x40000
	s_addc_u32 s25, s25, 0
	s_mov_b32 m0, s43
	v_lshl_add_u64 v[234:235], s[24:25], 0, v[152:153]
	ds_read_b128 v[196:199], v186 offset:32768
	ds_read_b128 v[200:203], v186 offset:33792
	ds_read_b128 v[204:207], v186 offset:34816
	ds_read_b128 v[208:211], v186 offset:35840
	ds_read_b128 v[212:215], v186 offset:36864
	ds_read_b128 v[216:219], v186 offset:37888
	ds_read_b128 v[220:223], v186 offset:38912
	ds_read_b128 v[224:227], v186 offset:39936
	global_load_lds_dwordx4 v[234:235], off
	v_lshl_add_u64 v[234:235], s[24:25], 0, v[150:151]
	s_mov_b32 m0, s45
	s_nop 0
	global_load_lds_dwordx4 v[234:235], off
	s_waitcnt vmcnt(8)
	s_waitcnt lgkmcnt(0)
	s_barrier
	s_setprio 1
	s_waitcnt lgkmcnt(0)
	v_mfma_f32_16x16x32_bf16 v[138:141], v[122:125], v[196:199], v[138:141]
	v_mfma_f32_16x16x32_bf16 v[130:133], v[134:137], v[196:199], v[130:133]
	v_mfma_f32_16x16x32_bf16 v[118:121], v[122:125], v[204:207], v[118:121]
	v_mfma_f32_16x16x32_bf16 v[106:109], v[134:137], v[204:207], v[106:109]
	v_mfma_f32_16x16x32_bf16 v[102:105], v[122:125], v[212:215], v[102:105]
	v_mfma_f32_16x16x32_bf16 v[90:93], v[134:137], v[212:215], v[90:93]
	v_mfma_f32_16x16x32_bf16 v[86:89], v[122:125], v[220:223], v[86:89]
	v_mfma_f32_16x16x32_bf16 v[74:77], v[134:137], v[220:223], v[74:77]
	v_mfma_f32_16x16x32_bf16 v[138:141], v[126:129], v[200:203], v[138:141]
	v_mfma_f32_16x16x32_bf16 v[130:133], v[142:145], v[200:203], v[130:133]
	v_mfma_f32_16x16x32_bf16 v[118:121], v[126:129], v[208:211], v[118:121]
	v_mfma_f32_16x16x32_bf16 v[106:109], v[142:145], v[208:211], v[106:109]
	v_mfma_f32_16x16x32_bf16 v[102:105], v[126:129], v[216:219], v[102:105]
	v_mfma_f32_16x16x32_bf16 v[90:93], v[142:145], v[216:219], v[90:93]
	v_mfma_f32_16x16x32_bf16 v[86:89], v[126:129], v[224:227], v[86:89]
	v_mfma_f32_16x16x32_bf16 v[74:77], v[142:145], v[224:227], v[74:77]
	s_setprio 0
	s_setprio 1
	v_mfma_f32_16x16x32_bf16 v[114:117], v[174:177], v[196:199], v[114:117]
	v_mfma_f32_16x16x32_bf16 v[110:113], v[188:191], v[196:199], v[110:113]
	v_mfma_f32_16x16x32_bf16 v[98:101], v[174:177], v[204:207], v[98:101]
	v_mfma_f32_16x16x32_bf16 v[94:97], v[188:191], v[204:207], v[94:97]
	v_mfma_f32_16x16x32_bf16 v[82:85], v[174:177], v[212:215], v[82:85]
	v_mfma_f32_16x16x32_bf16 v[78:81], v[188:191], v[212:215], v[78:81]
	v_mfma_f32_16x16x32_bf16 v[70:73], v[174:177], v[220:223], v[70:73]
	v_mfma_f32_16x16x32_bf16 v[66:69], v[188:191], v[220:223], v[66:69]
	v_mfma_f32_16x16x32_bf16 v[114:117], v[178:181], v[200:203], v[114:117]
	v_mfma_f32_16x16x32_bf16 v[110:113], v[192:195], v[200:203], v[110:113]
	v_mfma_f32_16x16x32_bf16 v[98:101], v[178:181], v[208:211], v[98:101]
	v_mfma_f32_16x16x32_bf16 v[94:97], v[192:195], v[208:211], v[94:97]
	v_mfma_f32_16x16x32_bf16 v[82:85], v[178:181], v[216:219], v[82:85]
	v_mfma_f32_16x16x32_bf16 v[78:81], v[192:195], v[216:219], v[78:81]
	v_mfma_f32_16x16x32_bf16 v[70:73], v[178:181], v[224:227], v[70:73]
	v_mfma_f32_16x16x32_bf16 v[66:69], v[192:195], v[224:227], v[66:69]
	s_setprio 0
	s_barrier
; #define PG8_STAGE(bufoff, gbase, voff) do { _Pragma("unroll") for (int _i = 0; _i < 2; ++_i) \
;         __builtin_amdgcn_global_load_lds((const unsigned*)((const char*)(gbase) + (voff)[_i]), (PG8_LAS unsigned*)(lds + (bufoff) + ldsw + _i * 8192), 16, 0, 0); } while (0)
; #define PG8_WAIT_V(n) asm volatile("s_waitcnt vmcnt(" #n ")" ::: "memory")
; #define PG8_BAR __builtin_amdgcn_s_barrier()
; template <class Epi, class Sched, bool ALIGN_EPI = false, bool SP2 = false, bool GATHER = false>
; __device__ __forceinline__ void gemm_phase(PG8_LAS unsigned char* lds, const Gemm g, const Sched& S, const Epi& E, int tid_in, const int* rowsrc = nullptr, PG8_LAS int* idx_lds = nullptr) {
;     ...
;         for (int t = 0; t < nt; t += 2) {
;             const bool last = (t == nt - 2);
;             if constexpr (GATHER) {
; #pragma unroll
;                 for (int h_ = 0; h_ < 2; ++h_) { gS[h_][0] = last ? gN[h_][0] : gA[h_][0]; gS[h_][1] = last ? gN[h_][1] : gA[h_][1]; } }
;             const char* a1 = cA + (size_t)(t + 1) * kstep;
;             const char* a2 = last ? nA : cA + (size_t)(t + 2) * kstep; const char* b2 = last ? nB : cB + (size_t)(t + 2) * kstep;
;             const char* a3 = a2 + kstep; const char* b3 = b2 + kstep;
;             if (last && has_next) S.a_ready(nxt);
;             if constexpr (SP2) {
;             PG8_LDB(B0, 0, 0); PG8_LDB(B1, 0, 1); PG8_SCHED; PG8_LDA(At, 0, 0); PG8_STAGE(PG8_SA(1, 1), a1 + hstepA, PG8_OA(1));
;             PG8_WAIT_V(8); PG8_WAIT_L(0); PG8_BAR; PG8_MMA(0, 0, At, B0); PG8_MMA(0, 1, At, B1); PG8_BAR; PG8_SCHED;
;             PG8_LDA(At, 0, 1); PG8_STAGE(PG8_SB(0, 0), b2, voffB); PG8_STAGE(PG8_SB(0, 1), b2 + hstep, voffB); PG8_STAGE(PG8_SA(0, 0), a2, PG8_OS(0));
;             PG8_WAIT_V(8); PG8_WAIT_L(0); PG8_BAR; PG8_MMA(1, 0, At, B0); PG8_MMA(1, 1, At, B1); PG8_BAR; PG8_SCHED;
;             PG8_LDB(B0, 1, 0); PG8_LDB(B1, 1, 1); PG8_SCHED; PG8_LDA(At, 1, 0); PG8_STAGE(PG8_SA(0, 1), a2 + hstepA, PG8_OS(1));
;             PG8_WAIT_V(8); PG8_WAIT_L(0); PG8_BAR; PG8_MMA(0, 0, At, B0); PG8_MMA(0, 1, At, B1); PG8_BAR; PG8_SCHED;
;             PG8_LDA(At, 1, 1); PG8_STAGE(PG8_SB(1, 0), b3, voffB); PG8_STAGE(PG8_SB(1, 1), b3 + hstep, voffB); PG8_STAGE(PG8_SA(1, 0), a3, PG8_OS(0));
;             PG8_WAIT_V(8); PG8_WAIT_L(0); PG8_BAR; PG8_MMA(1, 0, At, B0); PG8_MMA(1, 1, At, B1); PG8_BAR; PG8_SCHED;
	s_add_i32 s24, s58, s38
	v_lshl_add_u64 v[182:183], v[182:183], 0, s[10:11]
	s_mov_b32 m0, s24
	ds_read_b128 v[196:199], v186 offset:49152
	ds_read_b128 v[200:203], v186 offset:50176
	ds_read_b128 v[204:207], v186 offset:51200
	ds_read_b128 v[208:211], v186 offset:52224
	ds_read_b128 v[212:215], v186 offset:53248
	ds_read_b128 v[216:219], v186 offset:54272
	ds_read_b128 v[220:223], v186 offset:55296
	ds_read_b128 v[224:227], v186 offset:56320
	global_load_lds_dwordx4 v[182:183], off
	s_add_i32 m0, s24, 0x2000
	s_add_u32 s22, s22, 0x40080
	v_lshl_add_u64 v[182:183], v[228:229], 0, s[10:11]
	s_addc_u32 s23, s23, 0
	s_add_i32 s24, s59, s38
	global_load_lds_dwordx4 v[182:183], off
	v_lshl_add_u64 v[182:183], s[22:23], 0, v[0:1]
	s_mov_b32 m0, s24
	s_nop 0
	global_load_lds_dwordx4 v[182:183], off
	s_waitcnt vmcnt(5)
	s_waitcnt lgkmcnt(0)
	s_barrier
	s_setprio 1
	s_waitcnt lgkmcnt(0)
	v_mfma_f32_16x16x32_bf16 v[62:65], v[122:125], v[196:199], v[62:65]
	v_mfma_f32_16x16x32_bf16 v[58:61], v[134:137], v[196:199], v[58:61]
	v_mfma_f32_16x16x32_bf16 v[54:57], v[122:125], v[204:207], v[54:57]
	v_mfma_f32_16x16x32_bf16 v[42:45], v[134:137], v[204:207], v[42:45]
	v_mfma_f32_16x16x32_bf16 v[38:41], v[122:125], v[212:215], v[38:41]
	v_mfma_f32_16x16x32_bf16 v[26:29], v[134:137], v[212:215], v[26:29]
	v_mfma_f32_16x16x32_bf16 v[22:25], v[122:125], v[220:223], v[22:25]
	v_mfma_f32_16x16x32_bf16 v[10:13], v[134:137], v[220:223], v[10:13]
	v_lshl_add_u64 v[182:183], s[22:23], 0, v[148:149]
	s_add_i32 m0, s24, 0x2000
	s_nop 0
	global_load_lds_dwordx4 v[182:183], off
	v_mfma_f32_16x16x32_bf16 v[62:65], v[126:129], v[200:203], v[62:65]
	v_mfma_f32_16x16x32_bf16 v[58:61], v[142:145], v[200:203], v[58:61]
	v_mfma_f32_16x16x32_bf16 v[54:57], v[126:129], v[208:211], v[54:57]
	v_mfma_f32_16x16x32_bf16 v[42:45], v[142:145], v[208:211], v[42:45]
	v_mfma_f32_16x16x32_bf16 v[38:41], v[126:129], v[216:219], v[38:41]
	v_mfma_f32_16x16x32_bf16 v[26:29], v[142:145], v[216:219], v[26:29]
	v_mfma_f32_16x16x32_bf16 v[22:25], v[126:129], v[224:227], v[22:25]
	v_mfma_f32_16x16x32_bf16 v[10:13], v[142:145], v[224:227], v[10:13]
	v_lshl_add_u64 v[182:183], v[230:231], 0, s[10:11]
	s_mov_b32 m0, s52
	s_nop 0
	global_load_lds_dwordx4 v[182:183], off
	s_setprio 0
	s_setprio 1
	v_mfma_f32_16x16x32_bf16 v[50:53], v[174:177], v[196:199], v[50:53]
	v_mfma_f32_16x16x32_bf16 v[46:49], v[188:191], v[196:199], v[46:49]
	v_mfma_f32_16x16x32_bf16 v[34:37], v[174:177], v[204:207], v[34:37]
	v_mfma_f32_16x16x32_bf16 v[30:33], v[188:191], v[204:207], v[30:33]
	v_mfma_f32_16x16x32_bf16 v[18:21], v[174:177], v[212:215], v[18:21]
	v_mfma_f32_16x16x32_bf16 v[14:17], v[188:191], v[212:215], v[14:17]
	v_mfma_f32_16x16x32_bf16 v[6:9], v[174:177], v[220:223], v[6:9]
	v_mfma_f32_16x16x32_bf16 v[2:5], v[188:191], v[220:223], v[2:5]
	v_lshl_add_u64 v[182:183], v[232:233], 0, s[10:11]
	s_mov_b32 m0, s53
	s_nop 0
	global_load_lds_dwordx4 v[182:183], off
	v_mfma_f32_16x16x32_bf16 v[50:53], v[178:181], v[200:203], v[50:53]
	v_mfma_f32_16x16x32_bf16 v[46:49], v[192:195], v[200:203], v[46:49]
	v_mfma_f32_16x16x32_bf16 v[34:37], v[178:181], v[208:211], v[34:37]
	v_mfma_f32_16x16x32_bf16 v[30:33], v[192:195], v[208:211], v[30:33]
	v_mfma_f32_16x16x32_bf16 v[18:21], v[178:181], v[216:219], v[18:21]
	v_mfma_f32_16x16x32_bf16 v[14:17], v[192:195], v[216:219], v[14:17]
	v_mfma_f32_16x16x32_bf16 v[6:9], v[178:181], v[224:227], v[6:9]
	v_mfma_f32_16x16x32_bf16 v[2:5], v[192:195], v[224:227], v[2:5]
	s_setprio 0
	s_barrier
	s_add_i32 s57, s57, 2
	s_add_u32 s20, s20, 0x100
	s_addc_u32 s21, s21, 0
	s_add_u32 s55, s55, 0x100
	s_addc_u32 s56, s56, 0
	s_cmp_gt_u32 s57, 13
	s_cbranch_scc0 .LBB0_1101
	s_and_b64 vcc, exec, s[4:5]
	s_cbranch_vccz .LBB0_1104
	s_barrier

; __device__ __forceinline__ void mf_load(MfRow& R, int m, const bf16* KVPRE, const bf16* DOWN, const float* ca, const float* sa, int lane, int h, int p) {
;     const bf16* dr = DOWN + (size_t)m * 1024;
;     R.cq = *(const v4u*)(dr + 8 * lane); R.ckv = *(const v2u*)(dr + 512 + 4 * lane);
;     const bf16* s = KVPRE + (size_t)m * 2048 + h * 128; const bf16* kr = dr + 768;
;     { const v4u* pp = (const v4u*)(s + 16 * p); R.k0 = pp[0]; R.k1 = pp[1]; R.kr0 = *(const v2u*)(kr + 4 * p); R.kr1 = *(const v2u*)(kr + 16 + 4 * p); }
;     { const v4u* vs = (const v4u*)(s + 64 + 16 * p); R.v0 = vs[0]; R.v1 = vs[1]; }
;     if (m < NLAT) { const int t = m & 4095; R.cs = *(const f32x4*)(ca + t * 16 + 4 * p); R.sn = *(const f32x4*)(sa + t * 16 + 4 * p); }
;     else { R.cs = (f32x4){1.f, 1.f, 1.f, 1.f}; R.sn = (f32x4){0.f, 0.f, 0.f, 0.f}; }
; }
; __device__ __forceinline__ void mla_finish_phase(Frame& F, const InPtrs& A, int j) {
;     const int gw = F.vcu * NWAVES + F.wave, NGW = F.G * NWAVES, lane = F.lane, h = lane >> 2, p = lane & 3;
;     const bf16* DOWN = (const bf16*)(F.ws + R_DOWN); const bf16* KVPRE = (const bf16*)(F.ws + R_KVPRE);
;     bf16* MK = (bf16*)(F.ws + R_MK); bf16* MV = (bf16*)(F.ws + R_MV); float* RQ = (float*)(F.ws + WS_RQ);
;     const float* ca = (const float*)(F.ws + WS_ROPEA); const float* sa = ca + 4096 * 16;
;     float gk[24];
;     { const float* k = A[I_MLA_KN] + j * 96;
; #pragma unroll
;       for (int i = 0; i < 16; ++i) gk[i] = k[16 * p + i];
; #pragma unroll
;       for (int i = 0; i < 4; ++i) { gk[16 + i] = k[64 + 4 * p + i]; gk[20 + i] = k[80 + 4 * p + i]; } }
;     MfRow N;
;     if (gw < MROWS) mf_load(N, gw, KVPRE, DOWN, ca, sa, lane, h, p);
.LBB0_1327:
	s_andn2_b64 vcc, exec, s[0:1]
	s_cbranch_vccnz .LBB0_1396
	v_readlane_b32 s0, v251, 12
	v_mbcnt_lo_u32_b32 v0, -1, 0
	v_mbcnt_hi_u32_b32 v0, -1, v0
	s_mov_b64 s[6:7], 0
	v_readlane_b32 s2, v251, 2
	v_add_u32_e32 v45, s0, v0
	v_readlane_b32 s1, v251, 3
	s_lshl_b32 s1, s1, 3
	v_readfirstlane_b32 s0, v45
	s_ashr_i32 s0, s0, 6
	s_add_i32 s20, s1, s0
	v_readlane_b32 s0, v252, 21
	s_cmp_gt_i32 s20, 0x87ff
	s_nop 0
	v_mov_b32_e32 v0, s0
	ds_read_b32 v0, v0
	v_readlane_b32 s0, v252, 22
	s_waitcnt lgkmcnt(0)
	v_readfirstlane_b32 s8, v0
	v_mov_b32_e32 v0, s0
	ds_read_b32 v0, v0
	s_waitcnt lgkmcnt(0)
	v_readfirstlane_b32 s9, v0
	s_cbranch_scc1 .LBB0_1340
	v_readlane_b32 s12, v251, 4
	v_readlane_b32 s14, v251, 6
	v_readlane_b32 s15, v251, 7
	s_add_u32 s4, s14, s6
	v_readlane_b32 s13, v251, 5
	s_addc_u32 s5, s15, s7
	s_add_u32 s0, s4, 0x200000
	v_readlane_b32 s12, v252, 34
	s_addc_u32 s1, s5, 0
	v_readlane_b32 s13, v252, 35
	s_and_b64 s[12:13], s[12:13], exec
	s_cselect_b32 s12, 0x180, 0
	s_add_u32 s14, s4, 0x240000
	s_addc_u32 s15, s5, 0
	s_waitcnt vmcnt(0)
	v_and_b32_e32 v34, 3, v45
	s_add_u32 s8, s8, s12
	s_addc_u32 s9, s9, 0
	v_lshlrev_b32_e32 v0, 6, v34
	s_ashr_i32 s21, s20, 31
	v_lshlrev_b32_e32 v50, 4, v34
	global_load_dwordx4 v[2:5], v0, s[8:9] offset:48
	global_load_dwordx4 v[6:9], v0, s[8:9] offset:32
	global_load_dwordx4 v[10:13], v0, s[8:9] offset:16
	global_load_dwordx4 v[14:17], v0, s[8:9]
	global_load_dwordx4 v[18:21], v50, s[8:9] offset:256
	global_load_dwordx4 v[22:25], v50, s[8:9] offset:320
	s_lshl_b64 s[8:9], s[20:21], 12
	v_bfe_u32 v80, v45, 2, 4
	s_add_u32 s8, s4, s8
	s_addc_u32 s9, s5, s9
	s_lshl_b64 s[12:13], s[20:21], 11
	v_lshlrev_b32_e32 v0, 8, v80
	s_add_u32 s12, s4, s12
	v_lshl_add_u64 v[26:27], s[8:9], 0, v[0:1]
	v_lshlrev_b32_e32 v0, 5, v34
	s_addc_u32 s13, s5, s13
	v_lshl_add_u64 v[26:27], v[26:27], 0, v[0:1]
	s_mov_b64 s[8:9], 0x1ba00000
	v_and_b32_e32 v47, 63, v45
	s_add_u32 s12, s12, 0xdc00000
	v_lshl_add_u64 v[30:31], v[26:27], 0, s[8:9]
	v_add_co_u32_e32 v26, vcc, 0x1ba00000, v26
	s_addc_u32 s13, s13, 0
	v_lshlrev_b32_e32 v44, 3, v34
	v_lshlrev_b32_e32 v46, 4, v47
	v_addc_co_u32_e32 v27, vcc, 0, v27, vcc
	v_lshlrev_b32_e32 v42, 3, v47
	global_load_dwordx4 v[76:79], v46, s[12:13] nt
	global_load_dwordx2 v[110:111], v42, s[12:13] offset:1024 nt
	global_load_dwordx2 v[108:109], v44, s[12:13] offset:1536 nt
	global_load_dwordx2 v[106:107], v44, s[12:13] offset:1568 nt
	global_load_dwordx4 v[72:75], v[26:27], off nt
	s_nop 0
	global_load_dwordx4 v[26:29], v[30:31], off offset:144 nt
	global_load_dwordx4 v[68:71], v[30:31], off offset:16 nt
	s_nop 0
	global_load_dwordx4 v[30:33], v[30:31], off offset:128 nt
	v_lshlrev_b32_e32 v81, 2, v34
	s_cmpk_gt_i32 s20, 0x7fff
	v_lshlrev_b32_e32 v48, 2, v81
	s_cbranch_scc1 .LBB0_1331
	s_lshl_b32 s8, s20, 6
	s_and_b32 s12, s8, 0x3ffc0
	s_add_u32 s8, s0, s12
	s_addc_u32 s9, s1, 0
	s_add_u32 s12, s14, s12
	s_addc_u32 s13, s15, 0
	global_load_dwordx4 v[38:41], v48, s[8:9]
	global_load_dwordx4 v[34:37], v48, s[12:13]
	s_waitcnt vmcnt(1)
	v_mov_b32_e32 v96, v39
	v_mov_b32_e32 v39, v40
	s_waitcnt vmcnt(0)
	v_mov_b32_e32 v94, v35
	v_mov_b32_e32 v35, v36
	v_mov_b32_e32 v95, v37
	v_mov_b32_e32 v97, v41
	s_branch .LBB0_1332

; __device__ __forceinline__ void mf_load(MfRow& R, int m, const bf16* KVPRE, const bf16* DOWN, const float* ca, const float* sa, int lane, int h, int p) {
;     const bf16* dr = DOWN + (size_t)m * 1024;
;     R.cq = *(const v4u*)(dr + 8 * lane); R.ckv = *(const v2u*)(dr + 512 + 4 * lane);
;     const bf16* s = KVPRE + (size_t)m * 2048 + h * 128; const bf16* kr = dr + 768;
;     { const v4u* pp = (const v4u*)(s + 16 * p); R.k0 = pp[0]; R.k1 = pp[1]; R.kr0 = *(const v2u*)(kr + 4 * p); R.kr1 = *(const v2u*)(kr + 16 + 4 * p); }
;     { const v4u* vs = (const v4u*)(s + 64 + 16 * p); R.v0 = vs[0]; R.v1 = vs[1]; }
;     if (m < NLAT) { const int t = m & 4095; R.cs = *(const f32x4*)(ca + t * 16 + 4 * p); R.sn = *(const f32x4*)(sa + t * 16 + 4 * p); }
;     else { R.cs = (f32x4){1.f, 1.f, 1.f, 1.f}; R.sn = (f32x4){0.f, 0.f, 0.f, 0.f}; }
; }
; __device__ __forceinline__ void mla_finish_phase(Frame& F, const InPtrs& A, int j) {
;     const int gw = F.vcu * NWAVES + F.wave, NGW = F.G * NWAVES, lane = F.lane, h = lane >> 2, p = lane & 3;
;     const bf16* DOWN = (const bf16*)(F.ws + R_DOWN); const bf16* KVPRE = (const bf16*)(F.ws + R_KVPRE);
;     bf16* MK = (bf16*)(F.ws + R_MK); bf16* MV = (bf16*)(F.ws + R_MV); float* RQ = (float*)(F.ws + WS_RQ);
;     const float* ca = (const float*)(F.ws + WS_ROPEA); const float* sa = ca + 4096 * 16;
;     float gk[24];
;     { const float* k = A[I_MLA_KN] + j * 96;
; #pragma unroll
;       for (int i = 0; i < 16; ++i) gk[i] = k[16 * p + i];
; #pragma unroll
;       for (int i = 0; i < 4; ++i) { gk[16 + i] = k[64 + 4 * p + i]; gk[20 + i] = k[80 + 4 * p + i]; } }
;     MfRow N;
;     if (gw < MROWS) mf_load(N, gw, KVPRE, DOWN, ca, sa, lane, h, p);
;     for (int m = gw; m < MROWS; m += NGW) {
;         const MfRow R = N;
;         { const int mn = m + NGW; if (mn < MROWS) mf_load(N, mn, KVPRE, DOWN, ca, sa, lane, h, p); }
.LBB0_1334:
	s_add_i32 s9, s20, s8
	s_cmp_gt_i32 s9, 0x87ff
	s_cselect_b64 s[22:23], -1, 0
	s_and_b64 vcc, exec, s[22:23]
	v_mov_b32_e32 v60, v38
	v_mov_b32_e32 v61, v96
	v_mov_b32_e32 v62, v39
	v_mov_b32_e32 v63, v97
	v_mov_b32_e32 v64, v34
	v_mov_b32_e32 v65, v94
	v_mov_b32_e32 v66, v35
	v_mov_b32_e32 v67, v95
	s_cbranch_vccnz .LBB0_1338
	v_lshl_add_u64 v[52:53], v[98:99], 0, s[6:7]
	v_add_co_u32_e32 v52, vcc, 0xdc00000, v52
	v_lshl_add_u64 v[40:41], v[22:23], 0, s[6:7]
	v_lshl_add_u64 v[44:45], v[92:93], 0, s[6:7]
	v_lshl_add_u64 v[56:57], v[90:91], 0, s[6:7]
	v_addc_co_u32_e32 v53, vcc, 0, v53, vcc
	global_load_dwordx4 v[40:43], v[40:41], off nt
	s_cmpk_gt_i32 s9, 0x7fff
	global_load_dwordx2 v[100:101], v[44:45], off nt
	s_nop 0
	global_load_dwordx4 v[44:47], v[56:57], off offset:-112 nt
	global_load_dwordx4 v[48:51], v[56:57], off offset:-128 nt
	global_load_dwordx2 v[104:105], v[52:53], off offset:1536 nt
	global_load_dwordx2 v[102:103], v[52:53], off offset:1568 nt
	s_nop 0
	global_load_dwordx4 v[52:55], v[56:57], off offset:16 nt
	s_nop 0
	global_load_dwordx4 v[56:59], v[56:57], off nt
	s_cbranch_scc1 .LBB0_1337
	s_and_b32 s2, s27, 0xfff0
	s_lshl_b32 s2, s2, 2
	v_lshl_add_u64 v[60:61], v[82:83], 0, s[2:3]
	v_lshl_add_u64 v[64:65], v[36:37], 0, s[2:3]
	global_load_dwordx4 v[60:63], v[60:61], off
	s_nop 0
	global_load_dwordx4 v[64:67], v[64:65], off
	s_branch .LBB0_1338

; #define PG8_STAGE(bufoff, gbase, voff) do { _Pragma("unroll") for (int _i = 0; _i < 2; ++_i) \
;         __builtin_amdgcn_global_load_lds((const unsigned*)((const char*)(gbase) + (voff)[_i]), (PG8_LAS unsigned*)(lds + (bufoff) + ldsw + _i * 8192), 16, 0, 0); } while (0)
; #define PG8_WAIT_V(n) asm volatile("s_waitcnt vmcnt(" #n ")" ::: "memory")
; #define PG8_BAR __builtin_amdgcn_s_barrier()
; template <class Epi, class Sched, bool ALIGN_EPI = false, bool SP2 = false, bool GATHER = false>
; __device__ __forceinline__ void gemm_phase(PG8_LAS unsigned char* lds, const Gemm g, const Sched& S, const Epi& E, int tid_in, const int* rowsrc = nullptr, PG8_LAS int* idx_lds = nullptr) {
;     ...
;         for (int t = 0; t < nt; t += 2) {
;             const bool last = (t == nt - 2);
;             if constexpr (GATHER) {
; #pragma unroll
;                 for (int h_ = 0; h_ < 2; ++h_) { gS[h_][0] = last ? gN[h_][0] : gA[h_][0]; gS[h_][1] = last ? gN[h_][1] : gA[h_][1]; } }
;             const char* a1 = cA + (size_t)(t + 1) * kstep;
;             const char* a2 = last ? nA : cA + (size_t)(t + 2) * kstep; const char* b2 = last ? nB : cB + (size_t)(t + 2) * kstep;
;             const char* a3 = a2 + kstep; const char* b3 = b2 + kstep;
;             if (last && has_next) S.a_ready(nxt);
;             if constexpr (SP2) {
;             PG8_LDB(B0, 0, 0); PG8_LDB(B1, 0, 1); PG8_SCHED; PG8_LDA(At, 0, 0); PG8_STAGE(PG8_SA(1, 1), a1 + hstepA, PG8_OA(1));
;             PG8_WAIT_V(8); PG8_WAIT_L(0); PG8_BAR; PG8_MMA(0, 0, At, B0); PG8_MMA(0, 1, At, B1); PG8_BAR; PG8_SCHED;
;             PG8_LDA(At, 0, 1); PG8_STAGE(PG8_SB(0, 0), b2, voffB); PG8_STAGE(PG8_SB(0, 1), b2 + hstep, voffB); PG8_STAGE(PG8_SA(0, 0), a2, PG8_OS(0));
;             PG8_WAIT_V(8); PG8_WAIT_L(0); PG8_BAR; PG8_MMA(1, 0, At, B0); PG8_MMA(1, 1, At, B1); PG8_BAR; PG8_SCHED;
;             PG8_LDB(B0, 1, 0); PG8_LDB(B1, 1, 1); PG8_SCHED; PG8_LDA(At, 1, 0); PG8_STAGE(PG8_SA(0, 1), a2 + hstepA, PG8_OS(1));
;             PG8_WAIT_V(8); PG8_WAIT_L(0); PG8_BAR; PG8_MMA(0, 0, At, B0); PG8_MMA(0, 1, At, B1); PG8_BAR; PG8_SCHED;
;             PG8_LDA(At, 1, 1); PG8_STAGE(PG8_SB(1, 0), b3, voffB); PG8_STAGE(PG8_SB(1, 1), b3 + hstep, voffB); PG8_STAGE(PG8_SA(1, 0), a3, PG8_OS(0));
;             PG8_WAIT_V(8); PG8_WAIT_L(0); PG8_BAR; PG8_MMA(1, 0, At, B0); PG8_MMA(1, 1, At, B1); PG8_BAR; PG8_SCHED;
.LBB0_2005:
	s_add_u32 s28, s26, 0xfffc0080
	s_addc_u32 s29, s27, -1
	s_add_i32 s58, 0, 0x10000
	s_cmp_eq_u32 s57, 12
	s_cselect_b32 s31, s13, s29
	s_cselect_b32 s30, s23, s28
	v_add_u32_e32 v0, s58, v151
	s_cselect_b32 s29, s15, s56
	s_cselect_b32 s28, s43, s55
	s_add_i32 s60, 0, 0x14000
	ds_read_b128 v[142:145], v0
	ds_read_b128 v[154:157], v0 offset:1024
	ds_read_b128 v[158:161], v0 offset:2048
	ds_read_b128 v[162:165], v0 offset:3072
	v_add_u32_e32 v0, s60, v151
	ds_read_b128 v[166:169], v0
	ds_read_b128 v[170:173], v0 offset:1024
	ds_read_b128 v[174:177], v0 offset:2048
	ds_read_b128 v[178:181], v0 offset:3072
	v_lshl_add_u64 v[148:149], s[26:27], 0, v[138:139]
	s_add_i32 m0, s25, 0xc000
	ds_read_b128 v[182:185], v153
	ds_read_b128 v[186:189], v153 offset:1024
	ds_read_b128 v[190:193], v153 offset:2048
	ds_read_b128 v[194:197], v153 offset:3072
	ds_read_b128 v[198:201], v153 offset:4096
	ds_read_b128 v[202:205], v153 offset:5120
	ds_read_b128 v[206:209], v153 offset:6144
	ds_read_b128 v[210:213], v153 offset:7168
	global_load_lds_dwordx4 v[148:149], off
	v_lshl_add_u64 v[148:149], s[26:27], 0, v[140:141]
	s_add_i32 m0, s25, 0xe000
	s_nop 0
	global_load_lds_dwordx4 v[148:149], off
	s_waitcnt vmcnt(8)
	s_waitcnt lgkmcnt(0)
	s_barrier
	s_setprio 1
	s_waitcnt lgkmcnt(0)
	v_mfma_f32_16x16x32_bf16 v[126:129], v[142:145], v[182:185], v[126:129]
	v_mfma_f32_16x16x32_bf16 v[122:125], v[158:161], v[182:185], v[122:125]
	v_mfma_f32_16x16x32_bf16 v[110:113], v[142:145], v[190:193], v[110:113]
	v_mfma_f32_16x16x32_bf16 v[106:109], v[158:161], v[190:193], v[106:109]
	v_mfma_f32_16x16x32_bf16 v[94:97], v[142:145], v[198:201], v[94:97]
	v_mfma_f32_16x16x32_bf16 v[90:93], v[158:161], v[198:201], v[90:93]
	v_mfma_f32_16x16x32_bf16 v[78:81], v[142:145], v[206:209], v[78:81]
	v_mfma_f32_16x16x32_bf16 v[74:77], v[158:161], v[206:209], v[74:77]
	v_mfma_f32_16x16x32_bf16 v[126:129], v[154:157], v[186:189], v[126:129]
	v_mfma_f32_16x16x32_bf16 v[122:125], v[162:165], v[186:189], v[122:125]
	v_mfma_f32_16x16x32_bf16 v[110:113], v[154:157], v[194:197], v[110:113]
	v_mfma_f32_16x16x32_bf16 v[106:109], v[162:165], v[194:197], v[106:109]
	v_mfma_f32_16x16x32_bf16 v[94:97], v[154:157], v[202:205], v[94:97]
	v_mfma_f32_16x16x32_bf16 v[90:93], v[162:165], v[202:205], v[90:93]
	v_mfma_f32_16x16x32_bf16 v[78:81], v[154:157], v[210:213], v[78:81]
	v_mfma_f32_16x16x32_bf16 v[74:77], v[162:165], v[210:213], v[74:77]
	s_setprio 0
	s_setprio 1
	v_mfma_f32_16x16x32_bf16 v[118:121], v[166:169], v[182:185], v[118:121]
	v_mfma_f32_16x16x32_bf16 v[114:117], v[174:177], v[182:185], v[114:117]
	v_mfma_f32_16x16x32_bf16 v[102:105], v[166:169], v[190:193], v[102:105]
	v_mfma_f32_16x16x32_bf16 v[98:101], v[174:177], v[190:193], v[98:101]
	v_mfma_f32_16x16x32_bf16 v[86:89], v[166:169], v[198:201], v[86:89]
	v_mfma_f32_16x16x32_bf16 v[82:85], v[174:177], v[198:201], v[82:85]
	v_mfma_f32_16x16x32_bf16 v[70:73], v[166:169], v[206:209], v[70:73]
	v_mfma_f32_16x16x32_bf16 v[66:69], v[174:177], v[206:209], v[66:69]
	v_mfma_f32_16x16x32_bf16 v[118:121], v[170:173], v[186:189], v[118:121]
	v_mfma_f32_16x16x32_bf16 v[114:117], v[178:181], v[186:189], v[114:117]
	v_mfma_f32_16x16x32_bf16 v[102:105], v[170:173], v[194:197], v[102:105]
	v_mfma_f32_16x16x32_bf16 v[98:101], v[178:181], v[194:197], v[98:101]
	v_mfma_f32_16x16x32_bf16 v[86:89], v[170:173], v[202:205], v[86:89]
	v_mfma_f32_16x16x32_bf16 v[82:85], v[178:181], v[202:205], v[82:85]
	v_mfma_f32_16x16x32_bf16 v[70:73], v[170:173], v[210:213], v[70:73]
	v_mfma_f32_16x16x32_bf16 v[66:69], v[178:181], v[210:213], v[66:69]
	s_setprio 0
	s_barrier
	s_add_i32 s58, s58, s44
	v_lshl_add_u64 v[148:149], s[28:29], 0, v[134:135]
	s_mov_b32 m0, s58
	ds_read_b128 v[182:185], v153 offset:16384
	ds_read_b128 v[186:189], v153 offset:17408
	ds_read_b128 v[190:193], v153 offset:18432
	ds_read_b128 v[194:197], v153 offset:19456
	ds_read_b128 v[198:201], v153 offset:20480
	ds_read_b128 v[202:205], v153 offset:21504
	ds_read_b128 v[206:209], v153 offset:22528
	ds_read_b128 v[210:213], v153 offset:23552
	global_load_lds_dwordx4 v[148:149], off
	s_add_i32 m0, s58, 0x2000
	s_add_u32 s58, s28, 0x40000
	v_lshl_add_u64 v[214:215], s[28:29], 0, v[130:131]
	s_addc_u32 s59, s29, 0
	s_add_i32 s60, s60, s44
	global_load_lds_dwordx4 v[214:215], off
	v_lshl_add_u64 v[216:217], s[58:59], 0, v[134:135]
	s_mov_b32 m0, s60
	v_lshl_add_u64 v[218:219], s[30:31], 0, v[132:133]
	global_load_lds_dwordx4 v[216:217], off
	s_waitcnt vmcnt(5)
	s_waitcnt lgkmcnt(0)
	s_barrier
; #define PG8_STAGE(bufoff, gbase, voff) do { _Pragma("unroll") for (int _i = 0; _i < 2; ++_i) \
;         __builtin_amdgcn_global_load_lds((const unsigned*)((const char*)(gbase) + (voff)[_i]), (PG8_LAS unsigned*)(lds + (bufoff) + ldsw + _i * 8192), 16, 0, 0); } while (0)
; #define PG8_WAIT_V(n) asm volatile("s_waitcnt vmcnt(" #n ")" ::: "memory")
; #define PG8_BAR __builtin_amdgcn_s_barrier()
; template <class Epi, class Sched, bool ALIGN_EPI = false, bool SP2 = false, bool GATHER = false>
; __device__ __forceinline__ void gemm_phase(PG8_LAS unsigned char* lds, const Gemm g, const Sched& S, const Epi& E, int tid_in, const int* rowsrc = nullptr, PG8_LAS int* idx_lds = nullptr) {
;     ...
;         for (int t = 0; t < nt; t += 2) {
;             const bool last = (t == nt - 2);
;             if constexpr (GATHER) {
; #pragma unroll
;                 for (int h_ = 0; h_ < 2; ++h_) { gS[h_][0] = last ? gN[h_][0] : gA[h_][0]; gS[h_][1] = last ? gN[h_][1] : gA[h_][1]; } }
;             const char* a1 = cA + (size_t)(t + 1) * kstep;
;             const char* a2 = last ? nA : cA + (size_t)(t + 2) * kstep; const char* b2 = last ? nB : cB + (size_t)(t + 2) * kstep;
;             const char* a3 = a2 + kstep; const char* b3 = b2 + kstep;
;             if (last && has_next) S.a_ready(nxt);
;             if constexpr (SP2) {
;             PG8_LDB(B0, 0, 0); PG8_LDB(B1, 0, 1); PG8_SCHED; PG8_LDA(At, 0, 0); PG8_STAGE(PG8_SA(1, 1), a1 + hstepA, PG8_OA(1));
;             PG8_WAIT_V(8); PG8_WAIT_L(0); PG8_BAR; PG8_MMA(0, 0, At, B0); PG8_MMA(0, 1, At, B1); PG8_BAR; PG8_SCHED;
;             PG8_LDA(At, 0, 1); PG8_STAGE(PG8_SB(0, 0), b2, voffB); PG8_STAGE(PG8_SB(0, 1), b2 + hstep, voffB); PG8_STAGE(PG8_SA(0, 0), a2, PG8_OS(0));
;             PG8_WAIT_V(8); PG8_WAIT_L(0); PG8_BAR; PG8_MMA(1, 0, At, B0); PG8_MMA(1, 1, At, B1); PG8_BAR; PG8_SCHED;
;             PG8_LDB(B0, 1, 0); PG8_LDB(B1, 1, 1); PG8_SCHED; PG8_LDA(At, 1, 0); PG8_STAGE(PG8_SA(0, 1), a2 + hstepA, PG8_OS(1));
;             PG8_WAIT_V(8); PG8_WAIT_L(0); PG8_BAR; PG8_MMA(0, 0, At, B0); PG8_MMA(0, 1, At, B1); PG8_BAR; PG8_SCHED;
;             PG8_LDA(At, 1, 1); PG8_STAGE(PG8_SB(1, 0), b3, voffB); PG8_STAGE(PG8_SB(1, 1), b3 + hstep, voffB); PG8_STAGE(PG8_SA(1, 0), a3, PG8_OS(0));
;             PG8_WAIT_V(8); PG8_WAIT_L(0); PG8_BAR; PG8_MMA(1, 0, At, B0); PG8_MMA(1, 1, At, B1); PG8_BAR; PG8_SCHED;
	s_setprio 1
	s_waitcnt lgkmcnt(0)
	v_mfma_f32_16x16x32_bf16 v[62:65], v[142:145], v[182:185], v[62:65]
	v_mfma_f32_16x16x32_bf16 v[58:61], v[158:161], v[182:185], v[58:61]
	v_mfma_f32_16x16x32_bf16 v[46:49], v[142:145], v[190:193], v[46:49]
	v_mfma_f32_16x16x32_bf16 v[42:45], v[158:161], v[190:193], v[42:45]
	v_mfma_f32_16x16x32_bf16 v[30:33], v[142:145], v[198:201], v[30:33]
	v_mfma_f32_16x16x32_bf16 v[26:29], v[158:161], v[198:201], v[26:29]
	v_mfma_f32_16x16x32_bf16 v[14:17], v[142:145], v[206:209], v[14:17]
	v_mfma_f32_16x16x32_bf16 v[10:13], v[158:161], v[206:209], v[10:13]
	v_lshl_add_u64 v[216:217], s[58:59], 0, v[130:131]
	s_add_i32 m0, s60, 0x2000
	s_nop 0
	global_load_lds_dwordx4 v[216:217], off
	v_mfma_f32_16x16x32_bf16 v[62:65], v[154:157], v[186:189], v[62:65]
	v_mfma_f32_16x16x32_bf16 v[58:61], v[162:165], v[186:189], v[58:61]
	v_mfma_f32_16x16x32_bf16 v[46:49], v[154:157], v[194:197], v[46:49]
	v_mfma_f32_16x16x32_bf16 v[42:45], v[162:165], v[194:197], v[42:45]
	v_mfma_f32_16x16x32_bf16 v[30:33], v[154:157], v[202:205], v[30:33]
	v_mfma_f32_16x16x32_bf16 v[26:29], v[162:165], v[202:205], v[26:29]
	v_mfma_f32_16x16x32_bf16 v[14:17], v[154:157], v[210:213], v[14:17]
	v_mfma_f32_16x16x32_bf16 v[10:13], v[162:165], v[210:213], v[10:13]
	v_lshl_add_u64 v[216:217], s[30:31], 0, v[136:137]
	s_mov_b32 m0, s25
	s_nop 0
	global_load_lds_dwordx4 v[216:217], off
	s_setprio 0
	s_setprio 1
	v_mfma_f32_16x16x32_bf16 v[54:57], v[166:169], v[182:185], v[54:57]
	v_mfma_f32_16x16x32_bf16 v[50:53], v[174:177], v[182:185], v[50:53]
	v_mfma_f32_16x16x32_bf16 v[38:41], v[166:169], v[190:193], v[38:41]
	v_mfma_f32_16x16x32_bf16 v[34:37], v[174:177], v[190:193], v[34:37]
	v_mfma_f32_16x16x32_bf16 v[22:25], v[166:169], v[198:201], v[22:25]
	v_mfma_f32_16x16x32_bf16 v[18:21], v[174:177], v[198:201], v[18:21]
	v_mfma_f32_16x16x32_bf16 v[6:9], v[166:169], v[206:209], v[6:9]
	v_mfma_f32_16x16x32_bf16 v[2:5], v[174:177], v[206:209], v[2:5]
	s_mov_b32 m0, s48
	s_nop 0
	global_load_lds_dwordx4 v[218:219], off
	v_mfma_f32_16x16x32_bf16 v[54:57], v[170:173], v[186:189], v[54:57]
	v_mfma_f32_16x16x32_bf16 v[50:53], v[178:181], v[186:189], v[50:53]
	v_mfma_f32_16x16x32_bf16 v[38:41], v[170:173], v[194:197], v[38:41]
	v_mfma_f32_16x16x32_bf16 v[34:37], v[178:181], v[194:197], v[34:37]
	v_mfma_f32_16x16x32_bf16 v[22:25], v[170:173], v[202:205], v[22:25]
	v_mfma_f32_16x16x32_bf16 v[18:21], v[178:181], v[202:205], v[18:21]
	v_mfma_f32_16x16x32_bf16 v[6:9], v[170:173], v[210:213], v[6:9]
	v_mfma_f32_16x16x32_bf16 v[2:5], v[178:181], v[210:213], v[2:5]
	s_setprio 0
	s_barrier
	s_add_i32 s58, 0, 0x18000
	v_add_u32_e32 v0, s58, v151
	s_add_i32 s59, 0, 0x1c000
	ds_read_b128 v[142:145], v0
	ds_read_b128 v[154:157], v0 offset:1024
	ds_read_b128 v[158:161], v0 offset:2048
	ds_read_b128 v[162:165], v0 offset:3072
	v_add_u32_e32 v0, s59, v151
	ds_read_b128 v[166:169], v0
	ds_read_b128 v[170:173], v0 offset:1024
	ds_read_b128 v[174:177], v0 offset:2048
	ds_read_b128 v[178:181], v0 offset:3072
	s_add_u32 s30, s30, 0x40000
	s_addc_u32 s31, s31, 0
	s_mov_b32 m0, s49
	v_lshl_add_u64 v[220:221], s[30:31], 0, v[136:137]
	ds_read_b128 v[182:185], v153 offset:32768
	ds_read_b128 v[186:189], v153 offset:33792
	ds_read_b128 v[190:193], v153 offset:34816
	ds_read_b128 v[194:197], v153 offset:35840
	ds_read_b128 v[198:201], v153 offset:36864
	ds_read_b128 v[202:205], v153 offset:37888
	ds_read_b128 v[206:209], v153 offset:38912
	ds_read_b128 v[210:213], v153 offset:39936
	global_load_lds_dwordx4 v[220:221], off
	v_lshl_add_u64 v[220:221], s[30:31], 0, v[132:133]
	s_mov_b32 m0, s50
	s_nop 0
	global_load_lds_dwordx4 v[220:221], off
	s_waitcnt vmcnt(8)
	s_waitcnt lgkmcnt(0)
	s_barrier
	s_setprio 1
	s_waitcnt lgkmcnt(0)
	v_mfma_f32_16x16x32_bf16 v[126:129], v[142:145], v[182:185], v[126:129]
	v_mfma_f32_16x16x32_bf16 v[122:125], v[158:161], v[182:185], v[122:125]
	v_mfma_f32_16x16x32_bf16 v[110:113], v[142:145], v[190:193], v[110:113]
	v_mfma_f32_16x16x32_bf16 v[106:109], v[158:161], v[190:193], v[106:109]
	v_mfma_f32_16x16x32_bf16 v[94:97], v[142:145], v[198:201], v[94:97]
	v_mfma_f32_16x16x32_bf16 v[90:93], v[158:161], v[198:201], v[90:93]
	v_mfma_f32_16x16x32_bf16 v[78:81], v[142:145], v[206:209], v[78:81]
	v_mfma_f32_16x16x32_bf16 v[74:77], v[158:161], v[206:209], v[74:77]
	v_mfma_f32_16x16x32_bf16 v[126:129], v[154:157], v[186:189], v[126:129]
	v_mfma_f32_16x16x32_bf16 v[122:125], v[162:165], v[186:189], v[122:125]
	v_mfma_f32_16x16x32_bf16 v[110:113], v[154:157], v[194:197], v[110:113]
	v_mfma_f32_16x16x32_bf16 v[106:109], v[162:165], v[194:197], v[106:109]
	v_mfma_f32_16x16x32_bf16 v[94:97], v[154:157], v[202:205], v[94:97]
	v_mfma_f32_16x16x32_bf16 v[90:93], v[162:165], v[202:205], v[90:93]
	v_mfma_f32_16x16x32_bf16 v[78:81], v[154:157], v[210:213], v[78:81]
	v_mfma_f32_16x16x32_bf16 v[74:77], v[162:165], v[210:213], v[74:77]
	s_setprio 0
	s_setprio 1
	v_mfma_f32_16x16x32_bf16 v[118:121], v[166:169], v[182:185], v[118:121]
	v_mfma_f32_16x16x32_bf16 v[114:117], v[174:177], v[182:185], v[114:117]
	v_mfma_f32_16x16x32_bf16 v[102:105], v[166:169], v[190:193], v[102:105]
	v_mfma_f32_16x16x32_bf16 v[98:101], v[174:177], v[190:193], v[98:101]
	v_mfma_f32_16x16x32_bf16 v[86:89], v[166:169], v[198:201], v[86:89]
	v_mfma_f32_16x16x32_bf16 v[82:85], v[174:177], v[198:201], v[82:85]
	v_mfma_f32_16x16x32_bf16 v[70:73], v[166:169], v[206:209], v[70:73]
	v_mfma_f32_16x16x32_bf16 v[66:69], v[174:177], v[206:209], v[66:69]
	v_mfma_f32_16x16x32_bf16 v[118:121], v[170:173], v[186:189], v[118:121]
	v_mfma_f32_16x16x32_bf16 v[114:117], v[178:181], v[186:189], v[114:117]
	v_mfma_f32_16x16x32_bf16 v[102:105], v[170:173], v[194:197], v[102:105]
	v_mfma_f32_16x16x32_bf16 v[98:101], v[178:181], v[194:197], v[98:101]
	v_mfma_f32_16x16x32_bf16 v[86:89], v[170:173], v[202:205], v[86:89]
	v_mfma_f32_16x16x32_bf16 v[82:85], v[178:181], v[202:205], v[82:85]
	v_mfma_f32_16x16x32_bf16 v[70:73], v[170:173], v[210:213], v[70:73]
	v_mfma_f32_16x16x32_bf16 v[66:69], v[178:181], v[210:213], v[66:69]
	s_setprio 0
	s_barrier
; #define PG8_STAGE(bufoff, gbase, voff) do { _Pragma("unroll") for (int _i = 0; _i < 2; ++_i) \
;         __builtin_amdgcn_global_load_lds((const unsigned*)((const char*)(gbase) + (voff)[_i]), (PG8_LAS unsigned*)(lds + (bufoff) + ldsw + _i * 8192), 16, 0, 0); } while (0)
; #define PG8_WAIT_V(n) asm volatile("s_waitcnt vmcnt(" #n ")" ::: "memory")
; #define PG8_BAR __builtin_amdgcn_s_barrier()
; template <class Epi, class Sched, bool ALIGN_EPI = false, bool SP2 = false, bool GATHER = false>
; __device__ __forceinline__ void gemm_phase(PG8_LAS unsigned char* lds, const Gemm g, const Sched& S, const Epi& E, int tid_in, const int* rowsrc = nullptr, PG8_LAS int* idx_lds = nullptr) {
;     ...
;         for (int t = 0; t < nt; t += 2) {
;             const bool last = (t == nt - 2);
;             if constexpr (GATHER) {
; #pragma unroll
;                 for (int h_ = 0; h_ < 2; ++h_) { gS[h_][0] = last ? gN[h_][0] : gA[h_][0]; gS[h_][1] = last ? gN[h_][1] : gA[h_][1]; } }
;             const char* a1 = cA + (size_t)(t + 1) * kstep;
;             const char* a2 = last ? nA : cA + (size_t)(t + 2) * kstep; const char* b2 = last ? nB : cB + (size_t)(t + 2) * kstep;
;             const char* a3 = a2 + kstep; const char* b3 = b2 + kstep;
;             if (last && has_next) S.a_ready(nxt);
;             if constexpr (SP2) {
;             PG8_LDB(B0, 0, 0); PG8_LDB(B1, 0, 1); PG8_SCHED; PG8_LDA(At, 0, 0); PG8_STAGE(PG8_SA(1, 1), a1 + hstepA, PG8_OA(1));
;             PG8_WAIT_V(8); PG8_WAIT_L(0); PG8_BAR; PG8_MMA(0, 0, At, B0); PG8_MMA(0, 1, At, B1); PG8_BAR; PG8_SCHED;
;             PG8_LDA(At, 0, 1); PG8_STAGE(PG8_SB(0, 0), b2, voffB); PG8_STAGE(PG8_SB(0, 1), b2 + hstep, voffB); PG8_STAGE(PG8_SA(0, 0), a2, PG8_OS(0));
;             PG8_WAIT_V(8); PG8_WAIT_L(0); PG8_BAR; PG8_MMA(1, 0, At, B0); PG8_MMA(1, 1, At, B1); PG8_BAR; PG8_SCHED;
;             PG8_LDB(B0, 1, 0); PG8_LDB(B1, 1, 1); PG8_SCHED; PG8_LDA(At, 1, 0); PG8_STAGE(PG8_SA(0, 1), a2 + hstepA, PG8_OS(1));
;             PG8_WAIT_V(8); PG8_WAIT_L(0); PG8_BAR; PG8_MMA(0, 0, At, B0); PG8_MMA(0, 1, At, B1); PG8_BAR; PG8_SCHED;
;             PG8_LDA(At, 1, 1); PG8_STAGE(PG8_SB(1, 0), b3, voffB); PG8_STAGE(PG8_SB(1, 1), b3 + hstep, voffB); PG8_STAGE(PG8_SA(1, 0), a3, PG8_OS(0));
;             PG8_WAIT_V(8); PG8_WAIT_L(0); PG8_BAR; PG8_MMA(1, 0, At, B0); PG8_MMA(1, 1, At, B1); PG8_BAR; PG8_SCHED;
	s_add_i32 s30, s58, s44
	v_lshl_add_u64 v[148:149], v[148:149], 0, s[10:11]
	s_mov_b32 m0, s30
	ds_read_b128 v[182:185], v153 offset:49152
	ds_read_b128 v[186:189], v153 offset:50176
	ds_read_b128 v[190:193], v153 offset:51200
	ds_read_b128 v[194:197], v153 offset:52224
	ds_read_b128 v[198:201], v153 offset:53248
	ds_read_b128 v[202:205], v153 offset:54272
	ds_read_b128 v[206:209], v153 offset:55296
	ds_read_b128 v[210:213], v153 offset:56320
	global_load_lds_dwordx4 v[148:149], off
	s_add_i32 m0, s30, 0x2000
	s_add_u32 s28, s28, 0x40080
	v_lshl_add_u64 v[148:149], v[214:215], 0, s[10:11]
	s_addc_u32 s29, s29, 0
	s_add_i32 s30, s59, s44
	global_load_lds_dwordx4 v[148:149], off
	v_lshl_add_u64 v[148:149], s[28:29], 0, v[134:135]
	s_mov_b32 m0, s30
	s_nop 0
	global_load_lds_dwordx4 v[148:149], off
	s_waitcnt vmcnt(5)
	s_waitcnt lgkmcnt(0)
	s_barrier
	s_setprio 1
	s_waitcnt lgkmcnt(0)
	v_mfma_f32_16x16x32_bf16 v[62:65], v[142:145], v[182:185], v[62:65]
	v_mfma_f32_16x16x32_bf16 v[58:61], v[158:161], v[182:185], v[58:61]
	v_mfma_f32_16x16x32_bf16 v[46:49], v[142:145], v[190:193], v[46:49]
	v_mfma_f32_16x16x32_bf16 v[42:45], v[158:161], v[190:193], v[42:45]
	v_mfma_f32_16x16x32_bf16 v[30:33], v[142:145], v[198:201], v[30:33]
	v_mfma_f32_16x16x32_bf16 v[26:29], v[158:161], v[198:201], v[26:29]
	v_mfma_f32_16x16x32_bf16 v[14:17], v[142:145], v[206:209], v[14:17]
	v_mfma_f32_16x16x32_bf16 v[10:13], v[158:161], v[206:209], v[10:13]
	v_lshl_add_u64 v[148:149], s[28:29], 0, v[130:131]
	s_add_i32 m0, s30, 0x2000
	s_nop 0
	global_load_lds_dwordx4 v[148:149], off
	v_mfma_f32_16x16x32_bf16 v[62:65], v[154:157], v[186:189], v[62:65]
	v_mfma_f32_16x16x32_bf16 v[58:61], v[162:165], v[186:189], v[58:61]
	v_mfma_f32_16x16x32_bf16 v[46:49], v[154:157], v[194:197], v[46:49]
	v_mfma_f32_16x16x32_bf16 v[42:45], v[162:165], v[194:197], v[42:45]
	v_mfma_f32_16x16x32_bf16 v[30:33], v[154:157], v[202:205], v[30:33]
	v_mfma_f32_16x16x32_bf16 v[26:29], v[162:165], v[202:205], v[26:29]
	v_mfma_f32_16x16x32_bf16 v[14:17], v[154:157], v[210:213], v[14:17]
	v_mfma_f32_16x16x32_bf16 v[10:13], v[162:165], v[210:213], v[10:13]
	v_lshl_add_u64 v[148:149], v[216:217], 0, s[10:11]
	s_mov_b32 m0, s51
	s_nop 0
	global_load_lds_dwordx4 v[148:149], off
	s_setprio 0
	s_setprio 1
	v_mfma_f32_16x16x32_bf16 v[54:57], v[166:169], v[182:185], v[54:57]
	v_mfma_f32_16x16x32_bf16 v[50:53], v[174:177], v[182:185], v[50:53]
	v_mfma_f32_16x16x32_bf16 v[38:41], v[166:169], v[190:193], v[38:41]
	v_mfma_f32_16x16x32_bf16 v[34:37], v[174:177], v[190:193], v[34:37]
	v_mfma_f32_16x16x32_bf16 v[22:25], v[166:169], v[198:201], v[22:25]
	v_mfma_f32_16x16x32_bf16 v[18:21], v[174:177], v[198:201], v[18:21]
	v_mfma_f32_16x16x32_bf16 v[6:9], v[166:169], v[206:209], v[6:9]
	v_mfma_f32_16x16x32_bf16 v[2:5], v[174:177], v[206:209], v[2:5]
	v_lshl_add_u64 v[148:149], v[218:219], 0, s[10:11]
	s_mov_b32 m0, s52
	s_nop 0
	global_load_lds_dwordx4 v[148:149], off
	v_mfma_f32_16x16x32_bf16 v[54:57], v[170:173], v[186:189], v[54:57]
	v_mfma_f32_16x16x32_bf16 v[50:53], v[178:181], v[186:189], v[50:53]
	v_mfma_f32_16x16x32_bf16 v[38:41], v[170:173], v[194:197], v[38:41]
	v_mfma_f32_16x16x32_bf16 v[34:37], v[178:181], v[194:197], v[34:37]
	v_mfma_f32_16x16x32_bf16 v[22:25], v[170:173], v[202:205], v[22:25]
	v_mfma_f32_16x16x32_bf16 v[18:21], v[178:181], v[202:205], v[18:21]
	v_mfma_f32_16x16x32_bf16 v[6:9], v[170:173], v[210:213], v[6:9]
	v_mfma_f32_16x16x32_bf16 v[2:5], v[178:181], v[210:213], v[2:5]
	s_setprio 0
	s_barrier
	s_add_i32 s57, s57, 2
	s_add_u32 s26, s26, 0x100
	s_addc_u32 s27, s27, 0
	s_add_u32 s55, s55, 0x100
	s_addc_u32 s56, s56, 0
	s_cmp_gt_u32 s57, 13
	s_cbranch_scc0 .LBB0_2005
	s_and_b64 vcc, exec, s[8:9]
	s_cbranch_vccz .LBB0_2008
	s_barrier
